# K-loops: the repeated lgkmcnt(0) behind each pre-MFMA barrier removed (the one in front of the barrier already covers the fragment reads)
# baseline (speedup 1.0000x reference)
; #define GM_STAGE(bufoff, gbase, voff) do { _Pragma("unroll") for (int _i = 0; _i < 2; ++_i) \
;         __builtin_amdgcn_global_load_lds((const unsigned*)((const char*)(gbase) + (voff)[_i]), (LAS unsigned*)(lds + (bufoff) + ldsw + _i * 8192), 16, 0, 0); } while (0)
; #define GM_LDA(dst, b, h) do { _Pragma("unroll") for (int m = 0; m < 4; ++m) _Pragma("unroll") for (int k = 0; k < 2; ++k) dst[m][k] = *(const LAS s16x8*)(lds + GM_SA(b, h) + aoff + m * 2048 + k * 1024); } while (0)
; #define GM_LDB(dst, b, h) do { _Pragma("unroll") for (int n = 0; n < 2; ++n) _Pragma("unroll") for (int k = 0; k < 2; ++k) dst[n][k] = *(const LAS s16x8*)(lds + GM_SB(b, h) + boff + n * 2048 + k * 1024); } while (0)
; #define GM_MMA(ai, bj, At, Bt) do { __builtin_amdgcn_s_setprio(1); _Pragma("unroll") for (int m = 0; m < 4; ++m) _Pragma("unroll") for (int n = 0; n < 2; ++n) _Pragma("unroll") for (int k = 0; k < 2; ++k) \
;         acc[ai][bj][m][n] = mma16<BF>(Bt[n][k], At[m][k], acc[ai][bj][m][n]); __builtin_amdgcn_s_setprio(0); } while (0)
; #define GM_WAIT_V(n) asm volatile("s_waitcnt vmcnt(" #n ")" ::: "memory")
; #define GM_WAIT_L(n) asm volatile("s_waitcnt lgkmcnt(" #n ")" ::: "memory")
; #define GM_BAR __builtin_amdgcn_s_barrier()
; template <bool BF, bool GATHER = false, class Epi, class Hook>
; __device__ __forceinline__ void gemm_phase(LAS unsigned char* lds, const Gemm g, const Order& S, const Epi& E, Hook& HK) {
;     ...
;             GM_LDB(B0, 0, 0); GM_LDB(B1, 0, 1); GM_SCHED; GM_LDA(At, 0, 0); GM_STA_H1(GM_SA(1, 1), a1, gA1);
;             GM_WAIT_V(8); GM_WAIT_L(0); GM_BAR; GM_MMA(0, 0, At, B0); GM_MMA(0, 1, At, B1); GM_BAR; GM_SCHED;
;             GM_LDA(At, 0, 1); GM_STAGE(GM_SB(0, 0), b2, voffB); GM_STAGE(GM_SB(0, 1), b2 + hstepB, voffB); GM_STA_H0(GM_SA(0, 0), a2, s0);
;             GM_WAIT_V(8); GM_WAIT_L(0); GM_BAR; GM_MMA(1, 0, At, B0); GM_MMA(1, 1, At, B1); GM_BAR; GM_SCHED;
;             GM_LDB(B0, 1, 0); GM_LDB(B1, 1, 1); GM_SCHED; GM_LDA(At, 1, 0); GM_STA_H1(GM_SA(0, 1), a2, s1);
;             GM_WAIT_V(8); GM_WAIT_L(0); GM_BAR; GM_MMA(0, 0, At, B0); GM_MMA(0, 1, At, B1); GM_BAR; GM_SCHED;
;             GM_LDA(At, 1, 1); GM_STAGE(GM_SB(1, 0), b3, voffB); GM_STAGE(GM_SB(1, 1), b3 + hstepB, voffB); GM_STA_H0(GM_SA(1, 0), a3, s0);
;             GM_WAIT_V(8); GM_WAIT_L(0); GM_BAR; GM_MMA(1, 0, At, B0); GM_MMA(1, 1, At, B1); GM_BAR; GM_SCHED;
.LBB0_380:
	s_add_u32 s28, s2, 0xfffc0080
	s_addc_u32 s29, s3, -1
	s_cmp_eq_u32 s51, 12
	s_cselect_b32 s31, s9, s29
	s_cselect_b32 s30, s19, s28
	s_cselect_b32 s29, s21, s50
	s_cselect_b32 s28, s48, s49
	v_lshl_add_u64 v[150:151], s[2:3], 0, v[138:139]
	s_add_i32 m0, s27, 0xc000
	global_load_lds_dwordx4 v[150:151], off
	v_lshl_add_u64 v[150:151], s[2:3], 0, v[140:141]
	s_add_i32 m0, s27, 0xe000
	s_nop 0
	global_load_lds_dwordx4 v[150:151], off
	ds_read_b128 v[146:149], v158
	ds_read_b128 v[162:165], v158 offset:1024
	ds_read_b128 v[166:169], v158 offset:2048
	ds_read_b128 v[170:173], v158 offset:3072
	ds_read_b128 v[174:177], v159
	ds_read_b128 v[178:181], v159 offset:1024
	ds_read_b128 v[182:185], v159 offset:2048
	ds_read_b128 v[186:189], v159 offset:3072
	ds_read_b128 v[190:193], v160
	ds_read_b128 v[194:197], v160 offset:1024
	ds_read_b128 v[198:201], v160 offset:2048
	ds_read_b128 v[202:205], v160 offset:3072
	ds_read_b128 v[206:209], v160 offset:4096
	ds_read_b128 v[210:213], v160 offset:5120
	ds_read_b128 v[214:217], v160 offset:6144
	ds_read_b128 v[218:221], v160 offset:7168
	s_waitcnt vmcnt(8)
	s_waitcnt lgkmcnt(0)
	s_barrier
	v_mfma_f32_16x16x32_f16 v[126:129], v[146:149], v[190:193], v[126:129]
	v_mfma_f32_16x16x32_f16 v[122:125], v[166:169], v[190:193], v[122:125]
	v_mfma_f32_16x16x32_f16 v[110:113], v[146:149], v[198:201], v[110:113]
	v_mfma_f32_16x16x32_f16 v[106:109], v[166:169], v[198:201], v[106:109]
	v_mfma_f32_16x16x32_f16 v[94:97], v[146:149], v[206:209], v[94:97]
	v_mfma_f32_16x16x32_f16 v[90:93], v[166:169], v[206:209], v[90:93]
	v_mfma_f32_16x16x32_f16 v[78:81], v[146:149], v[214:217], v[78:81]
	v_mfma_f32_16x16x32_f16 v[74:77], v[166:169], v[214:217], v[74:77]
	v_mfma_f32_16x16x32_f16 v[126:129], v[162:165], v[194:197], v[126:129]
	v_mfma_f32_16x16x32_f16 v[122:125], v[170:173], v[194:197], v[122:125]
	v_mfma_f32_16x16x32_f16 v[110:113], v[162:165], v[202:205], v[110:113]
	v_mfma_f32_16x16x32_f16 v[106:109], v[170:173], v[202:205], v[106:109]
	v_mfma_f32_16x16x32_f16 v[94:97], v[162:165], v[210:213], v[94:97]
	v_mfma_f32_16x16x32_f16 v[90:93], v[170:173], v[210:213], v[90:93]
	v_mfma_f32_16x16x32_f16 v[78:81], v[162:165], v[218:221], v[78:81]
	v_mfma_f32_16x16x32_f16 v[74:77], v[170:173], v[218:221], v[74:77]
	v_mfma_f32_16x16x32_f16 v[118:121], v[174:177], v[190:193], v[118:121]
	v_mfma_f32_16x16x32_f16 v[114:117], v[182:185], v[190:193], v[114:117]
	v_mfma_f32_16x16x32_f16 v[102:105], v[174:177], v[198:201], v[102:105]
	v_mfma_f32_16x16x32_f16 v[98:101], v[182:185], v[198:201], v[98:101]
	v_mfma_f32_16x16x32_f16 v[86:89], v[174:177], v[206:209], v[86:89]
	v_mfma_f32_16x16x32_f16 v[82:85], v[182:185], v[206:209], v[82:85]
	v_mfma_f32_16x16x32_f16 v[70:73], v[174:177], v[214:217], v[70:73]
	v_mfma_f32_16x16x32_f16 v[66:69], v[182:185], v[214:217], v[66:69]
	v_mfma_f32_16x16x32_f16 v[118:121], v[178:181], v[194:197], v[118:121]
	v_mfma_f32_16x16x32_f16 v[114:117], v[186:189], v[194:197], v[114:117]
	v_mfma_f32_16x16x32_f16 v[102:105], v[178:181], v[202:205], v[102:105]
	v_mfma_f32_16x16x32_f16 v[98:101], v[186:189], v[202:205], v[98:101]
	v_mfma_f32_16x16x32_f16 v[86:89], v[178:181], v[210:213], v[86:89]
	v_mfma_f32_16x16x32_f16 v[82:85], v[186:189], v[210:213], v[82:85]
	v_mfma_f32_16x16x32_f16 v[70:73], v[178:181], v[218:221], v[70:73]
	v_mfma_f32_16x16x32_f16 v[66:69], v[186:189], v[218:221], v[66:69]
	s_barrier
	s_add_i32 s52, s45, s35
	v_lshl_add_u64 v[150:151], s[28:29], 0, v[132:133]
	s_mov_b32 m0, s52
	global_load_lds_dwordx4 v[150:151], off
	s_add_i32 m0, s52, 0x2000
	s_add_u32 s52, s28, 0x40000
	v_lshl_add_u64 v[222:223], s[28:29], 0, v[136:137]
	s_addc_u32 s53, s29, 0
	s_add_i32 s54, s46, s35
	global_load_lds_dwordx4 v[222:223], off
	v_lshl_add_u64 v[224:225], s[52:53], 0, v[132:133]
	s_mov_b32 m0, s54
	v_lshl_add_u64 v[226:227], s[30:31], 0, v[134:135]
	global_load_lds_dwordx4 v[224:225], off
	v_lshl_add_u64 v[224:225], s[52:53], 0, v[136:137]
	s_add_i32 m0, s54, 0x2000
	s_nop 0
	global_load_lds_dwordx4 v[224:225], off
	v_lshl_add_u64 v[224:225], s[30:31], 0, v[130:131]
	s_mov_b32 m0, s27
	s_nop 0
	global_load_lds_dwordx4 v[224:225], off
	s_mov_b32 m0, s36
	s_nop 0
	global_load_lds_dwordx4 v[226:227], off
	ds_read_b128 v[190:193], v160 offset:16384
	ds_read_b128 v[194:197], v160 offset:17408
	ds_read_b128 v[198:201], v160 offset:18432
	ds_read_b128 v[202:205], v160 offset:19456
	ds_read_b128 v[206:209], v160 offset:20480
	ds_read_b128 v[210:213], v160 offset:21504
	ds_read_b128 v[214:217], v160 offset:22528
	ds_read_b128 v[218:221], v160 offset:23552
	s_waitcnt vmcnt(8)
	s_waitcnt lgkmcnt(0)
	s_barrier
; #define GM_STAGE(bufoff, gbase, voff) do { _Pragma("unroll") for (int _i = 0; _i < 2; ++_i) \
;         __builtin_amdgcn_global_load_lds((const unsigned*)((const char*)(gbase) + (voff)[_i]), (LAS unsigned*)(lds + (bufoff) + ldsw + _i * 8192), 16, 0, 0); } while (0)
; #define GM_LDA(dst, b, h) do { _Pragma("unroll") for (int m = 0; m < 4; ++m) _Pragma("unroll") for (int k = 0; k < 2; ++k) dst[m][k] = *(const LAS s16x8*)(lds + GM_SA(b, h) + aoff + m * 2048 + k * 1024); } while (0)
; #define GM_LDB(dst, b, h) do { _Pragma("unroll") for (int n = 0; n < 2; ++n) _Pragma("unroll") for (int k = 0; k < 2; ++k) dst[n][k] = *(const LAS s16x8*)(lds + GM_SB(b, h) + boff + n * 2048 + k * 1024); } while (0)
; #define GM_MMA(ai, bj, At, Bt) do { __builtin_amdgcn_s_setprio(1); _Pragma("unroll") for (int m = 0; m < 4; ++m) _Pragma("unroll") for (int n = 0; n < 2; ++n) _Pragma("unroll") for (int k = 0; k < 2; ++k) \
;         acc[ai][bj][m][n] = mma16<BF>(Bt[n][k], At[m][k], acc[ai][bj][m][n]); __builtin_amdgcn_s_setprio(0); } while (0)
; #define GM_WAIT_V(n) asm volatile("s_waitcnt vmcnt(" #n ")" ::: "memory")
; #define GM_WAIT_L(n) asm volatile("s_waitcnt lgkmcnt(" #n ")" ::: "memory")
; #define GM_BAR __builtin_amdgcn_s_barrier()
; template <bool BF, bool GATHER = false, class Epi, class Hook>
; __device__ __forceinline__ void gemm_phase(LAS unsigned char* lds, const Gemm g, const Order& S, const Epi& E, Hook& HK) {
;     ...
;             GM_LDB(B0, 0, 0); GM_LDB(B1, 0, 1); GM_SCHED; GM_LDA(At, 0, 0); GM_STA_H1(GM_SA(1, 1), a1, gA1);
;             GM_WAIT_V(8); GM_WAIT_L(0); GM_BAR; GM_MMA(0, 0, At, B0); GM_MMA(0, 1, At, B1); GM_BAR; GM_SCHED;
;             GM_LDA(At, 0, 1); GM_STAGE(GM_SB(0, 0), b2, voffB); GM_STAGE(GM_SB(0, 1), b2 + hstepB, voffB); GM_STA_H0(GM_SA(0, 0), a2, s0);
;             GM_WAIT_V(8); GM_WAIT_L(0); GM_BAR; GM_MMA(1, 0, At, B0); GM_MMA(1, 1, At, B1); GM_BAR; GM_SCHED;
;             GM_LDB(B0, 1, 0); GM_LDB(B1, 1, 1); GM_SCHED; GM_LDA(At, 1, 0); GM_STA_H1(GM_SA(0, 1), a2, s1);
;             GM_WAIT_V(8); GM_WAIT_L(0); GM_BAR; GM_MMA(0, 0, At, B0); GM_MMA(0, 1, At, B1); GM_BAR; GM_SCHED;
;             GM_LDA(At, 1, 1); GM_STAGE(GM_SB(1, 0), b3, voffB); GM_STAGE(GM_SB(1, 1), b3 + hstepB, voffB); GM_STA_H0(GM_SA(1, 0), a3, s0);
;             GM_WAIT_V(8); GM_WAIT_L(0); GM_BAR; GM_MMA(1, 0, At, B0); GM_MMA(1, 1, At, B1); GM_BAR; GM_SCHED;
	v_mfma_f32_16x16x32_f16 v[62:65], v[146:149], v[190:193], v[62:65]
	v_mfma_f32_16x16x32_f16 v[58:61], v[166:169], v[190:193], v[58:61]
	v_mfma_f32_16x16x32_f16 v[46:49], v[146:149], v[198:201], v[46:49]
	v_mfma_f32_16x16x32_f16 v[42:45], v[166:169], v[198:201], v[42:45]
	v_mfma_f32_16x16x32_f16 v[30:33], v[146:149], v[206:209], v[30:33]
	v_mfma_f32_16x16x32_f16 v[26:29], v[166:169], v[206:209], v[26:29]
	v_mfma_f32_16x16x32_f16 v[14:17], v[146:149], v[214:217], v[14:17]
	v_mfma_f32_16x16x32_f16 v[10:13], v[166:169], v[214:217], v[10:13]
	v_mfma_f32_16x16x32_f16 v[62:65], v[162:165], v[194:197], v[62:65]
	v_mfma_f32_16x16x32_f16 v[58:61], v[170:173], v[194:197], v[58:61]
	v_mfma_f32_16x16x32_f16 v[46:49], v[162:165], v[202:205], v[46:49]
	v_mfma_f32_16x16x32_f16 v[42:45], v[170:173], v[202:205], v[42:45]
	v_mfma_f32_16x16x32_f16 v[30:33], v[162:165], v[210:213], v[30:33]
	v_mfma_f32_16x16x32_f16 v[26:29], v[170:173], v[210:213], v[26:29]
	v_mfma_f32_16x16x32_f16 v[14:17], v[162:165], v[218:221], v[14:17]
	v_mfma_f32_16x16x32_f16 v[10:13], v[170:173], v[218:221], v[10:13]
	v_mfma_f32_16x16x32_f16 v[54:57], v[174:177], v[190:193], v[54:57]
	v_mfma_f32_16x16x32_f16 v[50:53], v[182:185], v[190:193], v[50:53]
	v_mfma_f32_16x16x32_f16 v[38:41], v[174:177], v[198:201], v[38:41]
	v_mfma_f32_16x16x32_f16 v[34:37], v[182:185], v[198:201], v[34:37]
	v_mfma_f32_16x16x32_f16 v[22:25], v[174:177], v[206:209], v[22:25]
	v_mfma_f32_16x16x32_f16 v[18:21], v[182:185], v[206:209], v[18:21]
	v_mfma_f32_16x16x32_f16 v[6:9], v[174:177], v[214:217], v[6:9]
	v_mfma_f32_16x16x32_f16 v[2:5], v[182:185], v[214:217], v[2:5]
	v_mfma_f32_16x16x32_f16 v[54:57], v[178:181], v[194:197], v[54:57]
	v_mfma_f32_16x16x32_f16 v[50:53], v[186:189], v[194:197], v[50:53]
	v_mfma_f32_16x16x32_f16 v[38:41], v[178:181], v[202:205], v[38:41]
	v_mfma_f32_16x16x32_f16 v[34:37], v[186:189], v[202:205], v[34:37]
	v_mfma_f32_16x16x32_f16 v[22:25], v[178:181], v[210:213], v[22:25]
	v_mfma_f32_16x16x32_f16 v[18:21], v[186:189], v[210:213], v[18:21]
	v_mfma_f32_16x16x32_f16 v[6:9], v[178:181], v[218:221], v[6:9]
	v_mfma_f32_16x16x32_f16 v[2:5], v[186:189], v[218:221], v[2:5]
	s_barrier
	s_add_u32 s30, s30, 0x40000
	s_addc_u32 s31, s31, 0
	s_mov_b32 m0, s37
	v_lshl_add_u64 v[228:229], s[30:31], 0, v[130:131]
	global_load_lds_dwordx4 v[228:229], off
	v_lshl_add_u64 v[228:229], s[30:31], 0, v[134:135]
	s_mov_b32 m0, s38
	s_nop 0
	global_load_lds_dwordx4 v[228:229], off
	s_mov_b32 s53, 0x1c000
	s_mov_b32 s52, 0x18000
	v_add_u32_e32 v244, s52, v153
	v_add_u32_e32 v245, s53, v153
	ds_read_b128 v[146:149], v244
	ds_read_b128 v[162:165], v244 offset:1024
	ds_read_b128 v[166:169], v244 offset:2048
	ds_read_b128 v[170:173], v244 offset:3072
	ds_read_b128 v[174:177], v245
	ds_read_b128 v[178:181], v245 offset:1024
	ds_read_b128 v[182:185], v245 offset:2048
	ds_read_b128 v[186:189], v245 offset:3072
	ds_read_b128 v[190:193], v160 offset:32768
	ds_read_b128 v[194:197], v160 offset:33792
	ds_read_b128 v[198:201], v160 offset:34816
	ds_read_b128 v[202:205], v160 offset:35840
	ds_read_b128 v[206:209], v160 offset:36864
	ds_read_b128 v[210:213], v160 offset:37888
	ds_read_b128 v[214:217], v160 offset:38912
	ds_read_b128 v[218:221], v160 offset:39936
	s_waitcnt vmcnt(8)
	s_waitcnt lgkmcnt(0)
	s_barrier
	v_mfma_f32_16x16x32_f16 v[126:129], v[146:149], v[190:193], v[126:129]
	v_mfma_f32_16x16x32_f16 v[122:125], v[166:169], v[190:193], v[122:125]
	v_mfma_f32_16x16x32_f16 v[110:113], v[146:149], v[198:201], v[110:113]
	v_mfma_f32_16x16x32_f16 v[106:109], v[166:169], v[198:201], v[106:109]
	v_mfma_f32_16x16x32_f16 v[94:97], v[146:149], v[206:209], v[94:97]
	v_mfma_f32_16x16x32_f16 v[90:93], v[166:169], v[206:209], v[90:93]
	v_mfma_f32_16x16x32_f16 v[78:81], v[146:149], v[214:217], v[78:81]
	v_mfma_f32_16x16x32_f16 v[74:77], v[166:169], v[214:217], v[74:77]
	v_mfma_f32_16x16x32_f16 v[126:129], v[162:165], v[194:197], v[126:129]
	v_mfma_f32_16x16x32_f16 v[122:125], v[170:173], v[194:197], v[122:125]
	v_mfma_f32_16x16x32_f16 v[110:113], v[162:165], v[202:205], v[110:113]
	v_mfma_f32_16x16x32_f16 v[106:109], v[170:173], v[202:205], v[106:109]
	v_mfma_f32_16x16x32_f16 v[94:97], v[162:165], v[210:213], v[94:97]
	v_mfma_f32_16x16x32_f16 v[90:93], v[170:173], v[210:213], v[90:93]
	v_mfma_f32_16x16x32_f16 v[78:81], v[162:165], v[218:221], v[78:81]
	v_mfma_f32_16x16x32_f16 v[74:77], v[170:173], v[218:221], v[74:77]
	v_mfma_f32_16x16x32_f16 v[118:121], v[174:177], v[190:193], v[118:121]
	v_mfma_f32_16x16x32_f16 v[114:117], v[182:185], v[190:193], v[114:117]
	v_mfma_f32_16x16x32_f16 v[102:105], v[174:177], v[198:201], v[102:105]
	v_mfma_f32_16x16x32_f16 v[98:101], v[182:185], v[198:201], v[98:101]
	v_mfma_f32_16x16x32_f16 v[86:89], v[174:177], v[206:209], v[86:89]
	v_mfma_f32_16x16x32_f16 v[82:85], v[182:185], v[206:209], v[82:85]
	v_mfma_f32_16x16x32_f16 v[70:73], v[174:177], v[214:217], v[70:73]
	v_mfma_f32_16x16x32_f16 v[66:69], v[182:185], v[214:217], v[66:69]
	v_mfma_f32_16x16x32_f16 v[118:121], v[178:181], v[194:197], v[118:121]
	v_mfma_f32_16x16x32_f16 v[114:117], v[186:189], v[194:197], v[114:117]
	v_mfma_f32_16x16x32_f16 v[102:105], v[178:181], v[202:205], v[102:105]
	v_mfma_f32_16x16x32_f16 v[98:101], v[186:189], v[202:205], v[98:101]
	v_mfma_f32_16x16x32_f16 v[86:89], v[178:181], v[210:213], v[86:89]
	v_mfma_f32_16x16x32_f16 v[82:85], v[186:189], v[210:213], v[82:85]
	v_mfma_f32_16x16x32_f16 v[70:73], v[178:181], v[218:221], v[70:73]
	v_mfma_f32_16x16x32_f16 v[66:69], v[186:189], v[218:221], v[66:69]
	s_barrier
; #define GM_STAGE(bufoff, gbase, voff) do { _Pragma("unroll") for (int _i = 0; _i < 2; ++_i) \
;         __builtin_amdgcn_global_load_lds((const unsigned*)((const char*)(gbase) + (voff)[_i]), (LAS unsigned*)(lds + (bufoff) + ldsw + _i * 8192), 16, 0, 0); } while (0)
; #define GM_LDA(dst, b, h) do { _Pragma("unroll") for (int m = 0; m < 4; ++m) _Pragma("unroll") for (int k = 0; k < 2; ++k) dst[m][k] = *(const LAS s16x8*)(lds + GM_SA(b, h) + aoff + m * 2048 + k * 1024); } while (0)
; #define GM_LDB(dst, b, h) do { _Pragma("unroll") for (int n = 0; n < 2; ++n) _Pragma("unroll") for (int k = 0; k < 2; ++k) dst[n][k] = *(const LAS s16x8*)(lds + GM_SB(b, h) + boff + n * 2048 + k * 1024); } while (0)
; #define GM_MMA(ai, bj, At, Bt) do { __builtin_amdgcn_s_setprio(1); _Pragma("unroll") for (int m = 0; m < 4; ++m) _Pragma("unroll") for (int n = 0; n < 2; ++n) _Pragma("unroll") for (int k = 0; k < 2; ++k) \
;         acc[ai][bj][m][n] = mma16<BF>(Bt[n][k], At[m][k], acc[ai][bj][m][n]); __builtin_amdgcn_s_setprio(0); } while (0)
; #define GM_WAIT_V(n) asm volatile("s_waitcnt vmcnt(" #n ")" ::: "memory")
; #define GM_WAIT_L(n) asm volatile("s_waitcnt lgkmcnt(" #n ")" ::: "memory")
; template <bool BF, bool GATHER = false, class Epi, class Hook>
; __device__ __forceinline__ void gemm_phase(LAS unsigned char* lds, const Gemm g, const Order& S, const Epi& E, Hook& HK) {
;     ...
;             GM_LDB(B0, 0, 0); GM_LDB(B1, 0, 1); GM_SCHED; GM_LDA(At, 0, 0); GM_STA_H1(GM_SA(1, 1), a1, gA1);
;             GM_WAIT_V(8); GM_WAIT_L(0); GM_BAR; GM_MMA(0, 0, At, B0); GM_MMA(0, 1, At, B1); GM_BAR; GM_SCHED;
;             GM_LDA(At, 0, 1); GM_STAGE(GM_SB(0, 0), b2, voffB); GM_STAGE(GM_SB(0, 1), b2 + hstepB, voffB); GM_STA_H0(GM_SA(0, 0), a2, s0);
;             GM_WAIT_V(8); GM_WAIT_L(0); GM_BAR; GM_MMA(1, 0, At, B0); GM_MMA(1, 1, At, B1); GM_BAR; GM_SCHED;
;             GM_LDB(B0, 1, 0); GM_LDB(B1, 1, 1); GM_SCHED; GM_LDA(At, 1, 0); GM_STA_H1(GM_SA(0, 1), a2, s1);
;             GM_WAIT_V(8); GM_WAIT_L(0); GM_BAR; GM_MMA(0, 0, At, B0); GM_MMA(0, 1, At, B1); GM_BAR; GM_SCHED;
;             GM_LDA(At, 1, 1); GM_STAGE(GM_SB(1, 0), b3, voffB); GM_STAGE(GM_SB(1, 1), b3 + hstepB, voffB); GM_STA_H0(GM_SA(1, 0), a3, s0);
;             GM_WAIT_V(8); GM_WAIT_L(0); GM_BAR; GM_MMA(1, 0, At, B0); GM_MMA(1, 1, At, B1); GM_BAR; GM_SCHED;
;         }
;         if (wr == 0) GM_BAR;
	s_add_i32 s30, s52, s35
	v_lshl_add_u64 v[150:151], v[150:151], 0, s[14:15]
	s_mov_b32 m0, s30
	global_load_lds_dwordx4 v[150:151], off
	s_add_i32 m0, s30, 0x2000
	s_add_u32 s28, s28, 0x40080
	v_lshl_add_u64 v[150:151], v[222:223], 0, s[14:15]
	s_addc_u32 s29, s29, 0
	s_add_i32 s30, s53, s35
	global_load_lds_dwordx4 v[150:151], off
	v_lshl_add_u64 v[150:151], s[28:29], 0, v[132:133]
	s_mov_b32 m0, s30
	s_nop 0
	global_load_lds_dwordx4 v[150:151], off
	v_lshl_add_u64 v[150:151], s[28:29], 0, v[136:137]
	s_add_i32 m0, s30, 0x2000
	s_nop 0
	global_load_lds_dwordx4 v[150:151], off
	v_lshl_add_u64 v[150:151], v[224:225], 0, s[14:15]
	s_mov_b32 m0, s42
	s_nop 0
	global_load_lds_dwordx4 v[150:151], off
	v_lshl_add_u64 v[150:151], v[226:227], 0, s[14:15]
	s_mov_b32 m0, s43
	s_nop 0
	global_load_lds_dwordx4 v[150:151], off
	ds_read_b128 v[190:193], v160 offset:49152
	ds_read_b128 v[194:197], v160 offset:50176
	ds_read_b128 v[198:201], v160 offset:51200
	ds_read_b128 v[202:205], v160 offset:52224
	ds_read_b128 v[206:209], v160 offset:53248
	ds_read_b128 v[210:213], v160 offset:54272
	ds_read_b128 v[214:217], v160 offset:55296
	ds_read_b128 v[218:221], v160 offset:56320
	s_waitcnt vmcnt(8)
	s_waitcnt lgkmcnt(0)
	s_barrier
	v_mfma_f32_16x16x32_f16 v[62:65], v[146:149], v[190:193], v[62:65]
	v_mfma_f32_16x16x32_f16 v[58:61], v[166:169], v[190:193], v[58:61]
	v_mfma_f32_16x16x32_f16 v[46:49], v[146:149], v[198:201], v[46:49]
	v_mfma_f32_16x16x32_f16 v[42:45], v[166:169], v[198:201], v[42:45]
	v_mfma_f32_16x16x32_f16 v[30:33], v[146:149], v[206:209], v[30:33]
	v_mfma_f32_16x16x32_f16 v[26:29], v[166:169], v[206:209], v[26:29]
	v_mfma_f32_16x16x32_f16 v[14:17], v[146:149], v[214:217], v[14:17]
	v_mfma_f32_16x16x32_f16 v[10:13], v[166:169], v[214:217], v[10:13]
	v_mfma_f32_16x16x32_f16 v[62:65], v[162:165], v[194:197], v[62:65]
	v_mfma_f32_16x16x32_f16 v[58:61], v[170:173], v[194:197], v[58:61]
	v_mfma_f32_16x16x32_f16 v[46:49], v[162:165], v[202:205], v[46:49]
	v_mfma_f32_16x16x32_f16 v[42:45], v[170:173], v[202:205], v[42:45]
	v_mfma_f32_16x16x32_f16 v[30:33], v[162:165], v[210:213], v[30:33]
	v_mfma_f32_16x16x32_f16 v[26:29], v[170:173], v[210:213], v[26:29]
	v_mfma_f32_16x16x32_f16 v[14:17], v[162:165], v[218:221], v[14:17]
	v_mfma_f32_16x16x32_f16 v[10:13], v[170:173], v[218:221], v[10:13]
	v_mfma_f32_16x16x32_f16 v[54:57], v[174:177], v[190:193], v[54:57]
	v_mfma_f32_16x16x32_f16 v[50:53], v[182:185], v[190:193], v[50:53]
	v_mfma_f32_16x16x32_f16 v[38:41], v[174:177], v[198:201], v[38:41]
	v_mfma_f32_16x16x32_f16 v[34:37], v[182:185], v[198:201], v[34:37]
	v_mfma_f32_16x16x32_f16 v[22:25], v[174:177], v[206:209], v[22:25]
	v_mfma_f32_16x16x32_f16 v[18:21], v[182:185], v[206:209], v[18:21]
	v_mfma_f32_16x16x32_f16 v[6:9], v[174:177], v[214:217], v[6:9]
	v_mfma_f32_16x16x32_f16 v[2:5], v[182:185], v[214:217], v[2:5]
	v_mfma_f32_16x16x32_f16 v[54:57], v[178:181], v[194:197], v[54:57]
	v_mfma_f32_16x16x32_f16 v[50:53], v[186:189], v[194:197], v[50:53]
	v_mfma_f32_16x16x32_f16 v[38:41], v[178:181], v[202:205], v[38:41]
	v_mfma_f32_16x16x32_f16 v[34:37], v[186:189], v[202:205], v[34:37]
	v_mfma_f32_16x16x32_f16 v[22:25], v[178:181], v[210:213], v[22:25]
	v_mfma_f32_16x16x32_f16 v[18:21], v[186:189], v[210:213], v[18:21]
	v_mfma_f32_16x16x32_f16 v[6:9], v[178:181], v[218:221], v[6:9]
	v_mfma_f32_16x16x32_f16 v[2:5], v[186:189], v[218:221], v[2:5]
	s_barrier
	s_add_i32 s51, s51, 2
	s_add_u32 s2, s2, 0x100
	s_addc_u32 s3, s3, 0
	s_add_u32 s49, s49, 0x100
	s_addc_u32 s50, s50, 0
	s_cmp_gt_u32 s51, 13
	s_cbranch_scc0 .LBB0_380
	s_and_b64 vcc, exec, s[16:17]
	s_cbranch_vccz .LBB0_383
	s_barrier

; #define GM_STAGE(bufoff, gbase, voff) do { _Pragma("unroll") for (int _i = 0; _i < 2; ++_i) \
;         __builtin_amdgcn_global_load_lds((const unsigned*)((const char*)(gbase) + (voff)[_i]), (LAS unsigned*)(lds + (bufoff) + ldsw + _i * 8192), 16, 0, 0); } while (0)
; #define GM_LDA(dst, b, h) do { _Pragma("unroll") for (int m = 0; m < 4; ++m) _Pragma("unroll") for (int k = 0; k < 2; ++k) dst[m][k] = *(const LAS s16x8*)(lds + GM_SA(b, h) + aoff + m * 2048 + k * 1024); } while (0)
; #define GM_LDB(dst, b, h) do { _Pragma("unroll") for (int n = 0; n < 2; ++n) _Pragma("unroll") for (int k = 0; k < 2; ++k) dst[n][k] = *(const LAS s16x8*)(lds + GM_SB(b, h) + boff + n * 2048 + k * 1024); } while (0)
; #define GM_MMA(ai, bj, At, Bt) do { __builtin_amdgcn_s_setprio(1); _Pragma("unroll") for (int m = 0; m < 4; ++m) _Pragma("unroll") for (int n = 0; n < 2; ++n) _Pragma("unroll") for (int k = 0; k < 2; ++k) \
;         acc[ai][bj][m][n] = mma16<BF>(Bt[n][k], At[m][k], acc[ai][bj][m][n]); __builtin_amdgcn_s_setprio(0); } while (0)
; #define GM_WAIT_V(n) asm volatile("s_waitcnt vmcnt(" #n ")" ::: "memory")
; #define GM_WAIT_L(n) asm volatile("s_waitcnt lgkmcnt(" #n ")" ::: "memory")
; #define GM_BAR __builtin_amdgcn_s_barrier()
; template <bool BF, bool GATHER = false, class Epi, class Hook>
; __device__ __forceinline__ void gemm_phase(LAS unsigned char* lds, const Gemm g, const Order& S, const Epi& E, Hook& HK) {
;     ...
;             GM_LDB(B0, 0, 0); GM_LDB(B1, 0, 1); GM_SCHED; GM_LDA(At, 0, 0); GM_STA_H1(GM_SA(1, 1), a1, gA1);
;             GM_WAIT_V(8); GM_WAIT_L(0); GM_BAR; GM_MMA(0, 0, At, B0); GM_MMA(0, 1, At, B1); GM_BAR; GM_SCHED;
;             GM_LDA(At, 0, 1); GM_STAGE(GM_SB(0, 0), b2, voffB); GM_STAGE(GM_SB(0, 1), b2 + hstepB, voffB); GM_STA_H0(GM_SA(0, 0), a2, s0);
;             GM_WAIT_V(8); GM_WAIT_L(0); GM_BAR; GM_MMA(1, 0, At, B0); GM_MMA(1, 1, At, B1); GM_BAR; GM_SCHED;
;             GM_LDB(B0, 1, 0); GM_LDB(B1, 1, 1); GM_SCHED; GM_LDA(At, 1, 0); GM_STA_H1(GM_SA(0, 1), a2, s1);
;             GM_WAIT_V(8); GM_WAIT_L(0); GM_BAR; GM_MMA(0, 0, At, B0); GM_MMA(0, 1, At, B1); GM_BAR; GM_SCHED;
;             GM_LDA(At, 1, 1); GM_STAGE(GM_SB(1, 0), b3, voffB); GM_STAGE(GM_SB(1, 1), b3 + hstepB, voffB); GM_STA_H0(GM_SA(1, 0), a3, s0);
;             GM_WAIT_V(8); GM_WAIT_L(0); GM_BAR; GM_MMA(1, 0, At, B0); GM_MMA(1, 1, At, B1); GM_BAR; GM_SCHED;
.LBB0_715:
	s_add_u32 s22, s20, 0xfffc0080
	s_addc_u32 s23, s21, -1
	s_cmp_eq_u32 s47, 12
	s_cselect_b32 s25, s13, s23
	s_cselect_b32 s24, s43, s22
	s_cselect_b32 s23, s15, s46
	s_cselect_b32 s22, s44, s45
	v_lshl_add_u64 v[216:217], s[20:21], 0, v[154:155]
	s_add_i32 m0, s30, 0xc000
	global_load_lds_dwordx4 v[216:217], off
	v_lshl_add_u64 v[216:217], s[20:21], 0, v[156:157]
	s_add_i32 m0, s30, 0xe000
	s_nop 0
	global_load_lds_dwordx4 v[216:217], off
	ds_read_b128 v[130:133], v168
	ds_read_b128 v[134:137], v168 offset:1024
	ds_read_b128 v[138:141], v168 offset:2048
	ds_read_b128 v[142:145], v168 offset:3072
	ds_read_b128 v[162:165], v169
	ds_read_b128 v[172:175], v169 offset:1024
	ds_read_b128 v[176:179], v169 offset:2048
	ds_read_b128 v[180:183], v169 offset:3072
	ds_read_b128 v[184:187], v170
	ds_read_b128 v[188:191], v170 offset:1024
	ds_read_b128 v[192:195], v170 offset:2048
	ds_read_b128 v[196:199], v170 offset:3072
	ds_read_b128 v[200:203], v170 offset:4096
	ds_read_b128 v[204:207], v170 offset:5120
	ds_read_b128 v[208:211], v170 offset:6144
	ds_read_b128 v[212:215], v170 offset:7168
	s_waitcnt vmcnt(8)
	s_waitcnt lgkmcnt(0)
	s_barrier
	v_mfma_f32_16x16x32_f16 v[126:129], v[130:133], v[184:187], v[126:129]
	v_mfma_f32_16x16x32_f16 v[122:125], v[138:141], v[184:187], v[122:125]
	v_mfma_f32_16x16x32_f16 v[110:113], v[130:133], v[192:195], v[110:113]
	v_mfma_f32_16x16x32_f16 v[106:109], v[138:141], v[192:195], v[106:109]
	v_mfma_f32_16x16x32_f16 v[94:97], v[130:133], v[200:203], v[94:97]
	v_mfma_f32_16x16x32_f16 v[90:93], v[138:141], v[200:203], v[90:93]
	v_mfma_f32_16x16x32_f16 v[78:81], v[130:133], v[208:211], v[78:81]
	v_mfma_f32_16x16x32_f16 v[74:77], v[138:141], v[208:211], v[74:77]
	v_mfma_f32_16x16x32_f16 v[126:129], v[134:137], v[188:191], v[126:129]
	v_mfma_f32_16x16x32_f16 v[122:125], v[142:145], v[188:191], v[122:125]
	v_mfma_f32_16x16x32_f16 v[110:113], v[134:137], v[196:199], v[110:113]
	v_mfma_f32_16x16x32_f16 v[106:109], v[142:145], v[196:199], v[106:109]
	v_mfma_f32_16x16x32_f16 v[94:97], v[134:137], v[204:207], v[94:97]
	v_mfma_f32_16x16x32_f16 v[90:93], v[142:145], v[204:207], v[90:93]
	v_mfma_f32_16x16x32_f16 v[78:81], v[134:137], v[212:215], v[78:81]
	v_mfma_f32_16x16x32_f16 v[74:77], v[142:145], v[212:215], v[74:77]
	v_mfma_f32_16x16x32_f16 v[118:121], v[162:165], v[184:187], v[118:121]
	v_mfma_f32_16x16x32_f16 v[114:117], v[176:179], v[184:187], v[114:117]
	v_mfma_f32_16x16x32_f16 v[102:105], v[162:165], v[192:195], v[102:105]
	v_mfma_f32_16x16x32_f16 v[98:101], v[176:179], v[192:195], v[98:101]
	v_mfma_f32_16x16x32_f16 v[86:89], v[162:165], v[200:203], v[86:89]
	v_mfma_f32_16x16x32_f16 v[82:85], v[176:179], v[200:203], v[82:85]
	v_mfma_f32_16x16x32_f16 v[70:73], v[162:165], v[208:211], v[70:73]
	v_mfma_f32_16x16x32_f16 v[66:69], v[176:179], v[208:211], v[66:69]
	v_mfma_f32_16x16x32_f16 v[118:121], v[172:175], v[188:191], v[118:121]
	v_mfma_f32_16x16x32_f16 v[114:117], v[180:183], v[188:191], v[114:117]
	v_mfma_f32_16x16x32_f16 v[102:105], v[172:175], v[196:199], v[102:105]
	v_mfma_f32_16x16x32_f16 v[98:101], v[180:183], v[196:199], v[98:101]
	v_mfma_f32_16x16x32_f16 v[86:89], v[172:175], v[204:207], v[86:89]
	v_mfma_f32_16x16x32_f16 v[82:85], v[180:183], v[204:207], v[82:85]
	v_mfma_f32_16x16x32_f16 v[70:73], v[172:175], v[212:215], v[70:73]
	v_mfma_f32_16x16x32_f16 v[66:69], v[180:183], v[212:215], v[66:69]
	s_barrier
	s_add_i32 s48, s41, s29
	v_lshl_add_u64 v[216:217], s[22:23], 0, v[148:149]
	s_mov_b32 m0, s48
	global_load_lds_dwordx4 v[216:217], off
	s_add_i32 m0, s48, 0x2000
	s_add_u32 s48, s22, 0x40000
	v_lshl_add_u64 v[218:219], s[22:23], 0, v[152:153]
	s_addc_u32 s49, s23, 0
	s_add_i32 s50, s42, s29
	global_load_lds_dwordx4 v[218:219], off
	v_lshl_add_u64 v[220:221], s[48:49], 0, v[148:149]
	s_mov_b32 m0, s50
	v_lshl_add_u64 v[222:223], s[24:25], 0, v[150:151]
	global_load_lds_dwordx4 v[220:221], off
	v_lshl_add_u64 v[220:221], s[48:49], 0, v[152:153]
	s_add_i32 m0, s50, 0x2000
	s_nop 0
	global_load_lds_dwordx4 v[220:221], off
	v_lshl_add_u64 v[220:221], s[24:25], 0, v[146:147]
	s_mov_b32 m0, s30
	s_nop 0
	global_load_lds_dwordx4 v[220:221], off
	s_mov_b32 m0, s31
	s_nop 0
	global_load_lds_dwordx4 v[222:223], off
	ds_read_b128 v[184:187], v170 offset:16384
	ds_read_b128 v[188:191], v170 offset:17408
	ds_read_b128 v[192:195], v170 offset:18432
	ds_read_b128 v[196:199], v170 offset:19456
	ds_read_b128 v[200:203], v170 offset:20480
	ds_read_b128 v[204:207], v170 offset:21504
	ds_read_b128 v[208:211], v170 offset:22528
	ds_read_b128 v[212:215], v170 offset:23552
	s_waitcnt vmcnt(8)
	s_waitcnt lgkmcnt(0)
	s_barrier
; #define GM_STAGE(bufoff, gbase, voff) do { _Pragma("unroll") for (int _i = 0; _i < 2; ++_i) \
;         __builtin_amdgcn_global_load_lds((const unsigned*)((const char*)(gbase) + (voff)[_i]), (LAS unsigned*)(lds + (bufoff) + ldsw + _i * 8192), 16, 0, 0); } while (0)
; #define GM_LDA(dst, b, h) do { _Pragma("unroll") for (int m = 0; m < 4; ++m) _Pragma("unroll") for (int k = 0; k < 2; ++k) dst[m][k] = *(const LAS s16x8*)(lds + GM_SA(b, h) + aoff + m * 2048 + k * 1024); } while (0)
; #define GM_LDB(dst, b, h) do { _Pragma("unroll") for (int n = 0; n < 2; ++n) _Pragma("unroll") for (int k = 0; k < 2; ++k) dst[n][k] = *(const LAS s16x8*)(lds + GM_SB(b, h) + boff + n * 2048 + k * 1024); } while (0)
; #define GM_MMA(ai, bj, At, Bt) do { __builtin_amdgcn_s_setprio(1); _Pragma("unroll") for (int m = 0; m < 4; ++m) _Pragma("unroll") for (int n = 0; n < 2; ++n) _Pragma("unroll") for (int k = 0; k < 2; ++k) \
;         acc[ai][bj][m][n] = mma16<BF>(Bt[n][k], At[m][k], acc[ai][bj][m][n]); __builtin_amdgcn_s_setprio(0); } while (0)
; #define GM_WAIT_V(n) asm volatile("s_waitcnt vmcnt(" #n ")" ::: "memory")
; #define GM_WAIT_L(n) asm volatile("s_waitcnt lgkmcnt(" #n ")" ::: "memory")
; #define GM_BAR __builtin_amdgcn_s_barrier()
; template <bool BF, bool GATHER = false, class Epi, class Hook>
; __device__ __forceinline__ void gemm_phase(LAS unsigned char* lds, const Gemm g, const Order& S, const Epi& E, Hook& HK) {
;     ...
;             GM_LDB(B0, 0, 0); GM_LDB(B1, 0, 1); GM_SCHED; GM_LDA(At, 0, 0); GM_STA_H1(GM_SA(1, 1), a1, gA1);
;             GM_WAIT_V(8); GM_WAIT_L(0); GM_BAR; GM_MMA(0, 0, At, B0); GM_MMA(0, 1, At, B1); GM_BAR; GM_SCHED;
;             GM_LDA(At, 0, 1); GM_STAGE(GM_SB(0, 0), b2, voffB); GM_STAGE(GM_SB(0, 1), b2 + hstepB, voffB); GM_STA_H0(GM_SA(0, 0), a2, s0);
;             GM_WAIT_V(8); GM_WAIT_L(0); GM_BAR; GM_MMA(1, 0, At, B0); GM_MMA(1, 1, At, B1); GM_BAR; GM_SCHED;
;             GM_LDB(B0, 1, 0); GM_LDB(B1, 1, 1); GM_SCHED; GM_LDA(At, 1, 0); GM_STA_H1(GM_SA(0, 1), a2, s1);
;             GM_WAIT_V(8); GM_WAIT_L(0); GM_BAR; GM_MMA(0, 0, At, B0); GM_MMA(0, 1, At, B1); GM_BAR; GM_SCHED;
;             GM_LDA(At, 1, 1); GM_STAGE(GM_SB(1, 0), b3, voffB); GM_STAGE(GM_SB(1, 1), b3 + hstepB, voffB); GM_STA_H0(GM_SA(1, 0), a3, s0);
;             GM_WAIT_V(8); GM_WAIT_L(0); GM_BAR; GM_MMA(1, 0, At, B0); GM_MMA(1, 1, At, B1); GM_BAR; GM_SCHED;
	v_mfma_f32_16x16x32_f16 v[62:65], v[130:133], v[184:187], v[62:65]
	v_mfma_f32_16x16x32_f16 v[58:61], v[138:141], v[184:187], v[58:61]
	v_mfma_f32_16x16x32_f16 v[46:49], v[130:133], v[192:195], v[46:49]
	v_mfma_f32_16x16x32_f16 v[42:45], v[138:141], v[192:195], v[42:45]
	v_mfma_f32_16x16x32_f16 v[30:33], v[130:133], v[200:203], v[30:33]
	v_mfma_f32_16x16x32_f16 v[26:29], v[138:141], v[200:203], v[26:29]
	v_mfma_f32_16x16x32_f16 v[14:17], v[130:133], v[208:211], v[14:17]
	v_mfma_f32_16x16x32_f16 v[10:13], v[138:141], v[208:211], v[10:13]
	v_mfma_f32_16x16x32_f16 v[62:65], v[134:137], v[188:191], v[62:65]
	v_mfma_f32_16x16x32_f16 v[58:61], v[142:145], v[188:191], v[58:61]
	v_mfma_f32_16x16x32_f16 v[46:49], v[134:137], v[196:199], v[46:49]
	v_mfma_f32_16x16x32_f16 v[42:45], v[142:145], v[196:199], v[42:45]
	v_mfma_f32_16x16x32_f16 v[30:33], v[134:137], v[204:207], v[30:33]
	v_mfma_f32_16x16x32_f16 v[26:29], v[142:145], v[204:207], v[26:29]
	v_mfma_f32_16x16x32_f16 v[14:17], v[134:137], v[212:215], v[14:17]
	v_mfma_f32_16x16x32_f16 v[10:13], v[142:145], v[212:215], v[10:13]
	v_mfma_f32_16x16x32_f16 v[54:57], v[162:165], v[184:187], v[54:57]
	v_mfma_f32_16x16x32_f16 v[50:53], v[176:179], v[184:187], v[50:53]
	v_mfma_f32_16x16x32_f16 v[38:41], v[162:165], v[192:195], v[38:41]
	v_mfma_f32_16x16x32_f16 v[34:37], v[176:179], v[192:195], v[34:37]
	v_mfma_f32_16x16x32_f16 v[22:25], v[162:165], v[200:203], v[22:25]
	v_mfma_f32_16x16x32_f16 v[18:21], v[176:179], v[200:203], v[18:21]
	v_mfma_f32_16x16x32_f16 v[6:9], v[162:165], v[208:211], v[6:9]
	v_mfma_f32_16x16x32_f16 v[2:5], v[176:179], v[208:211], v[2:5]
	v_mfma_f32_16x16x32_f16 v[54:57], v[172:175], v[188:191], v[54:57]
	v_mfma_f32_16x16x32_f16 v[50:53], v[180:183], v[188:191], v[50:53]
	v_mfma_f32_16x16x32_f16 v[38:41], v[172:175], v[196:199], v[38:41]
	v_mfma_f32_16x16x32_f16 v[34:37], v[180:183], v[196:199], v[34:37]
	v_mfma_f32_16x16x32_f16 v[22:25], v[172:175], v[204:207], v[22:25]
	v_mfma_f32_16x16x32_f16 v[18:21], v[180:183], v[204:207], v[18:21]
	v_mfma_f32_16x16x32_f16 v[6:9], v[172:175], v[212:215], v[6:9]
	v_mfma_f32_16x16x32_f16 v[2:5], v[180:183], v[212:215], v[2:5]
	s_barrier
	s_add_u32 s24, s24, 0x40000
	s_addc_u32 s25, s25, 0
	s_mov_b32 m0, s33
	v_lshl_add_u64 v[224:225], s[24:25], 0, v[146:147]
	global_load_lds_dwordx4 v[224:225], off
	v_lshl_add_u64 v[224:225], s[24:25], 0, v[150:151]
	s_mov_b32 m0, s34
	s_nop 0
	global_load_lds_dwordx4 v[224:225], off
	s_mov_b32 s49, 0x1c000
	s_mov_b32 s48, 0x18000
	v_add_u32_e32 v244, s48, v166
	v_add_u32_e32 v245, s49, v166
	ds_read_b128 v[130:133], v244
	ds_read_b128 v[134:137], v244 offset:1024
	ds_read_b128 v[138:141], v244 offset:2048
	ds_read_b128 v[142:145], v244 offset:3072
	ds_read_b128 v[162:165], v245
	ds_read_b128 v[172:175], v245 offset:1024
	ds_read_b128 v[176:179], v245 offset:2048
	ds_read_b128 v[180:183], v245 offset:3072
	ds_read_b128 v[184:187], v170 offset:32768
	ds_read_b128 v[188:191], v170 offset:33792
	ds_read_b128 v[192:195], v170 offset:34816
	ds_read_b128 v[196:199], v170 offset:35840
	ds_read_b128 v[200:203], v170 offset:36864
	ds_read_b128 v[204:207], v170 offset:37888
	ds_read_b128 v[208:211], v170 offset:38912
	ds_read_b128 v[212:215], v170 offset:39936
	s_waitcnt vmcnt(8)
	s_waitcnt lgkmcnt(0)
	s_barrier
	v_mfma_f32_16x16x32_f16 v[126:129], v[130:133], v[184:187], v[126:129]
	v_mfma_f32_16x16x32_f16 v[122:125], v[138:141], v[184:187], v[122:125]
	v_mfma_f32_16x16x32_f16 v[110:113], v[130:133], v[192:195], v[110:113]
	v_mfma_f32_16x16x32_f16 v[106:109], v[138:141], v[192:195], v[106:109]
	v_mfma_f32_16x16x32_f16 v[94:97], v[130:133], v[200:203], v[94:97]
	v_mfma_f32_16x16x32_f16 v[90:93], v[138:141], v[200:203], v[90:93]
	v_mfma_f32_16x16x32_f16 v[78:81], v[130:133], v[208:211], v[78:81]
	v_mfma_f32_16x16x32_f16 v[74:77], v[138:141], v[208:211], v[74:77]
	v_mfma_f32_16x16x32_f16 v[126:129], v[134:137], v[188:191], v[126:129]
	v_mfma_f32_16x16x32_f16 v[122:125], v[142:145], v[188:191], v[122:125]
	v_mfma_f32_16x16x32_f16 v[110:113], v[134:137], v[196:199], v[110:113]
	v_mfma_f32_16x16x32_f16 v[106:109], v[142:145], v[196:199], v[106:109]
	v_mfma_f32_16x16x32_f16 v[94:97], v[134:137], v[204:207], v[94:97]
	v_mfma_f32_16x16x32_f16 v[90:93], v[142:145], v[204:207], v[90:93]
	v_mfma_f32_16x16x32_f16 v[78:81], v[134:137], v[212:215], v[78:81]
	v_mfma_f32_16x16x32_f16 v[74:77], v[142:145], v[212:215], v[74:77]
	v_mfma_f32_16x16x32_f16 v[118:121], v[162:165], v[184:187], v[118:121]
	v_mfma_f32_16x16x32_f16 v[114:117], v[176:179], v[184:187], v[114:117]
	v_mfma_f32_16x16x32_f16 v[102:105], v[162:165], v[192:195], v[102:105]
	v_mfma_f32_16x16x32_f16 v[98:101], v[176:179], v[192:195], v[98:101]
	v_mfma_f32_16x16x32_f16 v[86:89], v[162:165], v[200:203], v[86:89]
	v_mfma_f32_16x16x32_f16 v[82:85], v[176:179], v[200:203], v[82:85]
	v_mfma_f32_16x16x32_f16 v[70:73], v[162:165], v[208:211], v[70:73]
	v_mfma_f32_16x16x32_f16 v[66:69], v[176:179], v[208:211], v[66:69]
	v_mfma_f32_16x16x32_f16 v[118:121], v[172:175], v[188:191], v[118:121]
	v_mfma_f32_16x16x32_f16 v[114:117], v[180:183], v[188:191], v[114:117]
	v_mfma_f32_16x16x32_f16 v[102:105], v[172:175], v[196:199], v[102:105]
	v_mfma_f32_16x16x32_f16 v[98:101], v[180:183], v[196:199], v[98:101]
	v_mfma_f32_16x16x32_f16 v[86:89], v[172:175], v[204:207], v[86:89]
	v_mfma_f32_16x16x32_f16 v[82:85], v[180:183], v[204:207], v[82:85]
	v_mfma_f32_16x16x32_f16 v[70:73], v[172:175], v[212:215], v[70:73]
	v_mfma_f32_16x16x32_f16 v[66:69], v[180:183], v[212:215], v[66:69]
	s_barrier
; #define GM_STAGE(bufoff, gbase, voff) do { _Pragma("unroll") for (int _i = 0; _i < 2; ++_i) \
;         __builtin_amdgcn_global_load_lds((const unsigned*)((const char*)(gbase) + (voff)[_i]), (LAS unsigned*)(lds + (bufoff) + ldsw + _i * 8192), 16, 0, 0); } while (0)
; #define GM_LDA(dst, b, h) do { _Pragma("unroll") for (int m = 0; m < 4; ++m) _Pragma("unroll") for (int k = 0; k < 2; ++k) dst[m][k] = *(const LAS s16x8*)(lds + GM_SA(b, h) + aoff + m * 2048 + k * 1024); } while (0)
; #define GM_LDB(dst, b, h) do { _Pragma("unroll") for (int n = 0; n < 2; ++n) _Pragma("unroll") for (int k = 0; k < 2; ++k) dst[n][k] = *(const LAS s16x8*)(lds + GM_SB(b, h) + boff + n * 2048 + k * 1024); } while (0)
; #define GM_MMA(ai, bj, At, Bt) do { __builtin_amdgcn_s_setprio(1); _Pragma("unroll") for (int m = 0; m < 4; ++m) _Pragma("unroll") for (int n = 0; n < 2; ++n) _Pragma("unroll") for (int k = 0; k < 2; ++k) \
;         acc[ai][bj][m][n] = mma16<BF>(Bt[n][k], At[m][k], acc[ai][bj][m][n]); __builtin_amdgcn_s_setprio(0); } while (0)
; #define GM_WAIT_V(n) asm volatile("s_waitcnt vmcnt(" #n ")" ::: "memory")
; #define GM_WAIT_L(n) asm volatile("s_waitcnt lgkmcnt(" #n ")" ::: "memory")
; template <bool BF, bool GATHER = false, class Epi, class Hook>
; __device__ __forceinline__ void gemm_phase(LAS unsigned char* lds, const Gemm g, const Order& S, const Epi& E, Hook& HK) {
;     ...
;             GM_LDB(B0, 0, 0); GM_LDB(B1, 0, 1); GM_SCHED; GM_LDA(At, 0, 0); GM_STA_H1(GM_SA(1, 1), a1, gA1);
;             GM_WAIT_V(8); GM_WAIT_L(0); GM_BAR; GM_MMA(0, 0, At, B0); GM_MMA(0, 1, At, B1); GM_BAR; GM_SCHED;
;             GM_LDA(At, 0, 1); GM_STAGE(GM_SB(0, 0), b2, voffB); GM_STAGE(GM_SB(0, 1), b2 + hstepB, voffB); GM_STA_H0(GM_SA(0, 0), a2, s0);
;             GM_WAIT_V(8); GM_WAIT_L(0); GM_BAR; GM_MMA(1, 0, At, B0); GM_MMA(1, 1, At, B1); GM_BAR; GM_SCHED;
;             GM_LDB(B0, 1, 0); GM_LDB(B1, 1, 1); GM_SCHED; GM_LDA(At, 1, 0); GM_STA_H1(GM_SA(0, 1), a2, s1);
;             GM_WAIT_V(8); GM_WAIT_L(0); GM_BAR; GM_MMA(0, 0, At, B0); GM_MMA(0, 1, At, B1); GM_BAR; GM_SCHED;
;             GM_LDA(At, 1, 1); GM_STAGE(GM_SB(1, 0), b3, voffB); GM_STAGE(GM_SB(1, 1), b3 + hstepB, voffB); GM_STA_H0(GM_SA(1, 0), a3, s0);
;             GM_WAIT_V(8); GM_WAIT_L(0); GM_BAR; GM_MMA(1, 0, At, B0); GM_MMA(1, 1, At, B1); GM_BAR; GM_SCHED;
;         }
;         if (wr == 0) GM_BAR;
	s_add_i32 s24, s48, s29
	v_lshl_add_u64 v[216:217], v[216:217], 0, s[8:9]
	s_mov_b32 m0, s24
	global_load_lds_dwordx4 v[216:217], off
	s_add_i32 m0, s24, 0x2000
	s_add_u32 s22, s22, 0x40080
	v_lshl_add_u64 v[216:217], v[218:219], 0, s[8:9]
	s_addc_u32 s23, s23, 0
	s_add_i32 s24, s49, s29
	global_load_lds_dwordx4 v[216:217], off
	v_lshl_add_u64 v[216:217], s[22:23], 0, v[148:149]
	s_mov_b32 m0, s24
	s_nop 0
	global_load_lds_dwordx4 v[216:217], off
	v_lshl_add_u64 v[216:217], s[22:23], 0, v[152:153]
	s_add_i32 m0, s24, 0x2000
	s_nop 0
	global_load_lds_dwordx4 v[216:217], off
	v_lshl_add_u64 v[216:217], v[220:221], 0, s[8:9]
	s_mov_b32 m0, s38
	s_nop 0
	global_load_lds_dwordx4 v[216:217], off
	v_lshl_add_u64 v[216:217], v[222:223], 0, s[8:9]
	s_mov_b32 m0, s39
	s_nop 0
	global_load_lds_dwordx4 v[216:217], off
	ds_read_b128 v[184:187], v170 offset:49152
	ds_read_b128 v[188:191], v170 offset:50176
	ds_read_b128 v[192:195], v170 offset:51200
	ds_read_b128 v[196:199], v170 offset:52224
	ds_read_b128 v[200:203], v170 offset:53248
	ds_read_b128 v[204:207], v170 offset:54272
	ds_read_b128 v[208:211], v170 offset:55296
	ds_read_b128 v[212:215], v170 offset:56320
	s_waitcnt vmcnt(8)
	s_waitcnt lgkmcnt(0)
	s_barrier
	v_mfma_f32_16x16x32_f16 v[62:65], v[130:133], v[184:187], v[62:65]
	v_mfma_f32_16x16x32_f16 v[58:61], v[138:141], v[184:187], v[58:61]
	v_mfma_f32_16x16x32_f16 v[46:49], v[130:133], v[192:195], v[46:49]
	v_mfma_f32_16x16x32_f16 v[42:45], v[138:141], v[192:195], v[42:45]
	v_mfma_f32_16x16x32_f16 v[30:33], v[130:133], v[200:203], v[30:33]
	v_mfma_f32_16x16x32_f16 v[26:29], v[138:141], v[200:203], v[26:29]
	v_mfma_f32_16x16x32_f16 v[14:17], v[130:133], v[208:211], v[14:17]
	v_mfma_f32_16x16x32_f16 v[10:13], v[138:141], v[208:211], v[10:13]
	v_mfma_f32_16x16x32_f16 v[62:65], v[134:137], v[188:191], v[62:65]
	v_mfma_f32_16x16x32_f16 v[58:61], v[142:145], v[188:191], v[58:61]
	v_mfma_f32_16x16x32_f16 v[46:49], v[134:137], v[196:199], v[46:49]
	v_mfma_f32_16x16x32_f16 v[42:45], v[142:145], v[196:199], v[42:45]
	v_mfma_f32_16x16x32_f16 v[30:33], v[134:137], v[204:207], v[30:33]
	v_mfma_f32_16x16x32_f16 v[26:29], v[142:145], v[204:207], v[26:29]
	v_mfma_f32_16x16x32_f16 v[14:17], v[134:137], v[212:215], v[14:17]
	v_mfma_f32_16x16x32_f16 v[10:13], v[142:145], v[212:215], v[10:13]
	v_mfma_f32_16x16x32_f16 v[54:57], v[162:165], v[184:187], v[54:57]
	v_mfma_f32_16x16x32_f16 v[50:53], v[176:179], v[184:187], v[50:53]
	v_mfma_f32_16x16x32_f16 v[38:41], v[162:165], v[192:195], v[38:41]
	v_mfma_f32_16x16x32_f16 v[34:37], v[176:179], v[192:195], v[34:37]
	v_mfma_f32_16x16x32_f16 v[22:25], v[162:165], v[200:203], v[22:25]
	v_mfma_f32_16x16x32_f16 v[18:21], v[176:179], v[200:203], v[18:21]
	v_mfma_f32_16x16x32_f16 v[6:9], v[162:165], v[208:211], v[6:9]
	v_mfma_f32_16x16x32_f16 v[2:5], v[176:179], v[208:211], v[2:5]
	v_mfma_f32_16x16x32_f16 v[54:57], v[172:175], v[188:191], v[54:57]
	v_mfma_f32_16x16x32_f16 v[50:53], v[180:183], v[188:191], v[50:53]
	v_mfma_f32_16x16x32_f16 v[38:41], v[172:175], v[196:199], v[38:41]
	v_mfma_f32_16x16x32_f16 v[34:37], v[180:183], v[196:199], v[34:37]
	v_mfma_f32_16x16x32_f16 v[22:25], v[172:175], v[204:207], v[22:25]
	v_mfma_f32_16x16x32_f16 v[18:21], v[180:183], v[204:207], v[18:21]
	v_mfma_f32_16x16x32_f16 v[6:9], v[172:175], v[212:215], v[6:9]
	v_mfma_f32_16x16x32_f16 v[2:5], v[180:183], v[212:215], v[2:5]
	s_barrier
	s_add_i32 s47, s47, 2
	s_add_u32 s20, s20, 0x100
	s_addc_u32 s21, s21, 0
	s_add_u32 s45, s45, 0x100
	s_addc_u32 s46, s46, 0
	s_cmp_gt_u32 s47, 13
	s_cbranch_scc0 .LBB0_715
	s_and_b64 vcc, exec, s[10:11]
	s_cbranch_vccz .LBB0_718
	s_barrier

; #define GM_STAGE(bufoff, gbase, voff) do { _Pragma("unroll") for (int _i = 0; _i < 2; ++_i) \
;         __builtin_amdgcn_global_load_lds((const unsigned*)((const char*)(gbase) + (voff)[_i]), (LAS unsigned*)(lds + (bufoff) + ldsw + _i * 8192), 16, 0, 0); } while (0)
; #define GM_LDA(dst, b, h) do { _Pragma("unroll") for (int m = 0; m < 4; ++m) _Pragma("unroll") for (int k = 0; k < 2; ++k) dst[m][k] = *(const LAS s16x8*)(lds + GM_SA(b, h) + aoff + m * 2048 + k * 1024); } while (0)
; #define GM_LDB(dst, b, h) do { _Pragma("unroll") for (int n = 0; n < 2; ++n) _Pragma("unroll") for (int k = 0; k < 2; ++k) dst[n][k] = *(const LAS s16x8*)(lds + GM_SB(b, h) + boff + n * 2048 + k * 1024); } while (0)
; #define GM_MMA(ai, bj, At, Bt) do { __builtin_amdgcn_s_setprio(1); _Pragma("unroll") for (int m = 0; m < 4; ++m) _Pragma("unroll") for (int n = 0; n < 2; ++n) _Pragma("unroll") for (int k = 0; k < 2; ++k) \
;         acc[ai][bj][m][n] = mma16<BF>(Bt[n][k], At[m][k], acc[ai][bj][m][n]); __builtin_amdgcn_s_setprio(0); } while (0)
; #define GM_WAIT_V(n) asm volatile("s_waitcnt vmcnt(" #n ")" ::: "memory")
; #define GM_WAIT_L(n) asm volatile("s_waitcnt lgkmcnt(" #n ")" ::: "memory")
; #define GM_BAR __builtin_amdgcn_s_barrier()
; template <bool BF, bool GATHER = false, class Epi, class Hook>
; __device__ __forceinline__ void gemm_phase(LAS unsigned char* lds, const Gemm g, const Order& S, const Epi& E, Hook& HK) {
;     ...
;             GM_LDB(B0, 0, 0); GM_LDB(B1, 0, 1); GM_SCHED; GM_LDA(At, 0, 0); GM_STA_H1(GM_SA(1, 1), a1, gA1);
;             GM_WAIT_V(8); GM_WAIT_L(0); GM_BAR; GM_MMA(0, 0, At, B0); GM_MMA(0, 1, At, B1); GM_BAR; GM_SCHED;
;             GM_LDA(At, 0, 1); GM_STAGE(GM_SB(0, 0), b2, voffB); GM_STAGE(GM_SB(0, 1), b2 + hstepB, voffB); GM_STA_H0(GM_SA(0, 0), a2, s0);
;             GM_WAIT_V(8); GM_WAIT_L(0); GM_BAR; GM_MMA(1, 0, At, B0); GM_MMA(1, 1, At, B1); GM_BAR; GM_SCHED;
;             GM_LDB(B0, 1, 0); GM_LDB(B1, 1, 1); GM_SCHED; GM_LDA(At, 1, 0); GM_STA_H1(GM_SA(0, 1), a2, s1);
;             GM_WAIT_V(8); GM_WAIT_L(0); GM_BAR; GM_MMA(0, 0, At, B0); GM_MMA(0, 1, At, B1); GM_BAR; GM_SCHED;
;             GM_LDA(At, 1, 1); GM_STAGE(GM_SB(1, 0), b3, voffB); GM_STAGE(GM_SB(1, 1), b3 + hstepB, voffB); GM_STA_H0(GM_SA(1, 0), a3, s0);
;             GM_WAIT_V(8); GM_WAIT_L(0); GM_BAR; GM_MMA(1, 0, At, B0); GM_MMA(1, 1, At, B1); GM_BAR; GM_SCHED;
.LBB0_1011:
	s_add_u32 s22, s90, s2
	s_addc_u32 s23, s91, s3
	s_add_u32 s24, s22, 0x11e00100
	s_addc_u32 s25, s23, 0
	s_add_u32 s44, s21, s2
	s_addc_u32 s45, s42, s3
	s_cmpk_eq_i32 s2, 0x700
	s_cselect_b64 vcc, -1, 0
	s_and_b64 s[22:23], vcc, exec
	v_cndmask_b32_e32 v134, v142, v159, vcc
	s_cselect_b32 s25, s69, s25
	s_cselect_b32 s24, s68, s24
	v_cndmask_b32_e32 v228, v146, v162, vcc
	v_cndmask_b32_e32 v141, v158, v160, vcc
	v_cndmask_b32_e32 v145, v157, v161, vcc
	s_cselect_b32 s23, s1, s45
	s_cselect_b32 s22, s0, s44
	v_lshl_add_u64 v[230:231], v[150:151], 0, s[2:3]
	s_add_i32 m0, s28, 0xc000
	global_load_lds_dwordx4 v[230:231], off
	v_lshl_add_u64 v[230:231], v[148:149], 0, s[2:3]
	s_add_i32 m0, s28, 0xe000
	s_nop 0
	global_load_lds_dwordx4 v[230:231], off
	v_add_u32_e32 v244, s35, v156
	ds_read_b128 v[164:167], v244
	ds_read_b128 v[168:171], v244 offset:1024
	ds_read_b128 v[172:175], v244 offset:2048
	ds_read_b128 v[176:179], v244 offset:3072
	v_add_u32_e32 v244, s36, v156
	ds_read_b128 v[180:183], v244
	ds_read_b128 v[184:187], v244 offset:1024
	ds_read_b128 v[188:191], v244 offset:2048
	ds_read_b128 v[192:195], v244 offset:3072
	ds_read_b128 v[196:199], v147
	ds_read_b128 v[200:203], v147 offset:1024
	ds_read_b128 v[204:207], v147 offset:2048
	ds_read_b128 v[208:211], v147 offset:3072
	ds_read_b128 v[212:215], v147 offset:4096
	ds_read_b128 v[216:219], v147 offset:5120
	ds_read_b128 v[220:223], v147 offset:6144
	ds_read_b128 v[224:227], v147 offset:7168
	s_waitcnt vmcnt(8)
	s_waitcnt lgkmcnt(0)
	s_barrier
	v_mfma_f32_16x16x32_bf16 v[98:101], v[164:167], v[196:199], v[98:101]
	v_mfma_f32_16x16x32_bf16 v[94:97], v[172:175], v[196:199], v[94:97]
	v_mfma_f32_16x16x32_bf16 v[90:93], v[164:167], v[204:207], v[90:93]
	v_mfma_f32_16x16x32_bf16 v[86:89], v[172:175], v[204:207], v[86:89]
	v_mfma_f32_16x16x32_bf16 v[82:85], v[164:167], v[212:215], v[82:85]
	v_mfma_f32_16x16x32_bf16 v[78:81], v[172:175], v[212:215], v[78:81]
	v_mfma_f32_16x16x32_bf16 v[74:77], v[164:167], v[220:223], v[74:77]
	v_mfma_f32_16x16x32_bf16 v[70:73], v[172:175], v[220:223], v[70:73]
	v_mfma_f32_16x16x32_bf16 v[98:101], v[168:171], v[200:203], v[98:101]
	v_mfma_f32_16x16x32_bf16 v[94:97], v[176:179], v[200:203], v[94:97]
	v_mfma_f32_16x16x32_bf16 v[90:93], v[168:171], v[208:211], v[90:93]
	v_mfma_f32_16x16x32_bf16 v[86:89], v[176:179], v[208:211], v[86:89]
	v_mfma_f32_16x16x32_bf16 v[82:85], v[168:171], v[216:219], v[82:85]
	v_mfma_f32_16x16x32_bf16 v[78:81], v[176:179], v[216:219], v[78:81]
	v_mfma_f32_16x16x32_bf16 v[74:77], v[168:171], v[224:227], v[74:77]
	v_mfma_f32_16x16x32_bf16 v[70:73], v[176:179], v[224:227], v[70:73]
	v_mfma_f32_16x16x32_bf16 v[66:69], v[180:183], v[196:199], v[66:69]
	v_mfma_f32_16x16x32_bf16 v[62:65], v[188:191], v[196:199], v[62:65]
	v_mfma_f32_16x16x32_bf16 v[58:61], v[180:183], v[204:207], v[58:61]
	v_mfma_f32_16x16x32_bf16 v[54:57], v[188:191], v[204:207], v[54:57]
	v_mfma_f32_16x16x32_bf16 v[50:53], v[180:183], v[212:215], v[50:53]
	v_mfma_f32_16x16x32_bf16 v[46:49], v[188:191], v[212:215], v[46:49]
	v_mfma_f32_16x16x32_bf16 v[42:45], v[180:183], v[220:223], v[42:45]
	v_mfma_f32_16x16x32_bf16 v[38:41], v[188:191], v[220:223], v[38:41]
	v_mfma_f32_16x16x32_bf16 v[66:69], v[184:187], v[200:203], v[66:69]
	v_mfma_f32_16x16x32_bf16 v[62:65], v[192:195], v[200:203], v[62:65]
	v_mfma_f32_16x16x32_bf16 v[58:61], v[184:187], v[208:211], v[58:61]
	v_mfma_f32_16x16x32_bf16 v[54:57], v[192:195], v[208:211], v[54:57]
	v_mfma_f32_16x16x32_bf16 v[50:53], v[184:187], v[216:219], v[50:53]
	v_mfma_f32_16x16x32_bf16 v[46:49], v[192:195], v[216:219], v[46:49]
	v_mfma_f32_16x16x32_bf16 v[42:45], v[184:187], v[224:227], v[42:45]
	v_mfma_f32_16x16x32_bf16 v[38:41], v[192:195], v[224:227], v[38:41]
	s_barrier
	s_add_i32 s44, s35, s11
	v_lshl_add_u64 v[230:231], s[22:23], 0, v[130:131]
	s_mov_b32 m0, s44
	global_load_lds_dwordx4 v[230:231], off
	s_add_i32 m0, s44, 0x2000
	s_add_u32 s44, s22, 0x40000
	v_lshl_add_u64 v[232:233], s[22:23], 0, v[132:133]
	s_addc_u32 s45, s23, 0
	s_add_i32 s46, s36, s11
	global_load_lds_dwordx4 v[232:233], off
	v_lshl_add_u64 v[234:235], s[44:45], 0, v[130:131]
	s_mov_b32 m0, s46
	v_mov_b32_e32 v229, v135
	global_load_lds_dwordx4 v[234:235], off
	v_lshl_add_u64 v[234:235], s[44:45], 0, v[132:133]
	s_add_i32 m0, s46, 0x2000
	s_nop 0
	global_load_lds_dwordx4 v[234:235], off
	s_mov_b32 m0, s28
	v_lshl_add_u64 v[234:235], s[24:25], 0, v[134:135]
	global_load_lds_dwordx4 v134, s[24:25]
	s_mov_b32 m0, s29
	s_nop 0
	global_load_lds_dwordx4 v228, s[24:25]
	v_lshl_add_u64 v[228:229], s[24:25], 0, v[228:229]
	ds_read_b128 v[196:199], v147 offset:16384
	ds_read_b128 v[200:203], v147 offset:17408
	ds_read_b128 v[204:207], v147 offset:18432
	ds_read_b128 v[208:211], v147 offset:19456
	ds_read_b128 v[212:215], v147 offset:20480
	ds_read_b128 v[216:219], v147 offset:21504
	ds_read_b128 v[220:223], v147 offset:22528
	ds_read_b128 v[224:227], v147 offset:23552
	s_waitcnt vmcnt(8)
	s_waitcnt lgkmcnt(0)
	s_barrier
; #define GM_STAGE(bufoff, gbase, voff) do { _Pragma("unroll") for (int _i = 0; _i < 2; ++_i) \
;         __builtin_amdgcn_global_load_lds((const unsigned*)((const char*)(gbase) + (voff)[_i]), (LAS unsigned*)(lds + (bufoff) + ldsw + _i * 8192), 16, 0, 0); } while (0)
; #define GM_LDA(dst, b, h) do { _Pragma("unroll") for (int m = 0; m < 4; ++m) _Pragma("unroll") for (int k = 0; k < 2; ++k) dst[m][k] = *(const LAS s16x8*)(lds + GM_SA(b, h) + aoff + m * 2048 + k * 1024); } while (0)
; #define GM_LDB(dst, b, h) do { _Pragma("unroll") for (int n = 0; n < 2; ++n) _Pragma("unroll") for (int k = 0; k < 2; ++k) dst[n][k] = *(const LAS s16x8*)(lds + GM_SB(b, h) + boff + n * 2048 + k * 1024); } while (0)
; #define GM_MMA(ai, bj, At, Bt) do { __builtin_amdgcn_s_setprio(1); _Pragma("unroll") for (int m = 0; m < 4; ++m) _Pragma("unroll") for (int n = 0; n < 2; ++n) _Pragma("unroll") for (int k = 0; k < 2; ++k) \
;         acc[ai][bj][m][n] = mma16<BF>(Bt[n][k], At[m][k], acc[ai][bj][m][n]); __builtin_amdgcn_s_setprio(0); } while (0)
; #define GM_WAIT_V(n) asm volatile("s_waitcnt vmcnt(" #n ")" ::: "memory")
; #define GM_WAIT_L(n) asm volatile("s_waitcnt lgkmcnt(" #n ")" ::: "memory")
; #define GM_BAR __builtin_amdgcn_s_barrier()
; template <bool BF, bool GATHER = false, class Epi, class Hook>
; __device__ __forceinline__ void gemm_phase(LAS unsigned char* lds, const Gemm g, const Order& S, const Epi& E, Hook& HK) {
;     ...
;             GM_LDB(B0, 0, 0); GM_LDB(B1, 0, 1); GM_SCHED; GM_LDA(At, 0, 0); GM_STA_H1(GM_SA(1, 1), a1, gA1);
;             GM_WAIT_V(8); GM_WAIT_L(0); GM_BAR; GM_MMA(0, 0, At, B0); GM_MMA(0, 1, At, B1); GM_BAR; GM_SCHED;
;             GM_LDA(At, 0, 1); GM_STAGE(GM_SB(0, 0), b2, voffB); GM_STAGE(GM_SB(0, 1), b2 + hstepB, voffB); GM_STA_H0(GM_SA(0, 0), a2, s0);
;             GM_WAIT_V(8); GM_WAIT_L(0); GM_BAR; GM_MMA(1, 0, At, B0); GM_MMA(1, 1, At, B1); GM_BAR; GM_SCHED;
;             GM_LDB(B0, 1, 0); GM_LDB(B1, 1, 1); GM_SCHED; GM_LDA(At, 1, 0); GM_STA_H1(GM_SA(0, 1), a2, s1);
;             GM_WAIT_V(8); GM_WAIT_L(0); GM_BAR; GM_MMA(0, 0, At, B0); GM_MMA(0, 1, At, B1); GM_BAR; GM_SCHED;
;             GM_LDA(At, 1, 1); GM_STAGE(GM_SB(1, 0), b3, voffB); GM_STAGE(GM_SB(1, 1), b3 + hstepB, voffB); GM_STA_H0(GM_SA(1, 0), a3, s0);
;             GM_WAIT_V(8); GM_WAIT_L(0); GM_BAR; GM_MMA(1, 0, At, B0); GM_MMA(1, 1, At, B1); GM_BAR; GM_SCHED;
	v_mfma_f32_16x16x32_bf16 v[34:37], v[164:167], v[196:199], v[34:37]
	v_mfma_f32_16x16x32_bf16 v[30:33], v[172:175], v[196:199], v[30:33]
	v_mfma_f32_16x16x32_bf16 v[26:29], v[164:167], v[204:207], v[26:29]
	v_mfma_f32_16x16x32_bf16 v[22:25], v[172:175], v[204:207], v[22:25]
	v_mfma_f32_16x16x32_bf16 v[18:21], v[164:167], v[212:215], v[18:21]
	v_mfma_f32_16x16x32_bf16 v[14:17], v[172:175], v[212:215], v[14:17]
	v_mfma_f32_16x16x32_bf16 v[10:13], v[164:167], v[220:223], v[10:13]
	v_mfma_f32_16x16x32_bf16 v[6:9], v[172:175], v[220:223], v[6:9]
	v_mfma_f32_16x16x32_bf16 v[34:37], v[168:171], v[200:203], v[34:37]
	v_mfma_f32_16x16x32_bf16 v[30:33], v[176:179], v[200:203], v[30:33]
	v_mfma_f32_16x16x32_bf16 v[26:29], v[168:171], v[208:211], v[26:29]
	v_mfma_f32_16x16x32_bf16 v[22:25], v[176:179], v[208:211], v[22:25]
	v_mfma_f32_16x16x32_bf16 v[18:21], v[168:171], v[216:219], v[18:21]
	v_mfma_f32_16x16x32_bf16 v[14:17], v[176:179], v[216:219], v[14:17]
	v_mfma_f32_16x16x32_bf16 v[10:13], v[168:171], v[224:227], v[10:13]
	v_mfma_f32_16x16x32_bf16 v[6:9], v[176:179], v[224:227], v[6:9]
	v_mfma_f32_16x16x32_bf16 v[2:5], v[180:183], v[196:199], v[2:5]
	v_mfma_f32_16x16x32_bf16 v[102:105], v[188:191], v[196:199], v[102:105]
	v_mfma_f32_16x16x32_bf16 v[106:109], v[180:183], v[204:207], v[106:109]
	v_mfma_f32_16x16x32_bf16 v[110:113], v[188:191], v[204:207], v[110:113]
	v_mfma_f32_16x16x32_bf16 v[114:117], v[180:183], v[212:215], v[114:117]
	v_mfma_f32_16x16x32_bf16 v[118:121], v[188:191], v[212:215], v[118:121]
	v_mfma_f32_16x16x32_bf16 v[122:125], v[180:183], v[220:223], v[122:125]
	v_mfma_f32_16x16x32_bf16 v[126:129], v[188:191], v[220:223], v[126:129]
	v_mfma_f32_16x16x32_bf16 v[2:5], v[184:187], v[200:203], v[2:5]
	v_mfma_f32_16x16x32_bf16 v[102:105], v[192:195], v[200:203], v[102:105]
	v_mfma_f32_16x16x32_bf16 v[106:109], v[184:187], v[208:211], v[106:109]
	v_mfma_f32_16x16x32_bf16 v[110:113], v[192:195], v[208:211], v[110:113]
	v_mfma_f32_16x16x32_bf16 v[114:117], v[184:187], v[216:219], v[114:117]
	v_mfma_f32_16x16x32_bf16 v[118:121], v[192:195], v[216:219], v[118:121]
	v_mfma_f32_16x16x32_bf16 v[122:125], v[184:187], v[224:227], v[122:125]
	v_mfma_f32_16x16x32_bf16 v[126:129], v[192:195], v[224:227], v[126:129]
	s_barrier
	s_mov_b32 m0, s30
	global_load_lds_dwordx4 v141, s[24:25]
	s_mov_b32 m0, s31
	s_nop 0
	global_load_lds_dwordx4 v145, s[24:25]
	s_mov_b32 s45, 0x1c000
	s_mov_b32 s44, 0x18000
	v_add_u32_e32 v245, s44, v156
	ds_read_b128 v[164:167], v245
	ds_read_b128 v[168:171], v245 offset:1024
	ds_read_b128 v[172:175], v245 offset:2048
	ds_read_b128 v[176:179], v245 offset:3072
	v_add_u32_e32 v245, s45, v156
	ds_read_b128 v[180:183], v245
	ds_read_b128 v[184:187], v245 offset:1024
	ds_read_b128 v[188:191], v245 offset:2048
	ds_read_b128 v[192:195], v245 offset:3072
	ds_read_b128 v[196:199], v147 offset:32768
	ds_read_b128 v[200:203], v147 offset:33792
	ds_read_b128 v[204:207], v147 offset:34816
	ds_read_b128 v[208:211], v147 offset:35840
	ds_read_b128 v[212:215], v147 offset:36864
	ds_read_b128 v[216:219], v147 offset:37888
	ds_read_b128 v[220:223], v147 offset:38912
	ds_read_b128 v[224:227], v147 offset:39936
	s_waitcnt vmcnt(8)
	s_waitcnt lgkmcnt(0)
	s_barrier
	v_mfma_f32_16x16x32_bf16 v[98:101], v[164:167], v[196:199], v[98:101]
	v_mfma_f32_16x16x32_bf16 v[94:97], v[172:175], v[196:199], v[94:97]
	v_mfma_f32_16x16x32_bf16 v[90:93], v[164:167], v[204:207], v[90:93]
	v_mfma_f32_16x16x32_bf16 v[86:89], v[172:175], v[204:207], v[86:89]
	v_mfma_f32_16x16x32_bf16 v[82:85], v[164:167], v[212:215], v[82:85]
	v_mfma_f32_16x16x32_bf16 v[78:81], v[172:175], v[212:215], v[78:81]
	v_mfma_f32_16x16x32_bf16 v[74:77], v[164:167], v[220:223], v[74:77]
	v_mfma_f32_16x16x32_bf16 v[70:73], v[172:175], v[220:223], v[70:73]
	v_mfma_f32_16x16x32_bf16 v[98:101], v[168:171], v[200:203], v[98:101]
	v_mfma_f32_16x16x32_bf16 v[94:97], v[176:179], v[200:203], v[94:97]
	v_mfma_f32_16x16x32_bf16 v[90:93], v[168:171], v[208:211], v[90:93]
	v_mfma_f32_16x16x32_bf16 v[86:89], v[176:179], v[208:211], v[86:89]
	v_mfma_f32_16x16x32_bf16 v[82:85], v[168:171], v[216:219], v[82:85]
	v_mfma_f32_16x16x32_bf16 v[78:81], v[176:179], v[216:219], v[78:81]
	v_mfma_f32_16x16x32_bf16 v[74:77], v[168:171], v[224:227], v[74:77]
	v_mfma_f32_16x16x32_bf16 v[70:73], v[176:179], v[224:227], v[70:73]
	v_mfma_f32_16x16x32_bf16 v[66:69], v[180:183], v[196:199], v[66:69]
	v_mfma_f32_16x16x32_bf16 v[62:65], v[188:191], v[196:199], v[62:65]
	v_mfma_f32_16x16x32_bf16 v[58:61], v[180:183], v[204:207], v[58:61]
	v_mfma_f32_16x16x32_bf16 v[54:57], v[188:191], v[204:207], v[54:57]
	v_mfma_f32_16x16x32_bf16 v[50:53], v[180:183], v[212:215], v[50:53]
	v_mfma_f32_16x16x32_bf16 v[46:49], v[188:191], v[212:215], v[46:49]
	v_mfma_f32_16x16x32_bf16 v[42:45], v[180:183], v[220:223], v[42:45]
	v_mfma_f32_16x16x32_bf16 v[38:41], v[188:191], v[220:223], v[38:41]
	v_mfma_f32_16x16x32_bf16 v[66:69], v[184:187], v[200:203], v[66:69]
	v_mfma_f32_16x16x32_bf16 v[62:65], v[192:195], v[200:203], v[62:65]
	v_mfma_f32_16x16x32_bf16 v[58:61], v[184:187], v[208:211], v[58:61]
	v_mfma_f32_16x16x32_bf16 v[54:57], v[192:195], v[208:211], v[54:57]
	v_mfma_f32_16x16x32_bf16 v[50:53], v[184:187], v[216:219], v[50:53]
	v_mfma_f32_16x16x32_bf16 v[46:49], v[192:195], v[216:219], v[46:49]
	v_mfma_f32_16x16x32_bf16 v[42:45], v[184:187], v[224:227], v[42:45]
	v_mfma_f32_16x16x32_bf16 v[38:41], v[192:195], v[224:227], v[38:41]
	s_barrier
; #define GM_STAGE(bufoff, gbase, voff) do { _Pragma("unroll") for (int _i = 0; _i < 2; ++_i) \
;         __builtin_amdgcn_global_load_lds((const unsigned*)((const char*)(gbase) + (voff)[_i]), (LAS unsigned*)(lds + (bufoff) + ldsw + _i * 8192), 16, 0, 0); } while (0)
; #define GM_LDA(dst, b, h) do { _Pragma("unroll") for (int m = 0; m < 4; ++m) _Pragma("unroll") for (int k = 0; k < 2; ++k) dst[m][k] = *(const LAS s16x8*)(lds + GM_SA(b, h) + aoff + m * 2048 + k * 1024); } while (0)
; #define GM_LDB(dst, b, h) do { _Pragma("unroll") for (int n = 0; n < 2; ++n) _Pragma("unroll") for (int k = 0; k < 2; ++k) dst[n][k] = *(const LAS s16x8*)(lds + GM_SB(b, h) + boff + n * 2048 + k * 1024); } while (0)
; #define GM_MMA(ai, bj, At, Bt) do { __builtin_amdgcn_s_setprio(1); _Pragma("unroll") for (int m = 0; m < 4; ++m) _Pragma("unroll") for (int n = 0; n < 2; ++n) _Pragma("unroll") for (int k = 0; k < 2; ++k) \
;         acc[ai][bj][m][n] = mma16<BF>(Bt[n][k], At[m][k], acc[ai][bj][m][n]); __builtin_amdgcn_s_setprio(0); } while (0)
; #define GM_WAIT_V(n) asm volatile("s_waitcnt vmcnt(" #n ")" ::: "memory")
; #define GM_WAIT_L(n) asm volatile("s_waitcnt lgkmcnt(" #n ")" ::: "memory")
; template <bool BF, bool GATHER = false, class Epi, class Hook>
; __device__ __forceinline__ void gemm_phase(LAS unsigned char* lds, const Gemm g, const Order& S, const Epi& E, Hook& HK) {
;     ...
;             GM_LDB(B0, 0, 0); GM_LDB(B1, 0, 1); GM_SCHED; GM_LDA(At, 0, 0); GM_STA_H1(GM_SA(1, 1), a1, gA1);
;             GM_WAIT_V(8); GM_WAIT_L(0); GM_BAR; GM_MMA(0, 0, At, B0); GM_MMA(0, 1, At, B1); GM_BAR; GM_SCHED;
;             GM_LDA(At, 0, 1); GM_STAGE(GM_SB(0, 0), b2, voffB); GM_STAGE(GM_SB(0, 1), b2 + hstepB, voffB); GM_STA_H0(GM_SA(0, 0), a2, s0);
;             GM_WAIT_V(8); GM_WAIT_L(0); GM_BAR; GM_MMA(1, 0, At, B0); GM_MMA(1, 1, At, B1); GM_BAR; GM_SCHED;
;             GM_LDB(B0, 1, 0); GM_LDB(B1, 1, 1); GM_SCHED; GM_LDA(At, 1, 0); GM_STA_H1(GM_SA(0, 1), a2, s1);
;             GM_WAIT_V(8); GM_WAIT_L(0); GM_BAR; GM_MMA(0, 0, At, B0); GM_MMA(0, 1, At, B1); GM_BAR; GM_SCHED;
;             GM_LDA(At, 1, 1); GM_STAGE(GM_SB(1, 0), b3, voffB); GM_STAGE(GM_SB(1, 1), b3 + hstepB, voffB); GM_STA_H0(GM_SA(1, 0), a3, s0);
;             GM_WAIT_V(8); GM_WAIT_L(0); GM_BAR; GM_MMA(1, 0, At, B0); GM_MMA(1, 1, At, B1); GM_BAR; GM_SCHED;
;         }
;         if (wr == 0) GM_BAR;
	s_add_i32 s24, s44, s11
	v_lshl_add_u64 v[230:231], v[230:231], 0, s[14:15]
	s_mov_b32 m0, s24
	global_load_lds_dwordx4 v[230:231], off
	s_add_i32 m0, s24, 0x2000
	s_add_u32 s22, s22, 0x40080
	v_lshl_add_u64 v[230:231], v[232:233], 0, s[14:15]
	s_addc_u32 s23, s23, 0
	s_add_i32 s24, s45, s11
	global_load_lds_dwordx4 v[230:231], off
	v_lshl_add_u64 v[230:231], s[22:23], 0, v[130:131]
	s_mov_b32 m0, s24
	v_lshl_add_u64 v[228:229], v[228:229], 0, s[14:15]
	global_load_lds_dwordx4 v[230:231], off
	v_lshl_add_u64 v[230:231], s[22:23], 0, v[132:133]
	s_add_i32 m0, s24, 0x2000
	s_nop 0
	global_load_lds_dwordx4 v[230:231], off
	v_lshl_add_u64 v[230:231], v[234:235], 0, s[14:15]
	s_mov_b32 m0, s33
	s_nop 0
	global_load_lds_dwordx4 v[230:231], off
	s_mov_b32 m0, s34
	s_nop 0
	global_load_lds_dwordx4 v[228:229], off
	ds_read_b128 v[196:199], v147 offset:49152
	ds_read_b128 v[200:203], v147 offset:50176
	ds_read_b128 v[204:207], v147 offset:51200
	ds_read_b128 v[208:211], v147 offset:52224
	ds_read_b128 v[212:215], v147 offset:53248
	ds_read_b128 v[216:219], v147 offset:54272
	ds_read_b128 v[220:223], v147 offset:55296
	ds_read_b128 v[224:227], v147 offset:56320
	s_waitcnt vmcnt(8)
	s_waitcnt lgkmcnt(0)
	s_barrier
	v_mfma_f32_16x16x32_bf16 v[34:37], v[164:167], v[196:199], v[34:37]
	v_mfma_f32_16x16x32_bf16 v[30:33], v[172:175], v[196:199], v[30:33]
	v_mfma_f32_16x16x32_bf16 v[26:29], v[164:167], v[204:207], v[26:29]
	v_mfma_f32_16x16x32_bf16 v[22:25], v[172:175], v[204:207], v[22:25]
	v_mfma_f32_16x16x32_bf16 v[18:21], v[164:167], v[212:215], v[18:21]
	v_mfma_f32_16x16x32_bf16 v[14:17], v[172:175], v[212:215], v[14:17]
	v_mfma_f32_16x16x32_bf16 v[10:13], v[164:167], v[220:223], v[10:13]
	v_mfma_f32_16x16x32_bf16 v[6:9], v[172:175], v[220:223], v[6:9]
	v_mfma_f32_16x16x32_bf16 v[34:37], v[168:171], v[200:203], v[34:37]
	v_mfma_f32_16x16x32_bf16 v[30:33], v[176:179], v[200:203], v[30:33]
	v_mfma_f32_16x16x32_bf16 v[26:29], v[168:171], v[208:211], v[26:29]
	v_mfma_f32_16x16x32_bf16 v[22:25], v[176:179], v[208:211], v[22:25]
	v_mfma_f32_16x16x32_bf16 v[18:21], v[168:171], v[216:219], v[18:21]
	v_mfma_f32_16x16x32_bf16 v[14:17], v[176:179], v[216:219], v[14:17]
	v_mfma_f32_16x16x32_bf16 v[10:13], v[168:171], v[224:227], v[10:13]
	v_mfma_f32_16x16x32_bf16 v[6:9], v[176:179], v[224:227], v[6:9]
	v_mfma_f32_16x16x32_bf16 v[2:5], v[180:183], v[196:199], v[2:5]
	v_mfma_f32_16x16x32_bf16 v[102:105], v[188:191], v[196:199], v[102:105]
	v_mfma_f32_16x16x32_bf16 v[106:109], v[180:183], v[204:207], v[106:109]
	v_mfma_f32_16x16x32_bf16 v[110:113], v[188:191], v[204:207], v[110:113]
	v_mfma_f32_16x16x32_bf16 v[114:117], v[180:183], v[212:215], v[114:117]
	v_mfma_f32_16x16x32_bf16 v[118:121], v[188:191], v[212:215], v[118:121]
	v_mfma_f32_16x16x32_bf16 v[122:125], v[180:183], v[220:223], v[122:125]
	v_mfma_f32_16x16x32_bf16 v[126:129], v[188:191], v[220:223], v[126:129]
	v_mfma_f32_16x16x32_bf16 v[2:5], v[184:187], v[200:203], v[2:5]
	v_mfma_f32_16x16x32_bf16 v[102:105], v[192:195], v[200:203], v[102:105]
	v_mfma_f32_16x16x32_bf16 v[106:109], v[184:187], v[208:211], v[106:109]
	v_mfma_f32_16x16x32_bf16 v[110:113], v[192:195], v[208:211], v[110:113]
	v_mfma_f32_16x16x32_bf16 v[114:117], v[184:187], v[216:219], v[114:117]
	v_mfma_f32_16x16x32_bf16 v[118:121], v[192:195], v[216:219], v[118:121]
	v_mfma_f32_16x16x32_bf16 v[122:125], v[184:187], v[224:227], v[122:125]
	v_mfma_f32_16x16x32_bf16 v[126:129], v[192:195], v[224:227], v[126:129]
	s_barrier
	s_add_i32 s43, s43, 2
	s_add_u32 s2, s2, 0x100
	s_addc_u32 s3, s3, 0
	s_cmp_gt_u32 s43, 13
	s_cbranch_scc0 .LBB0_1011
	s_and_b64 vcc, exec, s[18:19]
	s_cbranch_vccz .LBB0_1014
	s_barrier

; #define GM_STAGE(bufoff, gbase, voff) do { _Pragma("unroll") for (int _i = 0; _i < 2; ++_i) \
;         __builtin_amdgcn_global_load_lds((const unsigned*)((const char*)(gbase) + (voff)[_i]), (LAS unsigned*)(lds + (bufoff) + ldsw + _i * 8192), 16, 0, 0); } while (0)
; #define GM_LDA(dst, b, h) do { _Pragma("unroll") for (int m = 0; m < 4; ++m) _Pragma("unroll") for (int k = 0; k < 2; ++k) dst[m][k] = *(const LAS s16x8*)(lds + GM_SA(b, h) + aoff + m * 2048 + k * 1024); } while (0)
; #define GM_LDB(dst, b, h) do { _Pragma("unroll") for (int n = 0; n < 2; ++n) _Pragma("unroll") for (int k = 0; k < 2; ++k) dst[n][k] = *(const LAS s16x8*)(lds + GM_SB(b, h) + boff + n * 2048 + k * 1024); } while (0)
; #define GM_MMA(ai, bj, At, Bt) do { __builtin_amdgcn_s_setprio(1); _Pragma("unroll") for (int m = 0; m < 4; ++m) _Pragma("unroll") for (int n = 0; n < 2; ++n) _Pragma("unroll") for (int k = 0; k < 2; ++k) \
;         acc[ai][bj][m][n] = mma16<BF>(Bt[n][k], At[m][k], acc[ai][bj][m][n]); __builtin_amdgcn_s_setprio(0); } while (0)
; #define GM_WAIT_V(n) asm volatile("s_waitcnt vmcnt(" #n ")" ::: "memory")
; #define GM_WAIT_L(n) asm volatile("s_waitcnt lgkmcnt(" #n ")" ::: "memory")
; #define GM_BAR __builtin_amdgcn_s_barrier()
; template <bool BF, bool GATHER = false, class Epi, class Hook>
; __device__ __forceinline__ void gemm_phase(LAS unsigned char* lds, const Gemm g, const Order& S, const Epi& E, Hook& HK) {
;     ...
;             GM_LDB(B0, 0, 0); GM_LDB(B1, 0, 1); GM_SCHED; GM_LDA(At, 0, 0); GM_STA_H1(GM_SA(1, 1), a1, gA1);
;             GM_WAIT_V(8); GM_WAIT_L(0); GM_BAR; GM_MMA(0, 0, At, B0); GM_MMA(0, 1, At, B1); GM_BAR; GM_SCHED;
;             GM_LDA(At, 0, 1); GM_STAGE(GM_SB(0, 0), b2, voffB); GM_STAGE(GM_SB(0, 1), b2 + hstepB, voffB); GM_STA_H0(GM_SA(0, 0), a2, s0);
;             GM_WAIT_V(8); GM_WAIT_L(0); GM_BAR; GM_MMA(1, 0, At, B0); GM_MMA(1, 1, At, B1); GM_BAR; GM_SCHED;
;             GM_LDB(B0, 1, 0); GM_LDB(B1, 1, 1); GM_SCHED; GM_LDA(At, 1, 0); GM_STA_H1(GM_SA(0, 1), a2, s1);
;             GM_WAIT_V(8); GM_WAIT_L(0); GM_BAR; GM_MMA(0, 0, At, B0); GM_MMA(0, 1, At, B1); GM_BAR; GM_SCHED;
;             GM_LDA(At, 1, 1); GM_STAGE(GM_SB(1, 0), b3, voffB); GM_STAGE(GM_SB(1, 1), b3 + hstepB, voffB); GM_STA_H0(GM_SA(1, 0), a3, s0);
;             GM_WAIT_V(8); GM_WAIT_L(0); GM_BAR; GM_MMA(1, 0, At, B0); GM_MMA(1, 1, At, B1); GM_BAR; GM_SCHED;
.LBB0_1102:
	s_add_u32 s22, s2, 0x100
	s_addc_u32 s23, s3, 0
	s_cmp_eq_u32 s51, 40
	s_cselect_b32 s27, s7, s23
	s_cselect_b32 s26, s6, s22
	s_cselect_b32 s25, s21, s50
	s_cselect_b32 s24, s20, s49
	v_lshl_add_u64 v[216:217], s[2:3], 0, v[138:139]
	s_add_i32 m0, s29, 0xc000
	global_load_lds_dwordx4 v[216:217], off
	v_lshl_add_u64 v[216:217], s[2:3], 0, v[140:141]
	s_add_i32 m0, s29, 0xe000
	s_nop 0
	global_load_lds_dwordx4 v[216:217], off
	ds_read_b128 v[146:149], v153
	ds_read_b128 v[156:159], v153 offset:1024
	ds_read_b128 v[160:163], v153 offset:2048
	ds_read_b128 v[164:167], v153 offset:3072
	ds_read_b128 v[168:171], v154
	ds_read_b128 v[172:175], v154 offset:1024
	ds_read_b128 v[176:179], v154 offset:2048
	ds_read_b128 v[180:183], v154 offset:3072
	ds_read_b128 v[184:187], v155
	ds_read_b128 v[188:191], v155 offset:1024
	ds_read_b128 v[192:195], v155 offset:2048
	ds_read_b128 v[196:199], v155 offset:3072
	ds_read_b128 v[200:203], v155 offset:4096
	ds_read_b128 v[204:207], v155 offset:5120
	ds_read_b128 v[208:211], v155 offset:6144
	ds_read_b128 v[212:215], v155 offset:7168
	s_waitcnt vmcnt(8)
	s_waitcnt lgkmcnt(0)
	s_barrier
	v_mfma_f32_16x16x32_bf16 v[126:129], v[146:149], v[184:187], v[126:129]
	v_mfma_f32_16x16x32_bf16 v[122:125], v[160:163], v[184:187], v[122:125]
	v_mfma_f32_16x16x32_bf16 v[110:113], v[146:149], v[192:195], v[110:113]
	v_mfma_f32_16x16x32_bf16 v[106:109], v[160:163], v[192:195], v[106:109]
	v_mfma_f32_16x16x32_bf16 v[94:97], v[146:149], v[200:203], v[94:97]
	v_mfma_f32_16x16x32_bf16 v[90:93], v[160:163], v[200:203], v[90:93]
	v_mfma_f32_16x16x32_bf16 v[78:81], v[146:149], v[208:211], v[78:81]
	v_mfma_f32_16x16x32_bf16 v[74:77], v[160:163], v[208:211], v[74:77]
	v_mfma_f32_16x16x32_bf16 v[126:129], v[156:159], v[188:191], v[126:129]
	v_mfma_f32_16x16x32_bf16 v[122:125], v[164:167], v[188:191], v[122:125]
	v_mfma_f32_16x16x32_bf16 v[110:113], v[156:159], v[196:199], v[110:113]
	v_mfma_f32_16x16x32_bf16 v[106:109], v[164:167], v[196:199], v[106:109]
	v_mfma_f32_16x16x32_bf16 v[94:97], v[156:159], v[204:207], v[94:97]
	v_mfma_f32_16x16x32_bf16 v[90:93], v[164:167], v[204:207], v[90:93]
	v_mfma_f32_16x16x32_bf16 v[78:81], v[156:159], v[212:215], v[78:81]
	v_mfma_f32_16x16x32_bf16 v[74:77], v[164:167], v[212:215], v[74:77]
	v_mfma_f32_16x16x32_bf16 v[118:121], v[168:171], v[184:187], v[118:121]
	v_mfma_f32_16x16x32_bf16 v[114:117], v[176:179], v[184:187], v[114:117]
	v_mfma_f32_16x16x32_bf16 v[102:105], v[168:171], v[192:195], v[102:105]
	v_mfma_f32_16x16x32_bf16 v[98:101], v[176:179], v[192:195], v[98:101]
	v_mfma_f32_16x16x32_bf16 v[86:89], v[168:171], v[200:203], v[86:89]
	v_mfma_f32_16x16x32_bf16 v[82:85], v[176:179], v[200:203], v[82:85]
	v_mfma_f32_16x16x32_bf16 v[70:73], v[168:171], v[208:211], v[70:73]
	v_mfma_f32_16x16x32_bf16 v[66:69], v[176:179], v[208:211], v[66:69]
	v_mfma_f32_16x16x32_bf16 v[118:121], v[172:175], v[188:191], v[118:121]
	v_mfma_f32_16x16x32_bf16 v[114:117], v[180:183], v[188:191], v[114:117]
	v_mfma_f32_16x16x32_bf16 v[102:105], v[172:175], v[196:199], v[102:105]
	v_mfma_f32_16x16x32_bf16 v[98:101], v[180:183], v[196:199], v[98:101]
	v_mfma_f32_16x16x32_bf16 v[86:89], v[172:175], v[204:207], v[86:89]
	v_mfma_f32_16x16x32_bf16 v[82:85], v[180:183], v[204:207], v[82:85]
	v_mfma_f32_16x16x32_bf16 v[70:73], v[172:175], v[212:215], v[70:73]
	v_mfma_f32_16x16x32_bf16 v[66:69], v[180:183], v[212:215], v[66:69]
	s_barrier
	s_add_i32 s2, s42, s28
	v_lshl_add_u64 v[216:217], s[24:25], 0, v[132:133]
	s_mov_b32 m0, s2
	global_load_lds_dwordx4 v[216:217], off
	s_add_i32 m0, s2, 0x2000
	s_add_u32 s2, s24, 0xb0000
	v_lshl_add_u64 v[218:219], s[24:25], 0, v[136:137]
	s_addc_u32 s3, s25, 0
	s_add_i32 s52, s43, s28
	global_load_lds_dwordx4 v[218:219], off
	v_lshl_add_u64 v[220:221], s[2:3], 0, v[132:133]
	s_mov_b32 m0, s52
	v_lshl_add_u64 v[222:223], s[26:27], 0, v[134:135]
	global_load_lds_dwordx4 v[220:221], off
	v_lshl_add_u64 v[220:221], s[2:3], 0, v[136:137]
	s_add_i32 m0, s52, 0x2000
	s_nop 0
	global_load_lds_dwordx4 v[220:221], off
	v_lshl_add_u64 v[220:221], s[26:27], 0, v[130:131]
	s_mov_b32 m0, s29
	s_nop 0
	global_load_lds_dwordx4 v[220:221], off
	s_mov_b32 m0, s30
	s_nop 0
	global_load_lds_dwordx4 v[222:223], off
	ds_read_b128 v[184:187], v155 offset:16384
	ds_read_b128 v[188:191], v155 offset:17408
	ds_read_b128 v[192:195], v155 offset:18432
	ds_read_b128 v[196:199], v155 offset:19456
	ds_read_b128 v[200:203], v155 offset:20480
	ds_read_b128 v[204:207], v155 offset:21504
	ds_read_b128 v[208:211], v155 offset:22528
	ds_read_b128 v[212:215], v155 offset:23552
	s_waitcnt vmcnt(8)
	s_waitcnt lgkmcnt(0)
	s_barrier
; #define GM_LDA(dst, b, h) do { _Pragma("unroll") for (int m = 0; m < 4; ++m) _Pragma("unroll") for (int k = 0; k < 2; ++k) dst[m][k] = *(const LAS s16x8*)(lds + GM_SA(b, h) + aoff + m * 2048 + k * 1024); } while (0)
; #define GM_LDB(dst, b, h) do { _Pragma("unroll") for (int n = 0; n < 2; ++n) _Pragma("unroll") for (int k = 0; k < 2; ++k) dst[n][k] = *(const LAS s16x8*)(lds + GM_SB(b, h) + boff + n * 2048 + k * 1024); } while (0)
; #define GM_MMA(ai, bj, At, Bt) do { __builtin_amdgcn_s_setprio(1); _Pragma("unroll") for (int m = 0; m < 4; ++m) _Pragma("unroll") for (int n = 0; n < 2; ++n) _Pragma("unroll") for (int k = 0; k < 2; ++k) \
;         acc[ai][bj][m][n] = mma16<BF>(Bt[n][k], At[m][k], acc[ai][bj][m][n]); __builtin_amdgcn_s_setprio(0); } while (0)
; #define GM_WAIT_V(n) asm volatile("s_waitcnt vmcnt(" #n ")" ::: "memory")
; #define GM_WAIT_L(n) asm volatile("s_waitcnt lgkmcnt(" #n ")" ::: "memory")
; #define GM_BAR __builtin_amdgcn_s_barrier()
; #define GM_SCHED __builtin_amdgcn_sched_barrier(0)
; #define GM_STA_H1(buf, p, o1) do { if constexpr (GATHER) GM_STAGE(buf, p, o1); else GM_STAGE(buf, (p) + hstepB, voffA); } while (0)
; template <bool BF, bool GATHER = false, class Epi, class Hook>
; __device__ __forceinline__ void gemm_phase(LAS unsigned char* lds, const Gemm g, const Order& S, const Epi& E, Hook& HK) {
;     ...
;             GM_WAIT_V(8); GM_WAIT_L(0); GM_BAR; GM_MMA(1, 0, At, B0); GM_MMA(1, 1, At, B1); GM_BAR; GM_SCHED;
;             GM_LDB(B0, 1, 0); GM_LDB(B1, 1, 1); GM_SCHED; GM_LDA(At, 1, 0); GM_STA_H1(GM_SA(0, 1), a2, s1);
;             GM_WAIT_V(8); GM_WAIT_L(0); GM_BAR; GM_MMA(0, 0, At, B0); GM_MMA(0, 1, At, B1); GM_BAR; GM_SCHED;
	v_mfma_f32_16x16x32_bf16 v[62:65], v[146:149], v[184:187], v[62:65]
	v_mfma_f32_16x16x32_bf16 v[58:61], v[160:163], v[184:187], v[58:61]
	v_mfma_f32_16x16x32_bf16 v[46:49], v[146:149], v[192:195], v[46:49]
	v_mfma_f32_16x16x32_bf16 v[42:45], v[160:163], v[192:195], v[42:45]
	v_mfma_f32_16x16x32_bf16 v[30:33], v[146:149], v[200:203], v[30:33]
	v_mfma_f32_16x16x32_bf16 v[26:29], v[160:163], v[200:203], v[26:29]
	v_mfma_f32_16x16x32_bf16 v[14:17], v[146:149], v[208:211], v[14:17]
	v_mfma_f32_16x16x32_bf16 v[10:13], v[160:163], v[208:211], v[10:13]
	v_mfma_f32_16x16x32_bf16 v[62:65], v[156:159], v[188:191], v[62:65]
	v_mfma_f32_16x16x32_bf16 v[58:61], v[164:167], v[188:191], v[58:61]
	v_mfma_f32_16x16x32_bf16 v[46:49], v[156:159], v[196:199], v[46:49]
	v_mfma_f32_16x16x32_bf16 v[42:45], v[164:167], v[196:199], v[42:45]
	v_mfma_f32_16x16x32_bf16 v[30:33], v[156:159], v[204:207], v[30:33]
	v_mfma_f32_16x16x32_bf16 v[26:29], v[164:167], v[204:207], v[26:29]
	v_mfma_f32_16x16x32_bf16 v[14:17], v[156:159], v[212:215], v[14:17]
	v_mfma_f32_16x16x32_bf16 v[10:13], v[164:167], v[212:215], v[10:13]
	v_mfma_f32_16x16x32_bf16 v[54:57], v[168:171], v[184:187], v[54:57]
	v_mfma_f32_16x16x32_bf16 v[50:53], v[176:179], v[184:187], v[50:53]
	v_mfma_f32_16x16x32_bf16 v[38:41], v[168:171], v[192:195], v[38:41]
	v_mfma_f32_16x16x32_bf16 v[34:37], v[176:179], v[192:195], v[34:37]
	v_mfma_f32_16x16x32_bf16 v[22:25], v[168:171], v[200:203], v[22:25]
	v_mfma_f32_16x16x32_bf16 v[18:21], v[176:179], v[200:203], v[18:21]
	v_mfma_f32_16x16x32_bf16 v[6:9], v[168:171], v[208:211], v[6:9]
	v_mfma_f32_16x16x32_bf16 v[2:5], v[176:179], v[208:211], v[2:5]
	v_mfma_f32_16x16x32_bf16 v[54:57], v[172:175], v[188:191], v[54:57]
	v_mfma_f32_16x16x32_bf16 v[50:53], v[180:183], v[188:191], v[50:53]
	v_mfma_f32_16x16x32_bf16 v[38:41], v[172:175], v[196:199], v[38:41]
	v_mfma_f32_16x16x32_bf16 v[34:37], v[180:183], v[196:199], v[34:37]
	v_mfma_f32_16x16x32_bf16 v[22:25], v[172:175], v[204:207], v[22:25]
	v_mfma_f32_16x16x32_bf16 v[18:21], v[180:183], v[204:207], v[18:21]
	v_mfma_f32_16x16x32_bf16 v[6:9], v[172:175], v[212:215], v[6:9]
	v_mfma_f32_16x16x32_bf16 v[2:5], v[180:183], v[212:215], v[2:5]
	s_barrier
	s_add_u32 s2, s26, 0xb0000
	s_addc_u32 s3, s27, 0
	s_mov_b32 m0, s31
	v_lshl_add_u64 v[224:225], s[2:3], 0, v[130:131]
	global_load_lds_dwordx4 v[224:225], off
	v_lshl_add_u64 v[224:225], s[2:3], 0, v[134:135]
	s_mov_b32 m0, s33
	s_nop 0
	global_load_lds_dwordx4 v[224:225], off
	s_mov_b32 s53, 0x1c000
	s_mov_b32 s52, 0x18000
	v_add_u32_e32 v244, s52, v150
	v_add_u32_e32 v245, s53, v150
	ds_read_b128 v[146:149], v244
	ds_read_b128 v[156:159], v244 offset:1024
	ds_read_b128 v[160:163], v244 offset:2048
	ds_read_b128 v[164:167], v244 offset:3072
	ds_read_b128 v[168:171], v245
	ds_read_b128 v[172:175], v245 offset:1024
	ds_read_b128 v[176:179], v245 offset:2048
	ds_read_b128 v[180:183], v245 offset:3072
	ds_read_b128 v[184:187], v155 offset:32768
	ds_read_b128 v[188:191], v155 offset:33792
	ds_read_b128 v[192:195], v155 offset:34816
	ds_read_b128 v[196:199], v155 offset:35840
	ds_read_b128 v[200:203], v155 offset:36864
	ds_read_b128 v[204:207], v155 offset:37888
	ds_read_b128 v[208:211], v155 offset:38912
	ds_read_b128 v[212:215], v155 offset:39936
	s_waitcnt vmcnt(8)
	s_waitcnt lgkmcnt(0)
	s_barrier
	v_mfma_f32_16x16x32_bf16 v[126:129], v[146:149], v[184:187], v[126:129]
	v_mfma_f32_16x16x32_bf16 v[122:125], v[160:163], v[184:187], v[122:125]
	v_mfma_f32_16x16x32_bf16 v[110:113], v[146:149], v[192:195], v[110:113]
	v_mfma_f32_16x16x32_bf16 v[106:109], v[160:163], v[192:195], v[106:109]
	v_mfma_f32_16x16x32_bf16 v[94:97], v[146:149], v[200:203], v[94:97]
	v_mfma_f32_16x16x32_bf16 v[90:93], v[160:163], v[200:203], v[90:93]
	v_mfma_f32_16x16x32_bf16 v[78:81], v[146:149], v[208:211], v[78:81]
	v_mfma_f32_16x16x32_bf16 v[74:77], v[160:163], v[208:211], v[74:77]
	v_mfma_f32_16x16x32_bf16 v[126:129], v[156:159], v[188:191], v[126:129]
	v_mfma_f32_16x16x32_bf16 v[122:125], v[164:167], v[188:191], v[122:125]
	v_mfma_f32_16x16x32_bf16 v[110:113], v[156:159], v[196:199], v[110:113]
	v_mfma_f32_16x16x32_bf16 v[106:109], v[164:167], v[196:199], v[106:109]
	v_mfma_f32_16x16x32_bf16 v[94:97], v[156:159], v[204:207], v[94:97]
	v_mfma_f32_16x16x32_bf16 v[90:93], v[164:167], v[204:207], v[90:93]
	v_mfma_f32_16x16x32_bf16 v[78:81], v[156:159], v[212:215], v[78:81]
	v_mfma_f32_16x16x32_bf16 v[74:77], v[164:167], v[212:215], v[74:77]
	v_mfma_f32_16x16x32_bf16 v[118:121], v[168:171], v[184:187], v[118:121]
	v_mfma_f32_16x16x32_bf16 v[114:117], v[176:179], v[184:187], v[114:117]
	v_mfma_f32_16x16x32_bf16 v[102:105], v[168:171], v[192:195], v[102:105]
	v_mfma_f32_16x16x32_bf16 v[98:101], v[176:179], v[192:195], v[98:101]
	v_mfma_f32_16x16x32_bf16 v[86:89], v[168:171], v[200:203], v[86:89]
	v_mfma_f32_16x16x32_bf16 v[82:85], v[176:179], v[200:203], v[82:85]
	v_mfma_f32_16x16x32_bf16 v[70:73], v[168:171], v[208:211], v[70:73]
	v_mfma_f32_16x16x32_bf16 v[66:69], v[176:179], v[208:211], v[66:69]
	v_mfma_f32_16x16x32_bf16 v[118:121], v[172:175], v[188:191], v[118:121]
	v_mfma_f32_16x16x32_bf16 v[114:117], v[180:183], v[188:191], v[114:117]
	v_mfma_f32_16x16x32_bf16 v[102:105], v[172:175], v[196:199], v[102:105]
	v_mfma_f32_16x16x32_bf16 v[98:101], v[180:183], v[196:199], v[98:101]
	v_mfma_f32_16x16x32_bf16 v[86:89], v[172:175], v[204:207], v[86:89]
	v_mfma_f32_16x16x32_bf16 v[82:85], v[180:183], v[204:207], v[82:85]
	v_mfma_f32_16x16x32_bf16 v[70:73], v[172:175], v[212:215], v[70:73]
	v_mfma_f32_16x16x32_bf16 v[66:69], v[180:183], v[212:215], v[66:69]
	s_barrier
; #define GM_STAGE(bufoff, gbase, voff) do { _Pragma("unroll") for (int _i = 0; _i < 2; ++_i) \
;         __builtin_amdgcn_global_load_lds((const unsigned*)((const char*)(gbase) + (voff)[_i]), (LAS unsigned*)(lds + (bufoff) + ldsw + _i * 8192), 16, 0, 0); } while (0)
; #define GM_LDA(dst, b, h) do { _Pragma("unroll") for (int m = 0; m < 4; ++m) _Pragma("unroll") for (int k = 0; k < 2; ++k) dst[m][k] = *(const LAS s16x8*)(lds + GM_SA(b, h) + aoff + m * 2048 + k * 1024); } while (0)
; #define GM_MMA(ai, bj, At, Bt) do { __builtin_amdgcn_s_setprio(1); _Pragma("unroll") for (int m = 0; m < 4; ++m) _Pragma("unroll") for (int n = 0; n < 2; ++n) _Pragma("unroll") for (int k = 0; k < 2; ++k) \
;         acc[ai][bj][m][n] = mma16<BF>(Bt[n][k], At[m][k], acc[ai][bj][m][n]); __builtin_amdgcn_s_setprio(0); } while (0)
; #define GM_WAIT_V(n) asm volatile("s_waitcnt vmcnt(" #n ")" ::: "memory")
; #define GM_WAIT_L(n) asm volatile("s_waitcnt lgkmcnt(" #n ")" ::: "memory")
; #define GM_BAR __builtin_amdgcn_s_barrier()
; #define GM_SCHED __builtin_amdgcn_sched_barrier(0)
; #define GM_STA_H0(buf, p, o0) do { if constexpr (GATHER) GM_STAGE(buf, p, o0); else GM_STAGE(buf, p, voffA); } while (0)
; template <bool BF, bool GATHER = false, class Epi, class Hook>
; __device__ __forceinline__ void gemm_phase(LAS unsigned char* lds, const Gemm g, const Order& S, const Epi& E, Hook& HK) {
;     ...
;             GM_LDA(At, 1, 1); GM_STAGE(GM_SB(1, 0), b3, voffB); GM_STAGE(GM_SB(1, 1), b3 + hstepB, voffB); GM_STA_H0(GM_SA(1, 0), a3, s0);
;             GM_WAIT_V(8); GM_WAIT_L(0); GM_BAR; GM_MMA(1, 0, At, B0); GM_MMA(1, 1, At, B1); GM_BAR; GM_SCHED;
;         }
;         if (wr == 0) GM_BAR;
	s_add_i32 s2, s52, s28
	v_lshl_add_u64 v[216:217], v[216:217], 0, s[12:13]
	s_mov_b32 m0, s2
	global_load_lds_dwordx4 v[216:217], off
	s_add_i32 m0, s2, 0x2000
	s_add_u32 s2, s24, 0xb0080
	v_lshl_add_u64 v[216:217], v[218:219], 0, s[12:13]
	s_addc_u32 s3, s25, 0
	s_add_i32 s24, s53, s28
	global_load_lds_dwordx4 v[216:217], off
	v_lshl_add_u64 v[216:217], s[2:3], 0, v[132:133]
	s_mov_b32 m0, s24
	s_nop 0
	global_load_lds_dwordx4 v[216:217], off
	v_lshl_add_u64 v[216:217], s[2:3], 0, v[136:137]
	s_add_i32 m0, s24, 0x2000
	s_nop 0
	global_load_lds_dwordx4 v[216:217], off
	v_lshl_add_u64 v[216:217], v[220:221], 0, s[12:13]
	s_mov_b32 m0, s36
	s_nop 0
	global_load_lds_dwordx4 v[216:217], off
	v_lshl_add_u64 v[216:217], v[222:223], 0, s[12:13]
	s_mov_b32 m0, s37
	s_nop 0
	global_load_lds_dwordx4 v[216:217], off
	ds_read_b128 v[184:187], v155 offset:49152
	ds_read_b128 v[188:191], v155 offset:50176
	ds_read_b128 v[192:195], v155 offset:51200
	ds_read_b128 v[196:199], v155 offset:52224
	ds_read_b128 v[200:203], v155 offset:53248
	ds_read_b128 v[204:207], v155 offset:54272
	ds_read_b128 v[208:211], v155 offset:55296
	ds_read_b128 v[212:215], v155 offset:56320
	s_waitcnt vmcnt(8)
	s_waitcnt lgkmcnt(0)
	s_barrier
	v_mfma_f32_16x16x32_bf16 v[62:65], v[146:149], v[184:187], v[62:65]
	v_mfma_f32_16x16x32_bf16 v[58:61], v[160:163], v[184:187], v[58:61]
	v_mfma_f32_16x16x32_bf16 v[46:49], v[146:149], v[192:195], v[46:49]
	v_mfma_f32_16x16x32_bf16 v[42:45], v[160:163], v[192:195], v[42:45]
	v_mfma_f32_16x16x32_bf16 v[30:33], v[146:149], v[200:203], v[30:33]
	v_mfma_f32_16x16x32_bf16 v[26:29], v[160:163], v[200:203], v[26:29]
	v_mfma_f32_16x16x32_bf16 v[14:17], v[146:149], v[208:211], v[14:17]
	v_mfma_f32_16x16x32_bf16 v[10:13], v[160:163], v[208:211], v[10:13]
	v_mfma_f32_16x16x32_bf16 v[62:65], v[156:159], v[188:191], v[62:65]
	v_mfma_f32_16x16x32_bf16 v[58:61], v[164:167], v[188:191], v[58:61]
	v_mfma_f32_16x16x32_bf16 v[46:49], v[156:159], v[196:199], v[46:49]
	v_mfma_f32_16x16x32_bf16 v[42:45], v[164:167], v[196:199], v[42:45]
	v_mfma_f32_16x16x32_bf16 v[30:33], v[156:159], v[204:207], v[30:33]
	v_mfma_f32_16x16x32_bf16 v[26:29], v[164:167], v[204:207], v[26:29]
	v_mfma_f32_16x16x32_bf16 v[14:17], v[156:159], v[212:215], v[14:17]
	v_mfma_f32_16x16x32_bf16 v[10:13], v[164:167], v[212:215], v[10:13]
	v_mfma_f32_16x16x32_bf16 v[54:57], v[168:171], v[184:187], v[54:57]
	v_mfma_f32_16x16x32_bf16 v[50:53], v[176:179], v[184:187], v[50:53]
	v_mfma_f32_16x16x32_bf16 v[38:41], v[168:171], v[192:195], v[38:41]
	v_mfma_f32_16x16x32_bf16 v[34:37], v[176:179], v[192:195], v[34:37]
	v_mfma_f32_16x16x32_bf16 v[22:25], v[168:171], v[200:203], v[22:25]
	v_mfma_f32_16x16x32_bf16 v[18:21], v[176:179], v[200:203], v[18:21]
	v_mfma_f32_16x16x32_bf16 v[6:9], v[168:171], v[208:211], v[6:9]
	v_mfma_f32_16x16x32_bf16 v[2:5], v[176:179], v[208:211], v[2:5]
	v_mfma_f32_16x16x32_bf16 v[54:57], v[172:175], v[188:191], v[54:57]
	v_mfma_f32_16x16x32_bf16 v[50:53], v[180:183], v[188:191], v[50:53]
	v_mfma_f32_16x16x32_bf16 v[38:41], v[172:175], v[196:199], v[38:41]
	v_mfma_f32_16x16x32_bf16 v[34:37], v[180:183], v[196:199], v[34:37]
	v_mfma_f32_16x16x32_bf16 v[22:25], v[172:175], v[204:207], v[22:25]
	v_mfma_f32_16x16x32_bf16 v[18:21], v[180:183], v[204:207], v[18:21]
	v_mfma_f32_16x16x32_bf16 v[6:9], v[172:175], v[212:215], v[6:9]
	v_mfma_f32_16x16x32_bf16 v[2:5], v[180:183], v[212:215], v[2:5]
	s_barrier
	s_add_i32 s51, s51, 2
	s_add_u32 s49, s49, 0x100
	s_addc_u32 s50, s50, 0
	s_cmp_gt_u32 s51, 41
	s_mov_b64 s[2:3], s[22:23]
	s_cbranch_scc0 .LBB0_1102
	s_and_b64 vcc, exec, s[14:15]
	s_cbranch_vccz .LBB0_1105
	s_barrier

; #define GM_STAGE(bufoff, gbase, voff) do { _Pragma("unroll") for (int _i = 0; _i < 2; ++_i) \
;         __builtin_amdgcn_global_load_lds((const unsigned*)((const char*)(gbase) + (voff)[_i]), (LAS unsigned*)(lds + (bufoff) + ldsw + _i * 8192), 16, 0, 0); } while (0)
; #define GM_LDA(dst, b, h) do { _Pragma("unroll") for (int m = 0; m < 4; ++m) _Pragma("unroll") for (int k = 0; k < 2; ++k) dst[m][k] = *(const LAS s16x8*)(lds + GM_SA(b, h) + aoff + m * 2048 + k * 1024); } while (0)
; #define GM_LDB(dst, b, h) do { _Pragma("unroll") for (int n = 0; n < 2; ++n) _Pragma("unroll") for (int k = 0; k < 2; ++k) dst[n][k] = *(const LAS s16x8*)(lds + GM_SB(b, h) + boff + n * 2048 + k * 1024); } while (0)
; #define GM_MMA(ai, bj, At, Bt) do { __builtin_amdgcn_s_setprio(1); _Pragma("unroll") for (int m = 0; m < 4; ++m) _Pragma("unroll") for (int n = 0; n < 2; ++n) _Pragma("unroll") for (int k = 0; k < 2; ++k) \
;         acc[ai][bj][m][n] = mma16<BF>(Bt[n][k], At[m][k], acc[ai][bj][m][n]); __builtin_amdgcn_s_setprio(0); } while (0)
; #define GM_WAIT_V(n) asm volatile("s_waitcnt vmcnt(" #n ")" ::: "memory")
; #define GM_WAIT_L(n) asm volatile("s_waitcnt lgkmcnt(" #n ")" ::: "memory")
; template <bool BF, bool GATHER = false, class Epi, class Hook>
; __device__ __forceinline__ void gemm_phase(LAS unsigned char* lds, const Gemm g, const Order& S, const Epi& E, Hook& HK) {
;     ...
;             const bool last = (t == nt - 2);
;             const char* a1 = cA + (size_t)(t + 1) * kstep;
;             const char* a2 = last ? nA : cA + (size_t)(t + 2) * kstep; const char* b2 = last ? nB : cB + (size_t)(t + 2) * kstep;
;             const char* a3 = a2 + kstep; const char* b3 = b2 + kstep;
;             unsigned s0[2], s1[2];
;             if constexpr (GATHER) { s0[0] = last ? nA0[0] : gA0[0]; s0[1] = last ? nA0[1] : gA0[1]; s1[0] = last ? nA1[0] : gA1[0]; s1[1] = last ? nA1[1] : gA1[1]; }
;             GM_LDB(B0, 0, 0); GM_LDB(B1, 0, 1); GM_SCHED; GM_LDA(At, 0, 0); GM_STA_H1(GM_SA(1, 1), a1, gA1);
;             GM_WAIT_V(8); GM_WAIT_L(0); GM_BAR; GM_MMA(0, 0, At, B0); GM_MMA(0, 1, At, B1); GM_BAR; GM_SCHED;
;             GM_LDA(At, 0, 1); GM_STAGE(GM_SB(0, 0), b2, voffB); GM_STAGE(GM_SB(0, 1), b2 + hstepB, voffB); GM_STA_H0(GM_SA(0, 0), a2, s0);
;             GM_WAIT_V(8); GM_WAIT_L(0); GM_BAR; GM_MMA(1, 0, At, B0); GM_MMA(1, 1, At, B1); GM_BAR; GM_SCHED;
.LBB0_1281:
	s_add_u32 s22, s20, 0xfffc0080
	s_addc_u32 s23, s21, -1
	s_cmp_eq_u32 s47, 12
	s_cselect_b32 s25, s3, s23
	s_cselect_b32 s24, s13, s22
	s_cselect_b32 s23, s15, s46
	s_cselect_b32 s22, s44, s45
	v_lshl_add_u64 v[218:219], s[20:21], 0, v[140:141]
	s_add_i32 m0, s30, 0xc000
	global_load_lds_dwordx4 v[218:219], off
	v_lshl_add_u64 v[218:219], s[20:21], 0, v[142:143]
	s_add_i32 m0, s30, 0xe000
	s_nop 0
	global_load_lds_dwordx4 v[218:219], off
	ds_read_b128 v[154:157], v151
	ds_read_b128 v[158:161], v151 offset:1024
	ds_read_b128 v[162:165], v151 offset:2048
	ds_read_b128 v[166:169], v151 offset:3072
	ds_read_b128 v[170:173], v152
	ds_read_b128 v[174:177], v152 offset:1024
	ds_read_b128 v[178:181], v152 offset:2048
	ds_read_b128 v[182:185], v152 offset:3072
	ds_read_b128 v[186:189], v153
	ds_read_b128 v[190:193], v153 offset:1024
	ds_read_b128 v[194:197], v153 offset:2048
	ds_read_b128 v[198:201], v153 offset:3072
	ds_read_b128 v[202:205], v153 offset:4096
	ds_read_b128 v[206:209], v153 offset:5120
	ds_read_b128 v[210:213], v153 offset:6144
	ds_read_b128 v[214:217], v153 offset:7168
	s_waitcnt vmcnt(8)
	s_waitcnt lgkmcnt(0)
	s_barrier
	v_mfma_f32_16x16x32_f16 v[126:129], v[154:157], v[186:189], v[126:129]
	v_mfma_f32_16x16x32_f16 v[118:121], v[162:165], v[186:189], v[118:121]
	v_mfma_f32_16x16x32_f16 v[110:113], v[154:157], v[194:197], v[110:113]
	v_mfma_f32_16x16x32_f16 v[102:105], v[162:165], v[194:197], v[102:105]
	v_mfma_f32_16x16x32_f16 v[94:97], v[154:157], v[202:205], v[94:97]
	v_mfma_f32_16x16x32_f16 v[86:89], v[162:165], v[202:205], v[86:89]
	v_mfma_f32_16x16x32_f16 v[78:81], v[154:157], v[210:213], v[78:81]
	v_mfma_f32_16x16x32_f16 v[70:73], v[162:165], v[210:213], v[70:73]
	v_mfma_f32_16x16x32_f16 v[126:129], v[158:161], v[190:193], v[126:129]
	v_mfma_f32_16x16x32_f16 v[118:121], v[166:169], v[190:193], v[118:121]
	v_mfma_f32_16x16x32_f16 v[110:113], v[158:161], v[198:201], v[110:113]
	v_mfma_f32_16x16x32_f16 v[102:105], v[166:169], v[198:201], v[102:105]
	v_mfma_f32_16x16x32_f16 v[94:97], v[158:161], v[206:209], v[94:97]
	v_mfma_f32_16x16x32_f16 v[86:89], v[166:169], v[206:209], v[86:89]
	v_mfma_f32_16x16x32_f16 v[78:81], v[158:161], v[214:217], v[78:81]
	v_mfma_f32_16x16x32_f16 v[70:73], v[166:169], v[214:217], v[70:73]
	v_mfma_f32_16x16x32_f16 v[122:125], v[170:173], v[186:189], v[122:125]
	v_mfma_f32_16x16x32_f16 v[114:117], v[178:181], v[186:189], v[114:117]
	v_mfma_f32_16x16x32_f16 v[106:109], v[170:173], v[194:197], v[106:109]
	v_mfma_f32_16x16x32_f16 v[98:101], v[178:181], v[194:197], v[98:101]
	v_mfma_f32_16x16x32_f16 v[90:93], v[170:173], v[202:205], v[90:93]
	v_mfma_f32_16x16x32_f16 v[82:85], v[178:181], v[202:205], v[82:85]
	v_mfma_f32_16x16x32_f16 v[74:77], v[170:173], v[210:213], v[74:77]
	v_mfma_f32_16x16x32_f16 v[66:69], v[178:181], v[210:213], v[66:69]
	v_mfma_f32_16x16x32_f16 v[122:125], v[174:177], v[190:193], v[122:125]
	v_mfma_f32_16x16x32_f16 v[114:117], v[182:185], v[190:193], v[114:117]
	v_mfma_f32_16x16x32_f16 v[106:109], v[174:177], v[198:201], v[106:109]
	v_mfma_f32_16x16x32_f16 v[98:101], v[182:185], v[198:201], v[98:101]
	v_mfma_f32_16x16x32_f16 v[90:93], v[174:177], v[206:209], v[90:93]
	v_mfma_f32_16x16x32_f16 v[82:85], v[182:185], v[206:209], v[82:85]
	v_mfma_f32_16x16x32_f16 v[74:77], v[174:177], v[214:217], v[74:77]
	v_mfma_f32_16x16x32_f16 v[66:69], v[182:185], v[214:217], v[66:69]
	s_barrier
	s_add_i32 s48, s40, s28
	v_lshl_add_u64 v[218:219], s[22:23], 0, v[134:135]
	s_mov_b32 m0, s48
	global_load_lds_dwordx4 v[218:219], off
	s_add_i32 m0, s48, 0x2000
	s_add_u32 s48, s22, 0x40000
	v_lshl_add_u64 v[220:221], s[22:23], 0, v[130:131]
	s_addc_u32 s49, s23, 0
	s_add_i32 s50, s41, s28
	global_load_lds_dwordx4 v[220:221], off
	v_lshl_add_u64 v[222:223], s[48:49], 0, v[134:135]
	s_mov_b32 m0, s50
	v_lshl_add_u64 v[224:225], s[24:25], 0, v[132:133]
	global_load_lds_dwordx4 v[222:223], off
	v_lshl_add_u64 v[222:223], s[48:49], 0, v[130:131]
	s_add_i32 m0, s50, 0x2000
	s_nop 0
	global_load_lds_dwordx4 v[222:223], off
	v_lshl_add_u64 v[222:223], s[24:25], 0, v[136:137]
	s_mov_b32 m0, s30
	s_nop 0
	global_load_lds_dwordx4 v[222:223], off
	s_mov_b32 m0, s31
	s_nop 0
	global_load_lds_dwordx4 v[224:225], off
	ds_read_b128 v[186:189], v153 offset:16384
	ds_read_b128 v[190:193], v153 offset:17408
	ds_read_b128 v[194:197], v153 offset:18432
	ds_read_b128 v[198:201], v153 offset:19456
	ds_read_b128 v[202:205], v153 offset:20480
	ds_read_b128 v[206:209], v153 offset:21504
	ds_read_b128 v[210:213], v153 offset:22528
	ds_read_b128 v[214:217], v153 offset:23552
	s_waitcnt vmcnt(8)
	s_waitcnt lgkmcnt(0)
	s_barrier
; #define GM_LDA(dst, b, h) do { _Pragma("unroll") for (int m = 0; m < 4; ++m) _Pragma("unroll") for (int k = 0; k < 2; ++k) dst[m][k] = *(const LAS s16x8*)(lds + GM_SA(b, h) + aoff + m * 2048 + k * 1024); } while (0)
; #define GM_LDB(dst, b, h) do { _Pragma("unroll") for (int n = 0; n < 2; ++n) _Pragma("unroll") for (int k = 0; k < 2; ++k) dst[n][k] = *(const LAS s16x8*)(lds + GM_SB(b, h) + boff + n * 2048 + k * 1024); } while (0)
; #define GM_MMA(ai, bj, At, Bt) do { __builtin_amdgcn_s_setprio(1); _Pragma("unroll") for (int m = 0; m < 4; ++m) _Pragma("unroll") for (int n = 0; n < 2; ++n) _Pragma("unroll") for (int k = 0; k < 2; ++k) \
;         acc[ai][bj][m][n] = mma16<BF>(Bt[n][k], At[m][k], acc[ai][bj][m][n]); __builtin_amdgcn_s_setprio(0); } while (0)
; #define GM_WAIT_V(n) asm volatile("s_waitcnt vmcnt(" #n ")" ::: "memory")
; #define GM_WAIT_L(n) asm volatile("s_waitcnt lgkmcnt(" #n ")" ::: "memory")
; #define GM_BAR __builtin_amdgcn_s_barrier()
; #define GM_SCHED __builtin_amdgcn_sched_barrier(0)
; #define GM_STA_H1(buf, p, o1) do { if constexpr (GATHER) GM_STAGE(buf, p, o1); else GM_STAGE(buf, (p) + hstepB, voffA); } while (0)
; template <bool BF, bool GATHER = false, class Epi, class Hook>
; __device__ __forceinline__ void gemm_phase(LAS unsigned char* lds, const Gemm g, const Order& S, const Epi& E, Hook& HK) {
;     ...
;             GM_WAIT_V(8); GM_WAIT_L(0); GM_BAR; GM_MMA(1, 0, At, B0); GM_MMA(1, 1, At, B1); GM_BAR; GM_SCHED;
;             GM_LDB(B0, 1, 0); GM_LDB(B1, 1, 1); GM_SCHED; GM_LDA(At, 1, 0); GM_STA_H1(GM_SA(0, 1), a2, s1);
;             GM_WAIT_V(8); GM_WAIT_L(0); GM_BAR; GM_MMA(0, 0, At, B0); GM_MMA(0, 1, At, B1); GM_BAR; GM_SCHED;
	v_mfma_f32_16x16x32_f16 v[62:65], v[154:157], v[186:189], v[62:65]
	v_mfma_f32_16x16x32_f16 v[54:57], v[162:165], v[186:189], v[54:57]
	v_mfma_f32_16x16x32_f16 v[46:49], v[154:157], v[194:197], v[46:49]
	v_mfma_f32_16x16x32_f16 v[38:41], v[162:165], v[194:197], v[38:41]
	v_mfma_f32_16x16x32_f16 v[30:33], v[154:157], v[202:205], v[30:33]
	v_mfma_f32_16x16x32_f16 v[22:25], v[162:165], v[202:205], v[22:25]
	v_mfma_f32_16x16x32_f16 v[14:17], v[154:157], v[210:213], v[14:17]
	v_mfma_f32_16x16x32_f16 v[6:9], v[162:165], v[210:213], v[6:9]
	v_mfma_f32_16x16x32_f16 v[62:65], v[158:161], v[190:193], v[62:65]
	v_mfma_f32_16x16x32_f16 v[54:57], v[166:169], v[190:193], v[54:57]
	v_mfma_f32_16x16x32_f16 v[46:49], v[158:161], v[198:201], v[46:49]
	v_mfma_f32_16x16x32_f16 v[38:41], v[166:169], v[198:201], v[38:41]
	v_mfma_f32_16x16x32_f16 v[30:33], v[158:161], v[206:209], v[30:33]
	v_mfma_f32_16x16x32_f16 v[22:25], v[166:169], v[206:209], v[22:25]
	v_mfma_f32_16x16x32_f16 v[14:17], v[158:161], v[214:217], v[14:17]
	v_mfma_f32_16x16x32_f16 v[6:9], v[166:169], v[214:217], v[6:9]
	v_mfma_f32_16x16x32_f16 v[58:61], v[170:173], v[186:189], v[58:61]
	v_mfma_f32_16x16x32_f16 v[50:53], v[178:181], v[186:189], v[50:53]
	v_mfma_f32_16x16x32_f16 v[42:45], v[170:173], v[194:197], v[42:45]
	v_mfma_f32_16x16x32_f16 v[34:37], v[178:181], v[194:197], v[34:37]
	v_mfma_f32_16x16x32_f16 v[26:29], v[170:173], v[202:205], v[26:29]
	v_mfma_f32_16x16x32_f16 v[18:21], v[178:181], v[202:205], v[18:21]
	v_mfma_f32_16x16x32_f16 v[10:13], v[170:173], v[210:213], v[10:13]
	v_mfma_f32_16x16x32_f16 v[2:5], v[178:181], v[210:213], v[2:5]
	v_mfma_f32_16x16x32_f16 v[58:61], v[174:177], v[190:193], v[58:61]
	v_mfma_f32_16x16x32_f16 v[50:53], v[182:185], v[190:193], v[50:53]
	v_mfma_f32_16x16x32_f16 v[42:45], v[174:177], v[198:201], v[42:45]
	v_mfma_f32_16x16x32_f16 v[34:37], v[182:185], v[198:201], v[34:37]
	v_mfma_f32_16x16x32_f16 v[26:29], v[174:177], v[206:209], v[26:29]
	v_mfma_f32_16x16x32_f16 v[18:21], v[182:185], v[206:209], v[18:21]
	v_mfma_f32_16x16x32_f16 v[10:13], v[174:177], v[214:217], v[10:13]
	v_mfma_f32_16x16x32_f16 v[2:5], v[182:185], v[214:217], v[2:5]
	s_barrier
	s_add_u32 s24, s24, 0x40000
	s_addc_u32 s25, s25, 0
	s_mov_b32 m0, s33
	v_lshl_add_u64 v[226:227], s[24:25], 0, v[136:137]
	global_load_lds_dwordx4 v[226:227], off
	v_lshl_add_u64 v[226:227], s[24:25], 0, v[132:133]
	s_mov_b32 m0, s34
	s_nop 0
	global_load_lds_dwordx4 v[226:227], off
	s_mov_b32 s49, 0x1c000
	s_mov_b32 s48, 0x18000
	v_add_u32_e32 v244, s48, v148
	ds_read_b128 v[154:157], v244
	ds_read_b128 v[158:161], v244 offset:1024
	ds_read_b128 v[162:165], v244 offset:2048
	ds_read_b128 v[166:169], v244 offset:3072
	v_add_u32_e32 v244, s49, v148
	ds_read_b128 v[170:173], v244
	ds_read_b128 v[174:177], v244 offset:1024
	ds_read_b128 v[178:181], v244 offset:2048
	ds_read_b128 v[182:185], v244 offset:3072
	ds_read_b128 v[186:189], v153 offset:32768
	ds_read_b128 v[190:193], v153 offset:33792
	ds_read_b128 v[194:197], v153 offset:34816
	ds_read_b128 v[198:201], v153 offset:35840
	ds_read_b128 v[202:205], v153 offset:36864
	ds_read_b128 v[206:209], v153 offset:37888
	ds_read_b128 v[210:213], v153 offset:38912
	ds_read_b128 v[214:217], v153 offset:39936
	s_waitcnt vmcnt(8)
	s_waitcnt lgkmcnt(0)
	s_barrier
	v_mfma_f32_16x16x32_f16 v[126:129], v[154:157], v[186:189], v[126:129]
	v_mfma_f32_16x16x32_f16 v[118:121], v[162:165], v[186:189], v[118:121]
	v_mfma_f32_16x16x32_f16 v[110:113], v[154:157], v[194:197], v[110:113]
	v_mfma_f32_16x16x32_f16 v[102:105], v[162:165], v[194:197], v[102:105]
	v_mfma_f32_16x16x32_f16 v[94:97], v[154:157], v[202:205], v[94:97]
	v_mfma_f32_16x16x32_f16 v[86:89], v[162:165], v[202:205], v[86:89]
	v_mfma_f32_16x16x32_f16 v[78:81], v[154:157], v[210:213], v[78:81]
	v_mfma_f32_16x16x32_f16 v[70:73], v[162:165], v[210:213], v[70:73]
	v_mfma_f32_16x16x32_f16 v[126:129], v[158:161], v[190:193], v[126:129]
	v_mfma_f32_16x16x32_f16 v[118:121], v[166:169], v[190:193], v[118:121]
	v_mfma_f32_16x16x32_f16 v[110:113], v[158:161], v[198:201], v[110:113]
	v_mfma_f32_16x16x32_f16 v[102:105], v[166:169], v[198:201], v[102:105]
	v_mfma_f32_16x16x32_f16 v[94:97], v[158:161], v[206:209], v[94:97]
	v_mfma_f32_16x16x32_f16 v[86:89], v[166:169], v[206:209], v[86:89]
	v_mfma_f32_16x16x32_f16 v[78:81], v[158:161], v[214:217], v[78:81]
	v_mfma_f32_16x16x32_f16 v[70:73], v[166:169], v[214:217], v[70:73]
	v_mfma_f32_16x16x32_f16 v[122:125], v[170:173], v[186:189], v[122:125]
	v_mfma_f32_16x16x32_f16 v[114:117], v[178:181], v[186:189], v[114:117]
	v_mfma_f32_16x16x32_f16 v[106:109], v[170:173], v[194:197], v[106:109]
	v_mfma_f32_16x16x32_f16 v[98:101], v[178:181], v[194:197], v[98:101]
	v_mfma_f32_16x16x32_f16 v[90:93], v[170:173], v[202:205], v[90:93]
	v_mfma_f32_16x16x32_f16 v[82:85], v[178:181], v[202:205], v[82:85]
	v_mfma_f32_16x16x32_f16 v[74:77], v[170:173], v[210:213], v[74:77]
	v_mfma_f32_16x16x32_f16 v[66:69], v[178:181], v[210:213], v[66:69]
	v_mfma_f32_16x16x32_f16 v[122:125], v[174:177], v[190:193], v[122:125]
	v_mfma_f32_16x16x32_f16 v[114:117], v[182:185], v[190:193], v[114:117]
	v_mfma_f32_16x16x32_f16 v[106:109], v[174:177], v[198:201], v[106:109]
	v_mfma_f32_16x16x32_f16 v[98:101], v[182:185], v[198:201], v[98:101]
	v_mfma_f32_16x16x32_f16 v[90:93], v[174:177], v[206:209], v[90:93]
	v_mfma_f32_16x16x32_f16 v[82:85], v[182:185], v[206:209], v[82:85]
	v_mfma_f32_16x16x32_f16 v[74:77], v[174:177], v[214:217], v[74:77]
	v_mfma_f32_16x16x32_f16 v[66:69], v[182:185], v[214:217], v[66:69]
	s_barrier
; #define GM_STAGE(bufoff, gbase, voff) do { _Pragma("unroll") for (int _i = 0; _i < 2; ++_i) \
;         __builtin_amdgcn_global_load_lds((const unsigned*)((const char*)(gbase) + (voff)[_i]), (LAS unsigned*)(lds + (bufoff) + ldsw + _i * 8192), 16, 0, 0); } while (0)
; #define GM_LDA(dst, b, h) do { _Pragma("unroll") for (int m = 0; m < 4; ++m) _Pragma("unroll") for (int k = 0; k < 2; ++k) dst[m][k] = *(const LAS s16x8*)(lds + GM_SA(b, h) + aoff + m * 2048 + k * 1024); } while (0)
; #define GM_MMA(ai, bj, At, Bt) do { __builtin_amdgcn_s_setprio(1); _Pragma("unroll") for (int m = 0; m < 4; ++m) _Pragma("unroll") for (int n = 0; n < 2; ++n) _Pragma("unroll") for (int k = 0; k < 2; ++k) \
;         acc[ai][bj][m][n] = mma16<BF>(Bt[n][k], At[m][k], acc[ai][bj][m][n]); __builtin_amdgcn_s_setprio(0); } while (0)
; #define GM_WAIT_V(n) asm volatile("s_waitcnt vmcnt(" #n ")" ::: "memory")
; #define GM_WAIT_L(n) asm volatile("s_waitcnt lgkmcnt(" #n ")" ::: "memory")
; #define GM_BAR __builtin_amdgcn_s_barrier()
; #define GM_SCHED __builtin_amdgcn_sched_barrier(0)
; #define GM_STA_H0(buf, p, o0) do { if constexpr (GATHER) GM_STAGE(buf, p, o0); else GM_STAGE(buf, p, voffA); } while (0)
;     __device__ __forceinline__ void operator()(const Acc& acc, const Unit& u, int wr, int wc, int fr, int fq) const {
;         const int row0 = u.pm * BM + wr * 64 + fr;
;         if (u.pn < 8) {
; template <bool BF, bool GATHER = false, class Epi, class Hook>
; __device__ __forceinline__ void gemm_phase(LAS unsigned char* lds, const Gemm g, const Order& S, const Epi& E, Hook& HK) {
;     ...
;             GM_LDA(At, 1, 1); GM_STAGE(GM_SB(1, 0), b3, voffB); GM_STAGE(GM_SB(1, 1), b3 + hstepB, voffB); GM_STA_H0(GM_SA(1, 0), a3, s0);
;             GM_WAIT_V(8); GM_WAIT_L(0); GM_BAR; GM_MMA(1, 0, At, B0); GM_MMA(1, 1, At, B1); GM_BAR; GM_SCHED;
;         }
;         if (wr == 0) GM_BAR;
	s_add_i32 s24, s48, s28
	v_lshl_add_u64 v[218:219], v[218:219], 0, s[8:9]
	s_mov_b32 m0, s24
	global_load_lds_dwordx4 v[218:219], off
	s_add_i32 m0, s24, 0x2000
	s_add_u32 s22, s22, 0x40080
	v_lshl_add_u64 v[218:219], v[220:221], 0, s[8:9]
	s_addc_u32 s23, s23, 0
	s_add_i32 s24, s49, s28
	global_load_lds_dwordx4 v[218:219], off
	v_lshl_add_u64 v[218:219], s[22:23], 0, v[134:135]
	s_mov_b32 m0, s24
	s_nop 0
	global_load_lds_dwordx4 v[218:219], off
	v_lshl_add_u64 v[218:219], s[22:23], 0, v[130:131]
	s_add_i32 m0, s24, 0x2000
	s_nop 0
	global_load_lds_dwordx4 v[218:219], off
	v_lshl_add_u64 v[218:219], v[222:223], 0, s[8:9]
	s_mov_b32 m0, s37
	s_nop 0
	global_load_lds_dwordx4 v[218:219], off
	v_lshl_add_u64 v[218:219], v[224:225], 0, s[8:9]
	s_mov_b32 m0, s38
	s_nop 0
	global_load_lds_dwordx4 v[218:219], off
	ds_read_b128 v[186:189], v153 offset:49152
	ds_read_b128 v[190:193], v153 offset:50176
	ds_read_b128 v[194:197], v153 offset:51200
	ds_read_b128 v[198:201], v153 offset:52224
	ds_read_b128 v[202:205], v153 offset:53248
	ds_read_b128 v[206:209], v153 offset:54272
	ds_read_b128 v[210:213], v153 offset:55296
	ds_read_b128 v[214:217], v153 offset:56320
	s_waitcnt vmcnt(8)
	s_waitcnt lgkmcnt(0)
	s_barrier
	v_mfma_f32_16x16x32_f16 v[62:65], v[154:157], v[186:189], v[62:65]
	v_mfma_f32_16x16x32_f16 v[54:57], v[162:165], v[186:189], v[54:57]
	v_mfma_f32_16x16x32_f16 v[46:49], v[154:157], v[194:197], v[46:49]
	v_mfma_f32_16x16x32_f16 v[38:41], v[162:165], v[194:197], v[38:41]
	v_mfma_f32_16x16x32_f16 v[30:33], v[154:157], v[202:205], v[30:33]
	v_mfma_f32_16x16x32_f16 v[22:25], v[162:165], v[202:205], v[22:25]
	v_mfma_f32_16x16x32_f16 v[14:17], v[154:157], v[210:213], v[14:17]
	v_mfma_f32_16x16x32_f16 v[6:9], v[162:165], v[210:213], v[6:9]
	v_mfma_f32_16x16x32_f16 v[62:65], v[158:161], v[190:193], v[62:65]
	v_mfma_f32_16x16x32_f16 v[54:57], v[166:169], v[190:193], v[54:57]
	v_mfma_f32_16x16x32_f16 v[46:49], v[158:161], v[198:201], v[46:49]
	v_mfma_f32_16x16x32_f16 v[38:41], v[166:169], v[198:201], v[38:41]
	v_mfma_f32_16x16x32_f16 v[30:33], v[158:161], v[206:209], v[30:33]
	v_mfma_f32_16x16x32_f16 v[22:25], v[166:169], v[206:209], v[22:25]
	v_mfma_f32_16x16x32_f16 v[14:17], v[158:161], v[214:217], v[14:17]
	v_mfma_f32_16x16x32_f16 v[6:9], v[166:169], v[214:217], v[6:9]
	v_mfma_f32_16x16x32_f16 v[58:61], v[170:173], v[186:189], v[58:61]
	v_mfma_f32_16x16x32_f16 v[50:53], v[178:181], v[186:189], v[50:53]
	v_mfma_f32_16x16x32_f16 v[42:45], v[170:173], v[194:197], v[42:45]
	v_mfma_f32_16x16x32_f16 v[34:37], v[178:181], v[194:197], v[34:37]
	v_mfma_f32_16x16x32_f16 v[26:29], v[170:173], v[202:205], v[26:29]
	v_mfma_f32_16x16x32_f16 v[18:21], v[178:181], v[202:205], v[18:21]
	v_mfma_f32_16x16x32_f16 v[10:13], v[170:173], v[210:213], v[10:13]
	v_mfma_f32_16x16x32_f16 v[2:5], v[178:181], v[210:213], v[2:5]
	v_mfma_f32_16x16x32_f16 v[58:61], v[174:177], v[190:193], v[58:61]
	v_mfma_f32_16x16x32_f16 v[50:53], v[182:185], v[190:193], v[50:53]
	v_mfma_f32_16x16x32_f16 v[42:45], v[174:177], v[198:201], v[42:45]
	v_mfma_f32_16x16x32_f16 v[34:37], v[182:185], v[198:201], v[34:37]
	v_mfma_f32_16x16x32_f16 v[26:29], v[174:177], v[206:209], v[26:29]
	v_mfma_f32_16x16x32_f16 v[18:21], v[182:185], v[206:209], v[18:21]
	v_mfma_f32_16x16x32_f16 v[10:13], v[174:177], v[214:217], v[10:13]
	v_mfma_f32_16x16x32_f16 v[2:5], v[182:185], v[214:217], v[2:5]
	s_barrier
	s_add_i32 s47, s47, 2
	s_add_u32 s20, s20, 0x100
	s_addc_u32 s21, s21, 0
	s_add_u32 s45, s45, 0x100
	s_addc_u32 s46, s46, 0
	s_cmp_gt_u32 s47, 13
	s_cbranch_scc0 .LBB0_1281
	s_and_b64 vcc, exec, s[10:11]
	s_cbranch_vccnz .LBB0_1286
	v_lshl_add_u32 v154, s2, 8, v1
	s_cmp_gt_i32 s43, 7
	s_mov_b64 s[2:3], -1
	s_cbranch_scc1 .LBB0_1287

; #define GM_STAGE(bufoff, gbase, voff) do { _Pragma("unroll") for (int _i = 0; _i < 2; ++_i) \
;         __builtin_amdgcn_global_load_lds((const unsigned*)((const char*)(gbase) + (voff)[_i]), (LAS unsigned*)(lds + (bufoff) + ldsw + _i * 8192), 16, 0, 0); } while (0)
; #define GM_LDA(dst, b, h) do { _Pragma("unroll") for (int m = 0; m < 4; ++m) _Pragma("unroll") for (int k = 0; k < 2; ++k) dst[m][k] = *(const LAS s16x8*)(lds + GM_SA(b, h) + aoff + m * 2048 + k * 1024); } while (0)
; #define GM_LDB(dst, b, h) do { _Pragma("unroll") for (int n = 0; n < 2; ++n) _Pragma("unroll") for (int k = 0; k < 2; ++k) dst[n][k] = *(const LAS s16x8*)(lds + GM_SB(b, h) + boff + n * 2048 + k * 1024); } while (0)
; #define GM_MMA(ai, bj, At, Bt) do { __builtin_amdgcn_s_setprio(1); _Pragma("unroll") for (int m = 0; m < 4; ++m) _Pragma("unroll") for (int n = 0; n < 2; ++n) _Pragma("unroll") for (int k = 0; k < 2; ++k) \
;         acc[ai][bj][m][n] = mma16<BF>(Bt[n][k], At[m][k], acc[ai][bj][m][n]); __builtin_amdgcn_s_setprio(0); } while (0)
; #define GM_WAIT_V(n) asm volatile("s_waitcnt vmcnt(" #n ")" ::: "memory")
; #define GM_WAIT_L(n) asm volatile("s_waitcnt lgkmcnt(" #n ")" ::: "memory")
; template <bool BF, bool GATHER = false, class Epi, class Hook>
; __device__ __forceinline__ void gemm_phase(LAS unsigned char* lds, const Gemm g, const Order& S, const Epi& E, Hook& HK) {
;     ...
;             const bool last = (t == nt - 2);
;             const char* a1 = cA + (size_t)(t + 1) * kstep;
;             const char* a2 = last ? nA : cA + (size_t)(t + 2) * kstep; const char* b2 = last ? nB : cB + (size_t)(t + 2) * kstep;
;             const char* a3 = a2 + kstep; const char* b3 = b2 + kstep;
;             unsigned s0[2], s1[2];
;             if constexpr (GATHER) { s0[0] = last ? nA0[0] : gA0[0]; s0[1] = last ? nA0[1] : gA0[1]; s1[0] = last ? nA1[0] : gA1[0]; s1[1] = last ? nA1[1] : gA1[1]; }
;             GM_LDB(B0, 0, 0); GM_LDB(B1, 0, 1); GM_SCHED; GM_LDA(At, 0, 0); GM_STA_H1(GM_SA(1, 1), a1, gA1);
;             GM_WAIT_V(8); GM_WAIT_L(0); GM_BAR; GM_MMA(0, 0, At, B0); GM_MMA(0, 1, At, B1); GM_BAR; GM_SCHED;
;             GM_LDA(At, 0, 1); GM_STAGE(GM_SB(0, 0), b2, voffB); GM_STAGE(GM_SB(0, 1), b2 + hstepB, voffB); GM_STA_H0(GM_SA(0, 0), a2, s0);
;             GM_WAIT_V(8); GM_WAIT_L(0); GM_BAR; GM_MMA(1, 0, At, B0); GM_MMA(1, 1, At, B1); GM_BAR; GM_SCHED;
.LBB0_1480:
	s_add_u32 s24, s22, 0xfffc0080
	s_addc_u32 s25, s23, -1
	s_cmp_eq_u32 s49, 12
	s_cselect_b32 s27, s15, s25
	s_cselect_b32 s26, s45, s24
	s_cselect_b32 s25, s17, s48
	s_cselect_b32 s24, s46, s47
	v_lshl_add_u64 v[216:217], s[22:23], 0, v[154:155]
	s_add_i32 m0, s33, 0xc000
	global_load_lds_dwordx4 v[216:217], off
	v_lshl_add_u64 v[216:217], s[22:23], 0, v[156:157]
	s_add_i32 m0, s33, 0xe000
	s_nop 0
	global_load_lds_dwordx4 v[216:217], off
	ds_read_b128 v[122:125], v168
	ds_read_b128 v[126:129], v168 offset:1024
	ds_read_b128 v[130:133], v168 offset:2048
	ds_read_b128 v[134:137], v168 offset:3072
	ds_read_b128 v[162:165], v169
	ds_read_b128 v[172:175], v169 offset:1024
	ds_read_b128 v[176:179], v169 offset:2048
	ds_read_b128 v[180:183], v169 offset:3072
	ds_read_b128 v[184:187], v170
	ds_read_b128 v[188:191], v170 offset:1024
	ds_read_b128 v[192:195], v170 offset:2048
	ds_read_b128 v[196:199], v170 offset:3072
	ds_read_b128 v[200:203], v170 offset:4096
	ds_read_b128 v[204:207], v170 offset:5120
	ds_read_b128 v[208:211], v170 offset:6144
	ds_read_b128 v[212:215], v170 offset:7168
	s_waitcnt vmcnt(8)
	s_waitcnt lgkmcnt(0)
	s_barrier
	v_mfma_f32_16x16x32_f16 v[142:145], v[122:125], v[184:187], v[142:145]
	v_mfma_f32_16x16x32_f16 v[138:141], v[130:133], v[184:187], v[138:141]
	v_mfma_f32_16x16x32_f16 v[110:113], v[122:125], v[192:195], v[110:113]
	v_mfma_f32_16x16x32_f16 v[106:109], v[130:133], v[192:195], v[106:109]
	v_mfma_f32_16x16x32_f16 v[94:97], v[122:125], v[200:203], v[94:97]
	v_mfma_f32_16x16x32_f16 v[90:93], v[130:133], v[200:203], v[90:93]
	v_mfma_f32_16x16x32_f16 v[78:81], v[122:125], v[208:211], v[78:81]
	v_mfma_f32_16x16x32_f16 v[74:77], v[130:133], v[208:211], v[74:77]
	v_mfma_f32_16x16x32_f16 v[142:145], v[126:129], v[188:191], v[142:145]
	v_mfma_f32_16x16x32_f16 v[138:141], v[134:137], v[188:191], v[138:141]
	v_mfma_f32_16x16x32_f16 v[110:113], v[126:129], v[196:199], v[110:113]
	v_mfma_f32_16x16x32_f16 v[106:109], v[134:137], v[196:199], v[106:109]
	v_mfma_f32_16x16x32_f16 v[94:97], v[126:129], v[204:207], v[94:97]
	v_mfma_f32_16x16x32_f16 v[90:93], v[134:137], v[204:207], v[90:93]
	v_mfma_f32_16x16x32_f16 v[78:81], v[126:129], v[212:215], v[78:81]
	v_mfma_f32_16x16x32_f16 v[74:77], v[134:137], v[212:215], v[74:77]
	v_mfma_f32_16x16x32_f16 v[118:121], v[162:165], v[184:187], v[118:121]
	v_mfma_f32_16x16x32_f16 v[114:117], v[176:179], v[184:187], v[114:117]
	v_mfma_f32_16x16x32_f16 v[102:105], v[162:165], v[192:195], v[102:105]
	v_mfma_f32_16x16x32_f16 v[98:101], v[176:179], v[192:195], v[98:101]
	v_mfma_f32_16x16x32_f16 v[86:89], v[162:165], v[200:203], v[86:89]
	v_mfma_f32_16x16x32_f16 v[82:85], v[176:179], v[200:203], v[82:85]
	v_mfma_f32_16x16x32_f16 v[70:73], v[162:165], v[208:211], v[70:73]
	v_mfma_f32_16x16x32_f16 v[66:69], v[176:179], v[208:211], v[66:69]
	v_mfma_f32_16x16x32_f16 v[118:121], v[172:175], v[188:191], v[118:121]
	v_mfma_f32_16x16x32_f16 v[114:117], v[180:183], v[188:191], v[114:117]
	v_mfma_f32_16x16x32_f16 v[102:105], v[172:175], v[196:199], v[102:105]
	v_mfma_f32_16x16x32_f16 v[98:101], v[180:183], v[196:199], v[98:101]
	v_mfma_f32_16x16x32_f16 v[86:89], v[172:175], v[204:207], v[86:89]
	v_mfma_f32_16x16x32_f16 v[82:85], v[180:183], v[204:207], v[82:85]
	v_mfma_f32_16x16x32_f16 v[70:73], v[172:175], v[212:215], v[70:73]
	v_mfma_f32_16x16x32_f16 v[66:69], v[180:183], v[212:215], v[66:69]
	s_barrier
	s_add_i32 s50, s43, s31
	v_lshl_add_u64 v[216:217], s[24:25], 0, v[148:149]
	s_mov_b32 m0, s50
	global_load_lds_dwordx4 v[216:217], off
	s_add_i32 m0, s50, 0x2000
	s_add_u32 s50, s24, 0x40000
	v_lshl_add_u64 v[218:219], s[24:25], 0, v[152:153]
	s_addc_u32 s51, s25, 0
	s_add_i32 s52, s44, s31
	global_load_lds_dwordx4 v[218:219], off
	v_lshl_add_u64 v[220:221], s[50:51], 0, v[148:149]
	s_mov_b32 m0, s52
	v_lshl_add_u64 v[222:223], s[26:27], 0, v[150:151]
	global_load_lds_dwordx4 v[220:221], off
	v_lshl_add_u64 v[220:221], s[50:51], 0, v[152:153]
	s_add_i32 m0, s52, 0x2000
	s_nop 0
	global_load_lds_dwordx4 v[220:221], off
	v_lshl_add_u64 v[220:221], s[26:27], 0, v[146:147]
	s_mov_b32 m0, s33
	s_nop 0
	global_load_lds_dwordx4 v[220:221], off
	s_mov_b32 m0, s34
	s_nop 0
	global_load_lds_dwordx4 v[222:223], off
	ds_read_b128 v[184:187], v170 offset:16384
	ds_read_b128 v[188:191], v170 offset:17408
	ds_read_b128 v[192:195], v170 offset:18432
	ds_read_b128 v[196:199], v170 offset:19456
	ds_read_b128 v[200:203], v170 offset:20480
	ds_read_b128 v[204:207], v170 offset:21504
	ds_read_b128 v[208:211], v170 offset:22528
	ds_read_b128 v[212:215], v170 offset:23552
	s_waitcnt vmcnt(8)
	s_waitcnt lgkmcnt(0)
	s_barrier
; #define GM_LDA(dst, b, h) do { _Pragma("unroll") for (int m = 0; m < 4; ++m) _Pragma("unroll") for (int k = 0; k < 2; ++k) dst[m][k] = *(const LAS s16x8*)(lds + GM_SA(b, h) + aoff + m * 2048 + k * 1024); } while (0)
; #define GM_LDB(dst, b, h) do { _Pragma("unroll") for (int n = 0; n < 2; ++n) _Pragma("unroll") for (int k = 0; k < 2; ++k) dst[n][k] = *(const LAS s16x8*)(lds + GM_SB(b, h) + boff + n * 2048 + k * 1024); } while (0)
; #define GM_MMA(ai, bj, At, Bt) do { __builtin_amdgcn_s_setprio(1); _Pragma("unroll") for (int m = 0; m < 4; ++m) _Pragma("unroll") for (int n = 0; n < 2; ++n) _Pragma("unroll") for (int k = 0; k < 2; ++k) \
;         acc[ai][bj][m][n] = mma16<BF>(Bt[n][k], At[m][k], acc[ai][bj][m][n]); __builtin_amdgcn_s_setprio(0); } while (0)
; #define GM_WAIT_V(n) asm volatile("s_waitcnt vmcnt(" #n ")" ::: "memory")
; #define GM_WAIT_L(n) asm volatile("s_waitcnt lgkmcnt(" #n ")" ::: "memory")
; #define GM_BAR __builtin_amdgcn_s_barrier()
; #define GM_SCHED __builtin_amdgcn_sched_barrier(0)
; #define GM_STA_H1(buf, p, o1) do { if constexpr (GATHER) GM_STAGE(buf, p, o1); else GM_STAGE(buf, (p) + hstepB, voffA); } while (0)
; template <bool BF, bool GATHER = false, class Epi, class Hook>
; __device__ __forceinline__ void gemm_phase(LAS unsigned char* lds, const Gemm g, const Order& S, const Epi& E, Hook& HK) {
;     ...
;             GM_WAIT_V(8); GM_WAIT_L(0); GM_BAR; GM_MMA(1, 0, At, B0); GM_MMA(1, 1, At, B1); GM_BAR; GM_SCHED;
;             GM_LDB(B0, 1, 0); GM_LDB(B1, 1, 1); GM_SCHED; GM_LDA(At, 1, 0); GM_STA_H1(GM_SA(0, 1), a2, s1);
;             GM_WAIT_V(8); GM_WAIT_L(0); GM_BAR; GM_MMA(0, 0, At, B0); GM_MMA(0, 1, At, B1); GM_BAR; GM_SCHED;
	v_mfma_f32_16x16x32_f16 v[62:65], v[122:125], v[184:187], v[62:65]
	v_mfma_f32_16x16x32_f16 v[58:61], v[130:133], v[184:187], v[58:61]
	v_mfma_f32_16x16x32_f16 v[46:49], v[122:125], v[192:195], v[46:49]
	v_mfma_f32_16x16x32_f16 v[42:45], v[130:133], v[192:195], v[42:45]
	v_mfma_f32_16x16x32_f16 v[30:33], v[122:125], v[200:203], v[30:33]
	v_mfma_f32_16x16x32_f16 v[26:29], v[130:133], v[200:203], v[26:29]
	v_mfma_f32_16x16x32_f16 v[14:17], v[122:125], v[208:211], v[14:17]
	v_mfma_f32_16x16x32_f16 v[10:13], v[130:133], v[208:211], v[10:13]
	v_mfma_f32_16x16x32_f16 v[62:65], v[126:129], v[188:191], v[62:65]
	v_mfma_f32_16x16x32_f16 v[58:61], v[134:137], v[188:191], v[58:61]
	v_mfma_f32_16x16x32_f16 v[46:49], v[126:129], v[196:199], v[46:49]
	v_mfma_f32_16x16x32_f16 v[42:45], v[134:137], v[196:199], v[42:45]
	v_mfma_f32_16x16x32_f16 v[30:33], v[126:129], v[204:207], v[30:33]
	v_mfma_f32_16x16x32_f16 v[26:29], v[134:137], v[204:207], v[26:29]
	v_mfma_f32_16x16x32_f16 v[14:17], v[126:129], v[212:215], v[14:17]
	v_mfma_f32_16x16x32_f16 v[10:13], v[134:137], v[212:215], v[10:13]
	v_mfma_f32_16x16x32_f16 v[54:57], v[162:165], v[184:187], v[54:57]
	v_mfma_f32_16x16x32_f16 v[50:53], v[176:179], v[184:187], v[50:53]
	v_mfma_f32_16x16x32_f16 v[38:41], v[162:165], v[192:195], v[38:41]
	v_mfma_f32_16x16x32_f16 v[34:37], v[176:179], v[192:195], v[34:37]
	v_mfma_f32_16x16x32_f16 v[22:25], v[162:165], v[200:203], v[22:25]
	v_mfma_f32_16x16x32_f16 v[18:21], v[176:179], v[200:203], v[18:21]
	v_mfma_f32_16x16x32_f16 v[6:9], v[162:165], v[208:211], v[6:9]
	v_mfma_f32_16x16x32_f16 v[2:5], v[176:179], v[208:211], v[2:5]
	v_mfma_f32_16x16x32_f16 v[54:57], v[172:175], v[188:191], v[54:57]
	v_mfma_f32_16x16x32_f16 v[50:53], v[180:183], v[188:191], v[50:53]
	v_mfma_f32_16x16x32_f16 v[38:41], v[172:175], v[196:199], v[38:41]
	v_mfma_f32_16x16x32_f16 v[34:37], v[180:183], v[196:199], v[34:37]
	v_mfma_f32_16x16x32_f16 v[22:25], v[172:175], v[204:207], v[22:25]
	v_mfma_f32_16x16x32_f16 v[18:21], v[180:183], v[204:207], v[18:21]
	v_mfma_f32_16x16x32_f16 v[6:9], v[172:175], v[212:215], v[6:9]
	v_mfma_f32_16x16x32_f16 v[2:5], v[180:183], v[212:215], v[2:5]
	s_barrier
	s_add_u32 s26, s26, 0x40000
	s_addc_u32 s27, s27, 0
	s_mov_b32 m0, s35
	v_lshl_add_u64 v[224:225], s[26:27], 0, v[146:147]
	global_load_lds_dwordx4 v[224:225], off
	v_lshl_add_u64 v[224:225], s[26:27], 0, v[150:151]
	s_mov_b32 m0, s36
	s_nop 0
	global_load_lds_dwordx4 v[224:225], off
	s_mov_b32 s51, 0x1c000
	s_mov_b32 s50, 0x18000
	v_add_u32_e32 v244, s50, v166
	v_add_u32_e32 v245, s51, v166
	ds_read_b128 v[122:125], v244
	ds_read_b128 v[126:129], v244 offset:1024
	ds_read_b128 v[130:133], v244 offset:2048
	ds_read_b128 v[134:137], v244 offset:3072
	ds_read_b128 v[162:165], v245
	ds_read_b128 v[172:175], v245 offset:1024
	ds_read_b128 v[176:179], v245 offset:2048
	ds_read_b128 v[180:183], v245 offset:3072
	ds_read_b128 v[184:187], v170 offset:32768
	ds_read_b128 v[188:191], v170 offset:33792
	ds_read_b128 v[192:195], v170 offset:34816
	ds_read_b128 v[196:199], v170 offset:35840
	ds_read_b128 v[200:203], v170 offset:36864
	ds_read_b128 v[204:207], v170 offset:37888
	ds_read_b128 v[208:211], v170 offset:38912
	ds_read_b128 v[212:215], v170 offset:39936
	s_waitcnt vmcnt(8)
	s_waitcnt lgkmcnt(0)
	s_barrier
	v_mfma_f32_16x16x32_f16 v[142:145], v[122:125], v[184:187], v[142:145]
	v_mfma_f32_16x16x32_f16 v[138:141], v[130:133], v[184:187], v[138:141]
	v_mfma_f32_16x16x32_f16 v[110:113], v[122:125], v[192:195], v[110:113]
	v_mfma_f32_16x16x32_f16 v[106:109], v[130:133], v[192:195], v[106:109]
	v_mfma_f32_16x16x32_f16 v[94:97], v[122:125], v[200:203], v[94:97]
	v_mfma_f32_16x16x32_f16 v[90:93], v[130:133], v[200:203], v[90:93]
	v_mfma_f32_16x16x32_f16 v[78:81], v[122:125], v[208:211], v[78:81]
	v_mfma_f32_16x16x32_f16 v[74:77], v[130:133], v[208:211], v[74:77]
	v_mfma_f32_16x16x32_f16 v[142:145], v[126:129], v[188:191], v[142:145]
	v_mfma_f32_16x16x32_f16 v[138:141], v[134:137], v[188:191], v[138:141]
	v_mfma_f32_16x16x32_f16 v[110:113], v[126:129], v[196:199], v[110:113]
	v_mfma_f32_16x16x32_f16 v[106:109], v[134:137], v[196:199], v[106:109]
	v_mfma_f32_16x16x32_f16 v[94:97], v[126:129], v[204:207], v[94:97]
	v_mfma_f32_16x16x32_f16 v[90:93], v[134:137], v[204:207], v[90:93]
	v_mfma_f32_16x16x32_f16 v[78:81], v[126:129], v[212:215], v[78:81]
	v_mfma_f32_16x16x32_f16 v[74:77], v[134:137], v[212:215], v[74:77]
	v_mfma_f32_16x16x32_f16 v[118:121], v[162:165], v[184:187], v[118:121]
	v_mfma_f32_16x16x32_f16 v[114:117], v[176:179], v[184:187], v[114:117]
	v_mfma_f32_16x16x32_f16 v[102:105], v[162:165], v[192:195], v[102:105]
	v_mfma_f32_16x16x32_f16 v[98:101], v[176:179], v[192:195], v[98:101]
	v_mfma_f32_16x16x32_f16 v[86:89], v[162:165], v[200:203], v[86:89]
	v_mfma_f32_16x16x32_f16 v[82:85], v[176:179], v[200:203], v[82:85]
	v_mfma_f32_16x16x32_f16 v[70:73], v[162:165], v[208:211], v[70:73]
	v_mfma_f32_16x16x32_f16 v[66:69], v[176:179], v[208:211], v[66:69]
	v_mfma_f32_16x16x32_f16 v[118:121], v[172:175], v[188:191], v[118:121]
	v_mfma_f32_16x16x32_f16 v[114:117], v[180:183], v[188:191], v[114:117]
	v_mfma_f32_16x16x32_f16 v[102:105], v[172:175], v[196:199], v[102:105]
	v_mfma_f32_16x16x32_f16 v[98:101], v[180:183], v[196:199], v[98:101]
	v_mfma_f32_16x16x32_f16 v[86:89], v[172:175], v[204:207], v[86:89]
	v_mfma_f32_16x16x32_f16 v[82:85], v[180:183], v[204:207], v[82:85]
	v_mfma_f32_16x16x32_f16 v[70:73], v[172:175], v[212:215], v[70:73]
	v_mfma_f32_16x16x32_f16 v[66:69], v[180:183], v[212:215], v[66:69]
	s_barrier
; #define GM_STAGE(bufoff, gbase, voff) do { _Pragma("unroll") for (int _i = 0; _i < 2; ++_i) \
;         __builtin_amdgcn_global_load_lds((const unsigned*)((const char*)(gbase) + (voff)[_i]), (LAS unsigned*)(lds + (bufoff) + ldsw + _i * 8192), 16, 0, 0); } while (0)
; #define GM_LDA(dst, b, h) do { _Pragma("unroll") for (int m = 0; m < 4; ++m) _Pragma("unroll") for (int k = 0; k < 2; ++k) dst[m][k] = *(const LAS s16x8*)(lds + GM_SA(b, h) + aoff + m * 2048 + k * 1024); } while (0)
; #define GM_MMA(ai, bj, At, Bt) do { __builtin_amdgcn_s_setprio(1); _Pragma("unroll") for (int m = 0; m < 4; ++m) _Pragma("unroll") for (int n = 0; n < 2; ++n) _Pragma("unroll") for (int k = 0; k < 2; ++k) \
;         acc[ai][bj][m][n] = mma16<BF>(Bt[n][k], At[m][k], acc[ai][bj][m][n]); __builtin_amdgcn_s_setprio(0); } while (0)
; #define GM_WAIT_V(n) asm volatile("s_waitcnt vmcnt(" #n ")" ::: "memory")
; #define GM_WAIT_L(n) asm volatile("s_waitcnt lgkmcnt(" #n ")" ::: "memory")
; #define GM_BAR __builtin_amdgcn_s_barrier()
; #define GM_SCHED __builtin_amdgcn_sched_barrier(0)
; #define GM_STA_H0(buf, p, o0) do { if constexpr (GATHER) GM_STAGE(buf, p, o0); else GM_STAGE(buf, p, voffA); } while (0)
; template <bool BF, bool GATHER = false, class Epi, class Hook>
; __device__ __forceinline__ void gemm_phase(LAS unsigned char* lds, const Gemm g, const Order& S, const Epi& E, Hook& HK) {
;     ...
;             GM_LDA(At, 1, 1); GM_STAGE(GM_SB(1, 0), b3, voffB); GM_STAGE(GM_SB(1, 1), b3 + hstepB, voffB); GM_STA_H0(GM_SA(1, 0), a3, s0);
;             GM_WAIT_V(8); GM_WAIT_L(0); GM_BAR; GM_MMA(1, 0, At, B0); GM_MMA(1, 1, At, B1); GM_BAR; GM_SCHED;
;         }
;         if (wr == 0) GM_BAR;
	s_add_i32 s26, s50, s31
	v_lshl_add_u64 v[216:217], v[216:217], 0, s[10:11]
	s_mov_b32 m0, s26
	global_load_lds_dwordx4 v[216:217], off
	s_add_i32 m0, s26, 0x2000
	s_add_u32 s24, s24, 0x40080
	v_lshl_add_u64 v[216:217], v[218:219], 0, s[10:11]
	s_addc_u32 s25, s25, 0
	s_add_i32 s26, s51, s31
	global_load_lds_dwordx4 v[216:217], off
	v_lshl_add_u64 v[216:217], s[24:25], 0, v[148:149]
	s_mov_b32 m0, s26
	s_nop 0
	global_load_lds_dwordx4 v[216:217], off
	v_lshl_add_u64 v[216:217], s[24:25], 0, v[152:153]
	s_add_i32 m0, s26, 0x2000
	s_nop 0
	global_load_lds_dwordx4 v[216:217], off
	v_lshl_add_u64 v[216:217], v[220:221], 0, s[10:11]
	s_mov_b32 m0, s40
	s_nop 0
	global_load_lds_dwordx4 v[216:217], off
	v_lshl_add_u64 v[216:217], v[222:223], 0, s[10:11]
	s_mov_b32 m0, s41
	s_nop 0
	global_load_lds_dwordx4 v[216:217], off
	ds_read_b128 v[184:187], v170 offset:49152
	ds_read_b128 v[188:191], v170 offset:50176
	ds_read_b128 v[192:195], v170 offset:51200
	ds_read_b128 v[196:199], v170 offset:52224
	ds_read_b128 v[200:203], v170 offset:53248
	ds_read_b128 v[204:207], v170 offset:54272
	ds_read_b128 v[208:211], v170 offset:55296
	ds_read_b128 v[212:215], v170 offset:56320
	s_waitcnt vmcnt(8)
	s_waitcnt lgkmcnt(0)
	s_barrier
	v_mfma_f32_16x16x32_f16 v[62:65], v[122:125], v[184:187], v[62:65]
	v_mfma_f32_16x16x32_f16 v[58:61], v[130:133], v[184:187], v[58:61]
	v_mfma_f32_16x16x32_f16 v[46:49], v[122:125], v[192:195], v[46:49]
	v_mfma_f32_16x16x32_f16 v[42:45], v[130:133], v[192:195], v[42:45]
	v_mfma_f32_16x16x32_f16 v[30:33], v[122:125], v[200:203], v[30:33]
	v_mfma_f32_16x16x32_f16 v[26:29], v[130:133], v[200:203], v[26:29]
	v_mfma_f32_16x16x32_f16 v[14:17], v[122:125], v[208:211], v[14:17]
	v_mfma_f32_16x16x32_f16 v[10:13], v[130:133], v[208:211], v[10:13]
	v_mfma_f32_16x16x32_f16 v[62:65], v[126:129], v[188:191], v[62:65]
	v_mfma_f32_16x16x32_f16 v[58:61], v[134:137], v[188:191], v[58:61]
	v_mfma_f32_16x16x32_f16 v[46:49], v[126:129], v[196:199], v[46:49]
	v_mfma_f32_16x16x32_f16 v[42:45], v[134:137], v[196:199], v[42:45]
	v_mfma_f32_16x16x32_f16 v[30:33], v[126:129], v[204:207], v[30:33]
	v_mfma_f32_16x16x32_f16 v[26:29], v[134:137], v[204:207], v[26:29]
	v_mfma_f32_16x16x32_f16 v[14:17], v[126:129], v[212:215], v[14:17]
	v_mfma_f32_16x16x32_f16 v[10:13], v[134:137], v[212:215], v[10:13]
	v_mfma_f32_16x16x32_f16 v[54:57], v[162:165], v[184:187], v[54:57]
	v_mfma_f32_16x16x32_f16 v[50:53], v[176:179], v[184:187], v[50:53]
	v_mfma_f32_16x16x32_f16 v[38:41], v[162:165], v[192:195], v[38:41]
	v_mfma_f32_16x16x32_f16 v[34:37], v[176:179], v[192:195], v[34:37]
	v_mfma_f32_16x16x32_f16 v[22:25], v[162:165], v[200:203], v[22:25]
	v_mfma_f32_16x16x32_f16 v[18:21], v[176:179], v[200:203], v[18:21]
	v_mfma_f32_16x16x32_f16 v[6:9], v[162:165], v[208:211], v[6:9]
	v_mfma_f32_16x16x32_f16 v[2:5], v[176:179], v[208:211], v[2:5]
	v_mfma_f32_16x16x32_f16 v[54:57], v[172:175], v[188:191], v[54:57]
	v_mfma_f32_16x16x32_f16 v[50:53], v[180:183], v[188:191], v[50:53]
	v_mfma_f32_16x16x32_f16 v[38:41], v[172:175], v[196:199], v[38:41]
	v_mfma_f32_16x16x32_f16 v[34:37], v[180:183], v[196:199], v[34:37]
	v_mfma_f32_16x16x32_f16 v[22:25], v[172:175], v[204:207], v[22:25]
	v_mfma_f32_16x16x32_f16 v[18:21], v[180:183], v[204:207], v[18:21]
	v_mfma_f32_16x16x32_f16 v[6:9], v[172:175], v[212:215], v[6:9]
	v_mfma_f32_16x16x32_f16 v[2:5], v[180:183], v[212:215], v[2:5]
	s_barrier
	s_add_i32 s49, s49, 2
	s_add_u32 s22, s22, 0x100
	s_addc_u32 s23, s23, 0
	s_add_u32 s47, s47, 0x100
	s_addc_u32 s48, s48, 0
	s_cmp_gt_u32 s49, 13
	s_cbranch_scc0 .LBB0_1480
	s_and_b64 vcc, exec, s[12:13]
	s_cbranch_vccz .LBB0_1483
	s_barrier

; #define GM_STAGE(bufoff, gbase, voff) do { _Pragma("unroll") for (int _i = 0; _i < 2; ++_i) \
;         __builtin_amdgcn_global_load_lds((const unsigned*)((const char*)(gbase) + (voff)[_i]), (LAS unsigned*)(lds + (bufoff) + ldsw + _i * 8192), 16, 0, 0); } while (0)
; #define GM_LDA(dst, b, h) do { _Pragma("unroll") for (int m = 0; m < 4; ++m) _Pragma("unroll") for (int k = 0; k < 2; ++k) dst[m][k] = *(const LAS s16x8*)(lds + GM_SA(b, h) + aoff + m * 2048 + k * 1024); } while (0)
; #define GM_LDB(dst, b, h) do { _Pragma("unroll") for (int n = 0; n < 2; ++n) _Pragma("unroll") for (int k = 0; k < 2; ++k) dst[n][k] = *(const LAS s16x8*)(lds + GM_SB(b, h) + boff + n * 2048 + k * 1024); } while (0)
; #define GM_MMA(ai, bj, At, Bt) do { __builtin_amdgcn_s_setprio(1); _Pragma("unroll") for (int m = 0; m < 4; ++m) _Pragma("unroll") for (int n = 0; n < 2; ++n) _Pragma("unroll") for (int k = 0; k < 2; ++k) \
;         acc[ai][bj][m][n] = mma16<BF>(Bt[n][k], At[m][k], acc[ai][bj][m][n]); __builtin_amdgcn_s_setprio(0); } while (0)
; #define GM_WAIT_V(n) asm volatile("s_waitcnt vmcnt(" #n ")" ::: "memory")
; #define GM_WAIT_L(n) asm volatile("s_waitcnt lgkmcnt(" #n ")" ::: "memory")
; template <bool BF, bool GATHER = false, class Epi, class Hook>
; __device__ __forceinline__ void gemm_phase(LAS unsigned char* lds, const Gemm g, const Order& S, const Epi& E, Hook& HK) {
;     ...
;             const bool last = (t == nt - 2);
;             const char* a1 = cA + (size_t)(t + 1) * kstep;
;             const char* a2 = last ? nA : cA + (size_t)(t + 2) * kstep; const char* b2 = last ? nB : cB + (size_t)(t + 2) * kstep;
;             const char* a3 = a2 + kstep; const char* b3 = b2 + kstep;
;             unsigned s0[2], s1[2];
;             if constexpr (GATHER) { s0[0] = last ? nA0[0] : gA0[0]; s0[1] = last ? nA0[1] : gA0[1]; s1[0] = last ? nA1[0] : gA1[0]; s1[1] = last ? nA1[1] : gA1[1]; }
;             GM_LDB(B0, 0, 0); GM_LDB(B1, 0, 1); GM_SCHED; GM_LDA(At, 0, 0); GM_STA_H1(GM_SA(1, 1), a1, gA1);
;             GM_WAIT_V(8); GM_WAIT_L(0); GM_BAR; GM_MMA(0, 0, At, B0); GM_MMA(0, 1, At, B1); GM_BAR; GM_SCHED;
;             GM_LDA(At, 0, 1); GM_STAGE(GM_SB(0, 0), b2, voffB); GM_STAGE(GM_SB(0, 1), b2 + hstepB, voffB); GM_STA_H0(GM_SA(0, 0), a2, s0);
;             GM_WAIT_V(8); GM_WAIT_L(0); GM_BAR; GM_MMA(1, 0, At, B0); GM_MMA(1, 1, At, B1); GM_BAR; GM_SCHED;
.LBB0_1867:
	s_add_u32 s22, s2, 0x100
	s_addc_u32 s23, s3, 0
	s_cmp_eq_u32 s52, 40
	s_cselect_b32 s27, s7, s23
	s_cselect_b32 s26, s6, s22
	s_cselect_b32 s25, s21, s51
	s_cselect_b32 s24, s20, s50
	v_lshl_add_u64 v[216:217], s[2:3], 0, v[138:139]
	s_add_i32 m0, s29, 0xc000
	global_load_lds_dwordx4 v[216:217], off
	v_lshl_add_u64 v[216:217], s[2:3], 0, v[140:141]
	s_add_i32 m0, s29, 0xe000
	s_nop 0
	global_load_lds_dwordx4 v[216:217], off
	ds_read_b128 v[146:149], v153
	ds_read_b128 v[156:159], v153 offset:1024
	ds_read_b128 v[160:163], v153 offset:2048
	ds_read_b128 v[164:167], v153 offset:3072
	ds_read_b128 v[168:171], v154
	ds_read_b128 v[172:175], v154 offset:1024
	ds_read_b128 v[176:179], v154 offset:2048
	ds_read_b128 v[180:183], v154 offset:3072
	ds_read_b128 v[184:187], v155
	ds_read_b128 v[188:191], v155 offset:1024
	ds_read_b128 v[192:195], v155 offset:2048
	ds_read_b128 v[196:199], v155 offset:3072
	ds_read_b128 v[200:203], v155 offset:4096
	ds_read_b128 v[204:207], v155 offset:5120
	ds_read_b128 v[208:211], v155 offset:6144
	ds_read_b128 v[212:215], v155 offset:7168
	s_waitcnt vmcnt(8)
	s_waitcnt lgkmcnt(0)
	s_barrier
	v_mfma_f32_16x16x32_bf16 v[126:129], v[146:149], v[184:187], v[126:129]
	v_mfma_f32_16x16x32_bf16 v[122:125], v[160:163], v[184:187], v[122:125]
	v_mfma_f32_16x16x32_bf16 v[110:113], v[146:149], v[192:195], v[110:113]
	v_mfma_f32_16x16x32_bf16 v[106:109], v[160:163], v[192:195], v[106:109]
	v_mfma_f32_16x16x32_bf16 v[94:97], v[146:149], v[200:203], v[94:97]
	v_mfma_f32_16x16x32_bf16 v[90:93], v[160:163], v[200:203], v[90:93]
	v_mfma_f32_16x16x32_bf16 v[78:81], v[146:149], v[208:211], v[78:81]
	v_mfma_f32_16x16x32_bf16 v[74:77], v[160:163], v[208:211], v[74:77]
	v_mfma_f32_16x16x32_bf16 v[126:129], v[156:159], v[188:191], v[126:129]
	v_mfma_f32_16x16x32_bf16 v[122:125], v[164:167], v[188:191], v[122:125]
	v_mfma_f32_16x16x32_bf16 v[110:113], v[156:159], v[196:199], v[110:113]
	v_mfma_f32_16x16x32_bf16 v[106:109], v[164:167], v[196:199], v[106:109]
	v_mfma_f32_16x16x32_bf16 v[94:97], v[156:159], v[204:207], v[94:97]
	v_mfma_f32_16x16x32_bf16 v[90:93], v[164:167], v[204:207], v[90:93]
	v_mfma_f32_16x16x32_bf16 v[78:81], v[156:159], v[212:215], v[78:81]
	v_mfma_f32_16x16x32_bf16 v[74:77], v[164:167], v[212:215], v[74:77]
	v_mfma_f32_16x16x32_bf16 v[118:121], v[168:171], v[184:187], v[118:121]
	v_mfma_f32_16x16x32_bf16 v[114:117], v[176:179], v[184:187], v[114:117]
	v_mfma_f32_16x16x32_bf16 v[102:105], v[168:171], v[192:195], v[102:105]
	v_mfma_f32_16x16x32_bf16 v[98:101], v[176:179], v[192:195], v[98:101]
	v_mfma_f32_16x16x32_bf16 v[86:89], v[168:171], v[200:203], v[86:89]
	v_mfma_f32_16x16x32_bf16 v[82:85], v[176:179], v[200:203], v[82:85]
	v_mfma_f32_16x16x32_bf16 v[70:73], v[168:171], v[208:211], v[70:73]
	v_mfma_f32_16x16x32_bf16 v[66:69], v[176:179], v[208:211], v[66:69]
	v_mfma_f32_16x16x32_bf16 v[118:121], v[172:175], v[188:191], v[118:121]
	v_mfma_f32_16x16x32_bf16 v[114:117], v[180:183], v[188:191], v[114:117]
	v_mfma_f32_16x16x32_bf16 v[102:105], v[172:175], v[196:199], v[102:105]
	v_mfma_f32_16x16x32_bf16 v[98:101], v[180:183], v[196:199], v[98:101]
	v_mfma_f32_16x16x32_bf16 v[86:89], v[172:175], v[204:207], v[86:89]
	v_mfma_f32_16x16x32_bf16 v[82:85], v[180:183], v[204:207], v[82:85]
	v_mfma_f32_16x16x32_bf16 v[70:73], v[172:175], v[212:215], v[70:73]
	v_mfma_f32_16x16x32_bf16 v[66:69], v[180:183], v[212:215], v[66:69]
	s_barrier
	s_add_i32 s2, s43, s28
	v_lshl_add_u64 v[216:217], s[24:25], 0, v[132:133]
	s_mov_b32 m0, s2
	global_load_lds_dwordx4 v[216:217], off
	s_add_i32 m0, s2, 0x2000
	s_add_u32 s2, s24, 0xb0000
	v_lshl_add_u64 v[218:219], s[24:25], 0, v[136:137]
	s_addc_u32 s3, s25, 0
	s_add_i32 s53, s44, s28
	global_load_lds_dwordx4 v[218:219], off
	v_lshl_add_u64 v[220:221], s[2:3], 0, v[132:133]
	s_mov_b32 m0, s53
	v_lshl_add_u64 v[222:223], s[26:27], 0, v[134:135]
	global_load_lds_dwordx4 v[220:221], off
	v_lshl_add_u64 v[220:221], s[2:3], 0, v[136:137]
	s_add_i32 m0, s53, 0x2000
	s_nop 0
	global_load_lds_dwordx4 v[220:221], off
	v_lshl_add_u64 v[220:221], s[26:27], 0, v[130:131]
	s_mov_b32 m0, s29
	s_nop 0
	global_load_lds_dwordx4 v[220:221], off
	s_mov_b32 m0, s30
	s_nop 0
	global_load_lds_dwordx4 v[222:223], off
	ds_read_b128 v[184:187], v155 offset:16384
	ds_read_b128 v[188:191], v155 offset:17408
	ds_read_b128 v[192:195], v155 offset:18432
	ds_read_b128 v[196:199], v155 offset:19456
	ds_read_b128 v[200:203], v155 offset:20480
	ds_read_b128 v[204:207], v155 offset:21504
	ds_read_b128 v[208:211], v155 offset:22528
	ds_read_b128 v[212:215], v155 offset:23552
	s_waitcnt vmcnt(8)
	s_waitcnt lgkmcnt(0)
	s_barrier
; #define GM_LDA(dst, b, h) do { _Pragma("unroll") for (int m = 0; m < 4; ++m) _Pragma("unroll") for (int k = 0; k < 2; ++k) dst[m][k] = *(const LAS s16x8*)(lds + GM_SA(b, h) + aoff + m * 2048 + k * 1024); } while (0)
; #define GM_LDB(dst, b, h) do { _Pragma("unroll") for (int n = 0; n < 2; ++n) _Pragma("unroll") for (int k = 0; k < 2; ++k) dst[n][k] = *(const LAS s16x8*)(lds + GM_SB(b, h) + boff + n * 2048 + k * 1024); } while (0)
; #define GM_MMA(ai, bj, At, Bt) do { __builtin_amdgcn_s_setprio(1); _Pragma("unroll") for (int m = 0; m < 4; ++m) _Pragma("unroll") for (int n = 0; n < 2; ++n) _Pragma("unroll") for (int k = 0; k < 2; ++k) \
;         acc[ai][bj][m][n] = mma16<BF>(Bt[n][k], At[m][k], acc[ai][bj][m][n]); __builtin_amdgcn_s_setprio(0); } while (0)
; #define GM_WAIT_V(n) asm volatile("s_waitcnt vmcnt(" #n ")" ::: "memory")
; #define GM_WAIT_L(n) asm volatile("s_waitcnt lgkmcnt(" #n ")" ::: "memory")
; #define GM_BAR __builtin_amdgcn_s_barrier()
; #define GM_SCHED __builtin_amdgcn_sched_barrier(0)
; #define GM_STA_H1(buf, p, o1) do { if constexpr (GATHER) GM_STAGE(buf, p, o1); else GM_STAGE(buf, (p) + hstepB, voffA); } while (0)
; template <bool BF, bool GATHER = false, class Epi, class Hook>
; __device__ __forceinline__ void gemm_phase(LAS unsigned char* lds, const Gemm g, const Order& S, const Epi& E, Hook& HK) {
;     ...
;             GM_WAIT_V(8); GM_WAIT_L(0); GM_BAR; GM_MMA(1, 0, At, B0); GM_MMA(1, 1, At, B1); GM_BAR; GM_SCHED;
;             GM_LDB(B0, 1, 0); GM_LDB(B1, 1, 1); GM_SCHED; GM_LDA(At, 1, 0); GM_STA_H1(GM_SA(0, 1), a2, s1);
;             GM_WAIT_V(8); GM_WAIT_L(0); GM_BAR; GM_MMA(0, 0, At, B0); GM_MMA(0, 1, At, B1); GM_BAR; GM_SCHED;
	v_mfma_f32_16x16x32_bf16 v[62:65], v[146:149], v[184:187], v[62:65]
	v_mfma_f32_16x16x32_bf16 v[58:61], v[160:163], v[184:187], v[58:61]
	v_mfma_f32_16x16x32_bf16 v[46:49], v[146:149], v[192:195], v[46:49]
	v_mfma_f32_16x16x32_bf16 v[42:45], v[160:163], v[192:195], v[42:45]
	v_mfma_f32_16x16x32_bf16 v[30:33], v[146:149], v[200:203], v[30:33]
	v_mfma_f32_16x16x32_bf16 v[26:29], v[160:163], v[200:203], v[26:29]
	v_mfma_f32_16x16x32_bf16 v[14:17], v[146:149], v[208:211], v[14:17]
	v_mfma_f32_16x16x32_bf16 v[10:13], v[160:163], v[208:211], v[10:13]
	v_mfma_f32_16x16x32_bf16 v[62:65], v[156:159], v[188:191], v[62:65]
	v_mfma_f32_16x16x32_bf16 v[58:61], v[164:167], v[188:191], v[58:61]
	v_mfma_f32_16x16x32_bf16 v[46:49], v[156:159], v[196:199], v[46:49]
	v_mfma_f32_16x16x32_bf16 v[42:45], v[164:167], v[196:199], v[42:45]
	v_mfma_f32_16x16x32_bf16 v[30:33], v[156:159], v[204:207], v[30:33]
	v_mfma_f32_16x16x32_bf16 v[26:29], v[164:167], v[204:207], v[26:29]
	v_mfma_f32_16x16x32_bf16 v[14:17], v[156:159], v[212:215], v[14:17]
	v_mfma_f32_16x16x32_bf16 v[10:13], v[164:167], v[212:215], v[10:13]
	v_mfma_f32_16x16x32_bf16 v[54:57], v[168:171], v[184:187], v[54:57]
	v_mfma_f32_16x16x32_bf16 v[50:53], v[176:179], v[184:187], v[50:53]
	v_mfma_f32_16x16x32_bf16 v[38:41], v[168:171], v[192:195], v[38:41]
	v_mfma_f32_16x16x32_bf16 v[34:37], v[176:179], v[192:195], v[34:37]
	v_mfma_f32_16x16x32_bf16 v[22:25], v[168:171], v[200:203], v[22:25]
	v_mfma_f32_16x16x32_bf16 v[18:21], v[176:179], v[200:203], v[18:21]
	v_mfma_f32_16x16x32_bf16 v[6:9], v[168:171], v[208:211], v[6:9]
	v_mfma_f32_16x16x32_bf16 v[2:5], v[176:179], v[208:211], v[2:5]
	v_mfma_f32_16x16x32_bf16 v[54:57], v[172:175], v[188:191], v[54:57]
	v_mfma_f32_16x16x32_bf16 v[50:53], v[180:183], v[188:191], v[50:53]
	v_mfma_f32_16x16x32_bf16 v[38:41], v[172:175], v[196:199], v[38:41]
	v_mfma_f32_16x16x32_bf16 v[34:37], v[180:183], v[196:199], v[34:37]
	v_mfma_f32_16x16x32_bf16 v[22:25], v[172:175], v[204:207], v[22:25]
	v_mfma_f32_16x16x32_bf16 v[18:21], v[180:183], v[204:207], v[18:21]
	v_mfma_f32_16x16x32_bf16 v[6:9], v[172:175], v[212:215], v[6:9]
	v_mfma_f32_16x16x32_bf16 v[2:5], v[180:183], v[212:215], v[2:5]
	s_barrier
	s_add_u32 s2, s26, 0xb0000
	s_addc_u32 s3, s27, 0
	s_mov_b32 m0, s31
	v_lshl_add_u64 v[224:225], s[2:3], 0, v[130:131]
	global_load_lds_dwordx4 v[224:225], off
	v_lshl_add_u64 v[224:225], s[2:3], 0, v[134:135]
	s_mov_b32 m0, s33
	s_nop 0
	global_load_lds_dwordx4 v[224:225], off
	s_mov_b32 s54, 0x1c000
	s_mov_b32 s53, 0x18000
	v_add_u32_e32 v244, s53, v150
	v_add_u32_e32 v245, s54, v150
	ds_read_b128 v[146:149], v244
	ds_read_b128 v[156:159], v244 offset:1024
	ds_read_b128 v[160:163], v244 offset:2048
	ds_read_b128 v[164:167], v244 offset:3072
	ds_read_b128 v[168:171], v245
	ds_read_b128 v[172:175], v245 offset:1024
	ds_read_b128 v[176:179], v245 offset:2048
	ds_read_b128 v[180:183], v245 offset:3072
	ds_read_b128 v[184:187], v155 offset:32768
	ds_read_b128 v[188:191], v155 offset:33792
	ds_read_b128 v[192:195], v155 offset:34816
	ds_read_b128 v[196:199], v155 offset:35840
	ds_read_b128 v[200:203], v155 offset:36864
	ds_read_b128 v[204:207], v155 offset:37888
	ds_read_b128 v[208:211], v155 offset:38912
	ds_read_b128 v[212:215], v155 offset:39936
	s_waitcnt vmcnt(8)
	s_waitcnt lgkmcnt(0)
	s_barrier
	v_mfma_f32_16x16x32_bf16 v[126:129], v[146:149], v[184:187], v[126:129]
	v_mfma_f32_16x16x32_bf16 v[122:125], v[160:163], v[184:187], v[122:125]
	v_mfma_f32_16x16x32_bf16 v[110:113], v[146:149], v[192:195], v[110:113]
	v_mfma_f32_16x16x32_bf16 v[106:109], v[160:163], v[192:195], v[106:109]
	v_mfma_f32_16x16x32_bf16 v[94:97], v[146:149], v[200:203], v[94:97]
	v_mfma_f32_16x16x32_bf16 v[90:93], v[160:163], v[200:203], v[90:93]
	v_mfma_f32_16x16x32_bf16 v[78:81], v[146:149], v[208:211], v[78:81]
	v_mfma_f32_16x16x32_bf16 v[74:77], v[160:163], v[208:211], v[74:77]
	v_mfma_f32_16x16x32_bf16 v[126:129], v[156:159], v[188:191], v[126:129]
	v_mfma_f32_16x16x32_bf16 v[122:125], v[164:167], v[188:191], v[122:125]
	v_mfma_f32_16x16x32_bf16 v[110:113], v[156:159], v[196:199], v[110:113]
	v_mfma_f32_16x16x32_bf16 v[106:109], v[164:167], v[196:199], v[106:109]
	v_mfma_f32_16x16x32_bf16 v[94:97], v[156:159], v[204:207], v[94:97]
	v_mfma_f32_16x16x32_bf16 v[90:93], v[164:167], v[204:207], v[90:93]
	v_mfma_f32_16x16x32_bf16 v[78:81], v[156:159], v[212:215], v[78:81]
	v_mfma_f32_16x16x32_bf16 v[74:77], v[164:167], v[212:215], v[74:77]
	v_mfma_f32_16x16x32_bf16 v[118:121], v[168:171], v[184:187], v[118:121]
	v_mfma_f32_16x16x32_bf16 v[114:117], v[176:179], v[184:187], v[114:117]
	v_mfma_f32_16x16x32_bf16 v[102:105], v[168:171], v[192:195], v[102:105]
	v_mfma_f32_16x16x32_bf16 v[98:101], v[176:179], v[192:195], v[98:101]
	v_mfma_f32_16x16x32_bf16 v[86:89], v[168:171], v[200:203], v[86:89]
	v_mfma_f32_16x16x32_bf16 v[82:85], v[176:179], v[200:203], v[82:85]
	v_mfma_f32_16x16x32_bf16 v[70:73], v[168:171], v[208:211], v[70:73]
	v_mfma_f32_16x16x32_bf16 v[66:69], v[176:179], v[208:211], v[66:69]
	v_mfma_f32_16x16x32_bf16 v[118:121], v[172:175], v[188:191], v[118:121]
	v_mfma_f32_16x16x32_bf16 v[114:117], v[180:183], v[188:191], v[114:117]
	v_mfma_f32_16x16x32_bf16 v[102:105], v[172:175], v[196:199], v[102:105]
	v_mfma_f32_16x16x32_bf16 v[98:101], v[180:183], v[196:199], v[98:101]
	v_mfma_f32_16x16x32_bf16 v[86:89], v[172:175], v[204:207], v[86:89]
	v_mfma_f32_16x16x32_bf16 v[82:85], v[180:183], v[204:207], v[82:85]
	v_mfma_f32_16x16x32_bf16 v[70:73], v[172:175], v[212:215], v[70:73]
	v_mfma_f32_16x16x32_bf16 v[66:69], v[180:183], v[212:215], v[66:69]
	s_barrier
; #define GM_STAGE(bufoff, gbase, voff) do { _Pragma("unroll") for (int _i = 0; _i < 2; ++_i) \
;         __builtin_amdgcn_global_load_lds((const unsigned*)((const char*)(gbase) + (voff)[_i]), (LAS unsigned*)(lds + (bufoff) + ldsw + _i * 8192), 16, 0, 0); } while (0)
; #define GM_LDA(dst, b, h) do { _Pragma("unroll") for (int m = 0; m < 4; ++m) _Pragma("unroll") for (int k = 0; k < 2; ++k) dst[m][k] = *(const LAS s16x8*)(lds + GM_SA(b, h) + aoff + m * 2048 + k * 1024); } while (0)
; #define GM_MMA(ai, bj, At, Bt) do { __builtin_amdgcn_s_setprio(1); _Pragma("unroll") for (int m = 0; m < 4; ++m) _Pragma("unroll") for (int n = 0; n < 2; ++n) _Pragma("unroll") for (int k = 0; k < 2; ++k) \
;         acc[ai][bj][m][n] = mma16<BF>(Bt[n][k], At[m][k], acc[ai][bj][m][n]); __builtin_amdgcn_s_setprio(0); } while (0)
; #define GM_WAIT_V(n) asm volatile("s_waitcnt vmcnt(" #n ")" ::: "memory")
; #define GM_WAIT_L(n) asm volatile("s_waitcnt lgkmcnt(" #n ")" ::: "memory")
; #define GM_BAR __builtin_amdgcn_s_barrier()
; #define GM_SCHED __builtin_amdgcn_sched_barrier(0)
; #define GM_STA_H0(buf, p, o0) do { if constexpr (GATHER) GM_STAGE(buf, p, o0); else GM_STAGE(buf, p, voffA); } while (0)
; template <bool BF, bool GATHER = false, class Epi, class Hook>
; __device__ __forceinline__ void gemm_phase(LAS unsigned char* lds, const Gemm g, const Order& S, const Epi& E, Hook& HK) {
;     ...
;             GM_LDA(At, 1, 1); GM_STAGE(GM_SB(1, 0), b3, voffB); GM_STAGE(GM_SB(1, 1), b3 + hstepB, voffB); GM_STA_H0(GM_SA(1, 0), a3, s0);
;             GM_WAIT_V(8); GM_WAIT_L(0); GM_BAR; GM_MMA(1, 0, At, B0); GM_MMA(1, 1, At, B1); GM_BAR; GM_SCHED;
;         }
;         if (wr == 0) GM_BAR;
	s_add_i32 s2, s53, s28
	v_lshl_add_u64 v[216:217], v[216:217], 0, s[12:13]
	s_mov_b32 m0, s2
	global_load_lds_dwordx4 v[216:217], off
	s_add_i32 m0, s2, 0x2000
	s_add_u32 s2, s24, 0xb0080
	v_lshl_add_u64 v[216:217], v[218:219], 0, s[12:13]
	s_addc_u32 s3, s25, 0
	s_add_i32 s24, s54, s28
	global_load_lds_dwordx4 v[216:217], off
	v_lshl_add_u64 v[216:217], s[2:3], 0, v[132:133]
	s_mov_b32 m0, s24
	s_nop 0
	global_load_lds_dwordx4 v[216:217], off
	v_lshl_add_u64 v[216:217], s[2:3], 0, v[136:137]
	s_add_i32 m0, s24, 0x2000
	s_nop 0
	global_load_lds_dwordx4 v[216:217], off
	v_lshl_add_u64 v[216:217], v[220:221], 0, s[12:13]
	s_mov_b32 m0, s36
	s_nop 0
	global_load_lds_dwordx4 v[216:217], off
	v_lshl_add_u64 v[216:217], v[222:223], 0, s[12:13]
	s_mov_b32 m0, s37
	s_nop 0
	global_load_lds_dwordx4 v[216:217], off
	ds_read_b128 v[184:187], v155 offset:49152
	ds_read_b128 v[188:191], v155 offset:50176
	ds_read_b128 v[192:195], v155 offset:51200
	ds_read_b128 v[196:199], v155 offset:52224
	ds_read_b128 v[200:203], v155 offset:53248
	ds_read_b128 v[204:207], v155 offset:54272
	ds_read_b128 v[208:211], v155 offset:55296
	ds_read_b128 v[212:215], v155 offset:56320
	s_waitcnt vmcnt(8)
	s_waitcnt lgkmcnt(0)
	s_barrier
	v_mfma_f32_16x16x32_bf16 v[62:65], v[146:149], v[184:187], v[62:65]
	v_mfma_f32_16x16x32_bf16 v[58:61], v[160:163], v[184:187], v[58:61]
	v_mfma_f32_16x16x32_bf16 v[46:49], v[146:149], v[192:195], v[46:49]
	v_mfma_f32_16x16x32_bf16 v[42:45], v[160:163], v[192:195], v[42:45]
	v_mfma_f32_16x16x32_bf16 v[30:33], v[146:149], v[200:203], v[30:33]
	v_mfma_f32_16x16x32_bf16 v[26:29], v[160:163], v[200:203], v[26:29]
	v_mfma_f32_16x16x32_bf16 v[14:17], v[146:149], v[208:211], v[14:17]
	v_mfma_f32_16x16x32_bf16 v[10:13], v[160:163], v[208:211], v[10:13]
	v_mfma_f32_16x16x32_bf16 v[62:65], v[156:159], v[188:191], v[62:65]
	v_mfma_f32_16x16x32_bf16 v[58:61], v[164:167], v[188:191], v[58:61]
	v_mfma_f32_16x16x32_bf16 v[46:49], v[156:159], v[196:199], v[46:49]
	v_mfma_f32_16x16x32_bf16 v[42:45], v[164:167], v[196:199], v[42:45]
	v_mfma_f32_16x16x32_bf16 v[30:33], v[156:159], v[204:207], v[30:33]
	v_mfma_f32_16x16x32_bf16 v[26:29], v[164:167], v[204:207], v[26:29]
	v_mfma_f32_16x16x32_bf16 v[14:17], v[156:159], v[212:215], v[14:17]
	v_mfma_f32_16x16x32_bf16 v[10:13], v[164:167], v[212:215], v[10:13]
	v_mfma_f32_16x16x32_bf16 v[54:57], v[168:171], v[184:187], v[54:57]
	v_mfma_f32_16x16x32_bf16 v[50:53], v[176:179], v[184:187], v[50:53]
	v_mfma_f32_16x16x32_bf16 v[38:41], v[168:171], v[192:195], v[38:41]
	v_mfma_f32_16x16x32_bf16 v[34:37], v[176:179], v[192:195], v[34:37]
	v_mfma_f32_16x16x32_bf16 v[22:25], v[168:171], v[200:203], v[22:25]
	v_mfma_f32_16x16x32_bf16 v[18:21], v[176:179], v[200:203], v[18:21]
	v_mfma_f32_16x16x32_bf16 v[6:9], v[168:171], v[208:211], v[6:9]
	v_mfma_f32_16x16x32_bf16 v[2:5], v[176:179], v[208:211], v[2:5]
	v_mfma_f32_16x16x32_bf16 v[54:57], v[172:175], v[188:191], v[54:57]
	v_mfma_f32_16x16x32_bf16 v[50:53], v[180:183], v[188:191], v[50:53]
	v_mfma_f32_16x16x32_bf16 v[38:41], v[172:175], v[196:199], v[38:41]
	v_mfma_f32_16x16x32_bf16 v[34:37], v[180:183], v[196:199], v[34:37]
	v_mfma_f32_16x16x32_bf16 v[22:25], v[172:175], v[204:207], v[22:25]
	v_mfma_f32_16x16x32_bf16 v[18:21], v[180:183], v[204:207], v[18:21]
	v_mfma_f32_16x16x32_bf16 v[6:9], v[172:175], v[212:215], v[6:9]
	v_mfma_f32_16x16x32_bf16 v[2:5], v[180:183], v[212:215], v[2:5]
	s_barrier
	s_add_i32 s52, s52, 2
	s_add_u32 s50, s50, 0x100
	s_addc_u32 s51, s51, 0
	s_cmp_gt_u32 s52, 41
	s_mov_b64 s[2:3], s[22:23]
	s_cbranch_scc0 .LBB0_1867
	s_and_b64 vcc, exec, s[14:15]
	s_cbranch_vccz .LBB0_1870
	s_barrier
